# in-proj epilogue: counted vmcnt waits for rope/bcum table loads instead of vmcnt(0) drains
# speedup vs baseline: 1.0119x; 1.0119x over previous
;     __device__ __forceinline__ void operator()(const f32x4 (&acc)[2][2][4][2], const Unit& u, int wr, int wc, int fr, int fq) const {
;     ...
;             BC_LOAD(0, 0);
; #pragma unroll
;             for (int g = 0; g < 16; ++g) {
;                 const int ai = g >> 3, m = (g >> 1) & 3, bj = g & 1;
;                 const int r = row0 + ai * HALF + m * 16;
;                 if (g + 1 < 16) BC_LOAD((g + 1) & 1, g + 1);
;                 {
;                     {
;                         const int col = cb + bj * HALF + lc;
;                         const size_t hoff = ((size_t)((r >> 11) * 4 + (col >> 7)) * SEQ + (r & (SEQ - 1))) * 128 + (col & 127);
;                         const f32x4 b0 = bc[g & 1][0], b1 = bc[g & 1][1];
;                         const f32x4 v0 = acc[ai][bj][m][0], v1 = acc[ai][bj][m][1];
;                         const float L2E = 1.4426950408889634f;
;                         if (isq) {
;                             const float s = 0.08838834764831845f;
;                             u32x4 o; o[0] = cvt_pk_bf16(v0[0] * s * __builtin_amdgcn_exp2f(b0[0] * L2E), v0[1] * s * __builtin_amdgcn_exp2f(b0[1] * L2E));
;                             o[1] = cvt_pk_bf16(v0[2] * s * __builtin_amdgcn_exp2f(b0[2] * L2E), v0[3] * s * __builtin_amdgcn_exp2f(b0[3] * L2E));
;                             o[2] = cvt_pk_bf16(v1[0] * s * __builtin_amdgcn_exp2f(b1[0] * L2E), v1[1] * s * __builtin_amdgcn_exp2f(b1[1] * L2E));
;                             o[3] = cvt_pk_bf16(v1[2] * s * __builtin_amdgcn_exp2f(b1[2] * L2E), v1[3] * s * __builtin_amdgcn_exp2f(b1[3] * L2E));
;                             __builtin_nontemporal_store(o, (u32x4*)(d0 + hoff));
;                         } else {
;                             u32x4 o;
;                             o[0] = cvt_pk_bf16(v0[0] * __builtin_amdgcn_exp2f(-b0[0] * L2E), v0[1] * __builtin_amdgcn_exp2f(-b0[1] * L2E));
;                             o[1] = cvt_pk_bf16(v0[2] * __builtin_amdgcn_exp2f(-b0[2] * L2E), v0[3] * __builtin_amdgcn_exp2f(-b0[3] * L2E));
;                             o[2] = cvt_pk_bf16(v1[0] * __builtin_amdgcn_exp2f(-b1[0] * L2E), v1[1] * __builtin_amdgcn_exp2f(-b1[1] * L2E));
;                             o[3] = cvt_pk_bf16(v1[2] * __builtin_amdgcn_exp2f(-b1[2] * L2E), v1[3] * __builtin_amdgcn_exp2f(-b1[3] * L2E));
;                             __builtin_nontemporal_store(o, (u32x4*)(d0 + hoff));
.LBB0_356:
	s_and_b64 vcc, exec, s[2:3]
	s_cbranch_vccz .LBB0_571
	s_cmp_gt_u32 s78, 13
	s_cselect_b64 s[42:43], -1, 0
	s_cmp_lt_u32 s78, 14
	s_cselect_b64 s[2:3], -1, 0
	s_and_b64 s[8:9], s[2:3], exec
	s_cselect_b32 s10, -12, -14
	v_ashrrev_i32_e32 v193, 31, v192
	s_add_i32 s10, s10, s78
	v_lshlrev_b64 v[128:129], 11, v[192:193]
	v_lshl_or_b32 v168, s10, 8, v170
	v_lshl_add_u64 v[128:129], s[22:23], 0, v[128:129]
	v_lshl_add_u64 v[136:137], v[168:169], 2, v[128:129]
	global_load_dwordx4 v[132:135], v[136:137], off offset:16
	global_load_dwordx4 v[144:147], v[136:137], off
	global_load_dwordx4 v[128:131], v[136:137], off offset:528
	s_nop 0
	global_load_dwordx4 v[136:139], v[136:137], off offset:512
	s_mov_b64 s[8:9], -1
	s_and_b64 vcc, exec, s[42:43]
	s_cbranch_vccz .LBB0_359
	s_waitcnt vmcnt(2)
	v_mul_f32_e32 v140, 0xbfb8aa3b, v144
	v_mul_f32_e32 v141, 0xbfb8aa3b, v145
	v_exp_f32_e32 v140, v140
	v_exp_f32_e32 v141, v141
	s_mov_b64 s[8:9], 0
	v_mov_b32_e32 v149, v123
	v_pk_mul_f32 v[140:141], v[124:125], v[140:141]
	s_nop 0
	v_cvt_pk_bf16_f32 v140, v140, v141
	v_mul_f32_e32 v141, 0xbfb8aa3b, v146
	v_exp_f32_e32 v142, v141
	v_mul_f32_e32 v141, 0xbfb8aa3b, v147
	v_exp_f32_e32 v143, v141
	s_nop 0
	v_pk_mul_f32 v[142:143], v[126:127], v[142:143]
	s_nop 0
	v_cvt_pk_bf16_f32 v141, v142, v143
	v_mul_f32_e32 v142, 0xbfb8aa3b, v132
	v_mul_f32_e32 v143, 0xbfb8aa3b, v133
	v_exp_f32_e32 v142, v142
	v_exp_f32_e32 v143, v143
	s_nop 0
	v_pk_mul_f32 v[142:143], v[120:121], v[142:143]
	s_nop 0
	v_cvt_pk_bf16_f32 v142, v142, v143
	v_mul_f32_e32 v143, 0xbfb8aa3b, v134
	v_exp_f32_e32 v143, v143
	s_nop 0
	v_mul_f32_e32 v148, v122, v143
.LBB0_359:
	s_andn2_b64 vcc, exec, s[8:9]
	s_mov_b32 s8, 0xbfb8aa3b
	s_cbranch_vccnz .LBB0_361
	s_waitcnt vmcnt(2)
	v_mul_f32_e32 v140, 0x3fb8aa3b, v144
	v_mul_f32_e32 v141, 0x3fb8aa3b, v145
	v_exp_f32_e32 v140, v140
	v_exp_f32_e32 v141, v141
	v_pk_mul_f32 v[142:143], v[124:125], s[34:35] op_sel_hi:[1,0]
	v_mul_f32_e32 v132, 0x3fb8aa3b, v132
	v_mul_f32_e32 v133, 0x3fb8aa3b, v133
	v_pk_mul_f32 v[140:141], v[142:143], v[140:141]
	v_exp_f32_e32 v132, v132
	v_cvt_pk_bf16_f32 v140, v140, v141
	v_mul_f32_e32 v141, 0x3fb8aa3b, v146
	v_exp_f32_e32 v142, v141
	v_mul_f32_e32 v141, 0x3fb8aa3b, v147
	v_exp_f32_e32 v143, v141
	v_exp_f32_e32 v133, v133
	v_pk_mul_f32 v[144:145], v[126:127], s[34:35] op_sel_hi:[1,0]
	s_mov_b32 s8, 0x3fb8aa3b
	v_pk_mul_f32 v[142:143], v[144:145], v[142:143]
	s_nop 0
	v_cvt_pk_bf16_f32 v141, v142, v143
	v_pk_mul_f32 v[142:143], v[120:121], s[34:35] op_sel_hi:[1,0]
	s_nop 0
	v_pk_mul_f32 v[132:133], v[142:143], v[132:133]
	s_nop 0
	v_cvt_pk_bf16_f32 v142, v132, v133
	v_mul_f32_e32 v133, 0x3fb8aa3b, v134
	v_exp_f32_e32 v190, v133
	v_mul_f32_e32 v132, 0x3db504f3, v122
	v_mov_b32_e32 v133, v123
	v_pk_mul_f32 v[148:149], v[132:133], v[190:191]
.LBB0_361:
	s_and_b64 s[2:3], s[2:3], exec
	s_mov_b32 s2, 0x46188000
	s_cselect_b32 s2, s2, 0x47188000
	v_readlane_b32 s80, v252, 28
	v_readlane_b32 s81, v252, 29
	s_add_u32 s2, s80, s2
	s_addc_u32 s3, s81, 0
	s_ashr_i32 s9, s15, 9
	s_and_b32 s33, s9, -4
	s_lshl_b32 s17, s10, 1
	s_waitcnt vmcnt(2)
	v_mul_f32_e32 v132, s8, v135
	s_add_i32 s10, s33, s17
	v_exp_f32_e32 v132, v132
	s_ashr_i32 s11, s10, 31
	v_lshlrev_b32_e32 v133, 7, v192
	s_lshl_b64 s[8:9], s[10:11], 19
	v_and_b32_e32 v156, 0x3e780, v133
	s_add_u32 s10, s2, s8
	v_mul_f32_e32 v132, v149, v132
	s_addc_u32 s11, s3, s9
	v_lshlrev_b32_e32 v150, 1, v156
	v_mov_b32_e32 v151, v169
	v_cvt_pk_bf16_f32 v143, v148, v132
	v_lshl_add_u64 v[132:133], s[10:11], 0, v[150:151]
	v_lshlrev_b32_e32 v148, 1, v170
	v_mov_b32_e32 v149, v169
	v_lshl_add_u64 v[132:133], v[132:133], 0, v[148:149]
	global_store_dwordx4 v[132:133], v[140:143], off nt
	v_or_b32_e32 v132, 16, v192
	v_ashrrev_i32_e32 v133, 31, v132
	v_lshlrev_b64 v[132:133], 11, v[132:133]
	v_lshl_add_u64 v[132:133], s[22:23], 0, v[132:133]
	v_lshl_add_u64 v[152:153], v[168:169], 2, v[132:133]
	global_load_dwordx4 v[132:135], v[152:153], off offset:16
	global_load_dwordx4 v[140:143], v[152:153], off
	s_waitcnt vmcnt(3)
	v_cndmask_b32_e64 v144, 0, 1, s[42:43]
	v_cmp_ne_u32_e64 s[8:9], 1, v144
	s_andn2_b64 vcc, exec, s[42:43]
	s_mov_b64 s[42:43], -1
	v_readlane_b32 s82, v252, 30
	v_readlane_b32 s83, v252, 31
	s_cbranch_vccnz .LBB0_363
	v_mul_f32_e32 v144, 0xbfb8aa3b, v136
	v_mul_f32_e32 v145, 0xbfb8aa3b, v137
	v_exp_f32_e32 v144, v144
	v_exp_f32_e32 v145, v145
	s_mov_b64 s[42:43], 0
	v_mov_b32_e32 v155, v115
	v_pk_mul_f32 v[144:145], v[116:117], v[144:145]
	s_nop 0
	v_cvt_pk_bf16_f32 v144, v144, v145
	v_mul_f32_e32 v145, 0xbfb8aa3b, v138
	v_exp_f32_e32 v146, v145
	v_mul_f32_e32 v145, 0xbfb8aa3b, v139
	v_exp_f32_e32 v147, v145
	s_nop 0
	v_pk_mul_f32 v[146:147], v[118:119], v[146:147]
	s_nop 0
	v_cvt_pk_bf16_f32 v145, v146, v147
	v_mul_f32_e32 v146, 0xbfb8aa3b, v128
	v_mul_f32_e32 v147, 0xbfb8aa3b, v129
	v_exp_f32_e32 v146, v146
	v_exp_f32_e32 v147, v147
	s_nop 0
	v_pk_mul_f32 v[146:147], v[112:113], v[146:147]
	s_nop 0
	v_cvt_pk_bf16_f32 v146, v146, v147
	v_mul_f32_e32 v147, 0xbfb8aa3b, v130
	v_exp_f32_e32 v147, v147
	s_nop 0
	v_mul_f32_e32 v154, v114, v147

;     __device__ __forceinline__ void operator()(const f32x4 (&acc)[2][2][4][2], const Unit& u, int wr, int wc, int fr, int fq) const {
;     ...
;             BC_LOAD(0, 0);
; #pragma unroll
;             for (int g = 0; g < 16; ++g) {
;                 const int ai = g >> 3, m = (g >> 1) & 3, bj = g & 1;
;                 const int r = row0 + ai * HALF + m * 16;
;                 if (g + 1 < 16) BC_LOAD((g + 1) & 1, g + 1);
;                 {
;                     {
;                         const int col = cb + bj * HALF + lc;
;                         const size_t hoff = ((size_t)((r >> 11) * 4 + (col >> 7)) * SEQ + (r & (SEQ - 1))) * 128 + (col & 127);
;                         const f32x4 b0 = bc[g & 1][0], b1 = bc[g & 1][1];
;                         const f32x4 v0 = acc[ai][bj][m][0], v1 = acc[ai][bj][m][1];
;                         const float L2E = 1.4426950408889634f;
;                         if (isq) {
;                             const float s = 0.08838834764831845f;
;                             u32x4 o; o[0] = cvt_pk_bf16(v0[0] * s * __builtin_amdgcn_exp2f(b0[0] * L2E), v0[1] * s * __builtin_amdgcn_exp2f(b0[1] * L2E));
;                             o[1] = cvt_pk_bf16(v0[2] * s * __builtin_amdgcn_exp2f(b0[2] * L2E), v0[3] * s * __builtin_amdgcn_exp2f(b0[3] * L2E));
;                             o[2] = cvt_pk_bf16(v1[0] * s * __builtin_amdgcn_exp2f(b1[0] * L2E), v1[1] * s * __builtin_amdgcn_exp2f(b1[1] * L2E));
;                             o[3] = cvt_pk_bf16(v1[2] * s * __builtin_amdgcn_exp2f(b1[2] * L2E), v1[3] * s * __builtin_amdgcn_exp2f(b1[3] * L2E));
;                             __builtin_nontemporal_store(o, (u32x4*)(d0 + hoff));
;                         } else {
;                             u32x4 o;
;                             o[0] = cvt_pk_bf16(v0[0] * __builtin_amdgcn_exp2f(-b0[0] * L2E), v0[1] * __builtin_amdgcn_exp2f(-b0[1] * L2E));
;                             o[1] = cvt_pk_bf16(v0[2] * __builtin_amdgcn_exp2f(-b0[2] * L2E), v0[3] * __builtin_amdgcn_exp2f(-b0[3] * L2E));
;                             o[2] = cvt_pk_bf16(v1[0] * __builtin_amdgcn_exp2f(-b1[0] * L2E), v1[1] * __builtin_amdgcn_exp2f(-b1[1] * L2E));
;                             o[3] = cvt_pk_bf16(v1[2] * __builtin_amdgcn_exp2f(-b1[2] * L2E), v1[3] * __builtin_amdgcn_exp2f(-b1[3] * L2E));
;                             __builtin_nontemporal_store(o, (u32x4*)(d0 + hoff));
.LBB0_365:
	v_mul_f32_e32 v128, s18, v131
	s_or_b32 s18, s17, 1
	v_exp_f32_e32 v128, v128
	s_add_i32 s42, s33, s18
	s_ashr_i32 s43, s42, 31
	s_lshl_b64 s[42:43], s[42:43], 19
	s_add_u32 s42, s2, s42
	v_mul_f32_e32 v128, v155, v128
	s_addc_u32 s43, s3, s43
	v_mov_b32_e32 v151, v169
	v_cvt_pk_bf16_f32 v147, v154, v128
	v_lshl_add_u64 v[128:129], s[42:43], 0, v[150:151]
	v_mov_b32_e32 v149, v169
	v_lshl_add_u64 v[128:129], v[128:129], 0, v[148:149]
	global_store_dwordx4 v[128:129], v[144:147], off nt
	global_load_dwordx4 v[128:131], v[152:153], off offset:528
	s_nop 0
	global_load_dwordx4 v[136:139], v[152:153], off offset:512
	s_and_b64 vcc, exec, s[8:9]
	s_mov_b64 s[54:55], -1
	s_cbranch_vccnz .LBB0_367
	s_waitcnt vmcnt(3)
	v_mul_f32_e32 v144, 0xbfb8aa3b, v140
	v_mul_f32_e32 v145, 0xbfb8aa3b, v141
	v_exp_f32_e32 v144, v144
	v_exp_f32_e32 v145, v145
	s_mov_b64 s[54:55], 0
	v_mov_b32_e32 v153, v107
	v_pk_mul_f32 v[144:145], v[108:109], v[144:145]
	s_nop 0
	v_cvt_pk_bf16_f32 v144, v144, v145
	v_mul_f32_e32 v145, 0xbfb8aa3b, v142
	v_exp_f32_e32 v146, v145
	v_mul_f32_e32 v145, 0xbfb8aa3b, v143
	v_exp_f32_e32 v147, v145
	s_nop 0
	v_pk_mul_f32 v[146:147], v[110:111], v[146:147]
	s_nop 0
	v_cvt_pk_bf16_f32 v145, v146, v147
	v_mul_f32_e32 v146, 0xbfb8aa3b, v132
	v_mul_f32_e32 v147, 0xbfb8aa3b, v133
	v_exp_f32_e32 v146, v146
	v_exp_f32_e32 v147, v147
	s_nop 0
	v_pk_mul_f32 v[146:147], v[104:105], v[146:147]
	s_nop 0
	v_cvt_pk_bf16_f32 v146, v146, v147
	v_mul_f32_e32 v147, 0xbfb8aa3b, v134
	v_exp_f32_e32 v147, v147
	s_nop 0
	v_mul_f32_e32 v152, v106, v147
.LBB0_367:
	s_andn2_b64 vcc, exec, s[54:55]
	s_mov_b32 s33, 0xbfb8aa3b
	s_cbranch_vccnz .LBB0_369
	s_waitcnt vmcnt(3)
	v_mul_f32_e32 v140, 0x3fb8aa3b, v140
	v_mul_f32_e32 v141, 0x3fb8aa3b, v141
	v_exp_f32_e32 v140, v140
	v_exp_f32_e32 v141, v141
	v_pk_mul_f32 v[144:145], v[108:109], s[34:35] op_sel_hi:[1,0]
	v_mul_f32_e32 v132, 0x3fb8aa3b, v132
	v_mul_f32_e32 v133, 0x3fb8aa3b, v133
	v_pk_mul_f32 v[140:141], v[144:145], v[140:141]
	v_exp_f32_e32 v132, v132
	v_cvt_pk_bf16_f32 v144, v140, v141
	v_mul_f32_e32 v140, 0x3fb8aa3b, v142
	v_mul_f32_e32 v141, 0x3fb8aa3b, v143
	v_exp_f32_e32 v140, v140
	v_exp_f32_e32 v141, v141
	v_exp_f32_e32 v133, v133
	v_pk_mul_f32 v[142:143], v[110:111], s[34:35] op_sel_hi:[1,0]
	s_mov_b32 s33, 0x3fb8aa3b
	v_pk_mul_f32 v[140:141], v[142:143], v[140:141]
	s_nop 0
	v_cvt_pk_bf16_f32 v145, v140, v141
	v_pk_mul_f32 v[140:141], v[104:105], s[34:35] op_sel_hi:[1,0]
	s_nop 0
	v_pk_mul_f32 v[132:133], v[140:141], v[132:133]
	s_nop 0
	v_cvt_pk_bf16_f32 v146, v132, v133
	v_mul_f32_e32 v133, 0x3fb8aa3b, v134
	v_exp_f32_e32 v190, v133
	v_mul_f32_e32 v132, 0x3db504f3, v106
	v_mov_b32_e32 v133, v107
	v_pk_mul_f32 v[152:153], v[132:133], v[190:191]
.LBB0_369:
	s_waitcnt vmcnt(3)
	v_mul_f32_e32 v132, s33, v135
	v_exp_f32_e32 v132, v132
	v_or_b32_e32 v133, 0x800, v156
	v_mov_b32_e32 v151, v169
	v_lshlrev_b32_e32 v150, 1, v133
	v_mul_f32_e32 v132, v153, v132
	v_cvt_pk_bf16_f32 v147, v152, v132
	v_lshl_add_u64 v[132:133], s[10:11], 0, v[150:151]
	v_mov_b32_e32 v149, v169
	v_lshl_add_u64 v[132:133], v[132:133], 0, v[148:149]
	global_store_dwordx4 v[132:133], v[144:147], off nt
	v_or_b32_e32 v132, 32, v192
	v_ashrrev_i32_e32 v133, 31, v132
	v_lshlrev_b64 v[132:133], 11, v[132:133]
	v_lshl_add_u64 v[132:133], s[22:23], 0, v[132:133]
	v_lshl_add_u64 v[152:153], v[168:169], 2, v[132:133]
	global_load_dwordx4 v[132:135], v[152:153], off offset:16
	global_load_dwordx4 v[140:143], v[152:153], off
	s_waitcnt vmcnt(3)
	s_and_b64 vcc, exec, s[8:9]
	s_mov_b64 s[54:55], -1
	s_cbranch_vccnz .LBB0_371
	v_mul_f32_e32 v144, 0xbfb8aa3b, v136
	v_mul_f32_e32 v145, 0xbfb8aa3b, v137
	v_exp_f32_e32 v144, v144
	v_exp_f32_e32 v145, v145
	s_mov_b64 s[54:55], 0
	v_mov_b32_e32 v155, v99
	v_pk_mul_f32 v[144:145], v[100:101], v[144:145]
	s_nop 0
	v_cvt_pk_bf16_f32 v144, v144, v145
	v_mul_f32_e32 v145, 0xbfb8aa3b, v138
	v_exp_f32_e32 v146, v145
	v_mul_f32_e32 v145, 0xbfb8aa3b, v139
	v_exp_f32_e32 v147, v145
	s_nop 0
	v_pk_mul_f32 v[146:147], v[102:103], v[146:147]
	s_nop 0
	v_cvt_pk_bf16_f32 v145, v146, v147
	v_mul_f32_e32 v146, 0xbfb8aa3b, v128
	v_mul_f32_e32 v147, 0xbfb8aa3b, v129
	v_exp_f32_e32 v146, v146
	v_exp_f32_e32 v147, v147
	s_nop 0
	v_pk_mul_f32 v[146:147], v[96:97], v[146:147]
	s_nop 0
	v_cvt_pk_bf16_f32 v146, v146, v147
	v_mul_f32_e32 v147, 0xbfb8aa3b, v130
	v_exp_f32_e32 v147, v147
	s_nop 0
	v_mul_f32_e32 v154, v98, v147

;     __device__ __forceinline__ void operator()(const f32x4 (&acc)[2][2][4][2], const Unit& u, int wr, int wc, int fr, int fq) const {
;     ...
;             BC_LOAD(0, 0);
; #pragma unroll
;             for (int g = 0; g < 16; ++g) {
;                 const int ai = g >> 3, m = (g >> 1) & 3, bj = g & 1;
;                 const int r = row0 + ai * HALF + m * 16;
;                 if (g + 1 < 16) BC_LOAD((g + 1) & 1, g + 1);
;                 {
;                     {
;                         const int col = cb + bj * HALF + lc;
;                         const size_t hoff = ((size_t)((r >> 11) * 4 + (col >> 7)) * SEQ + (r & (SEQ - 1))) * 128 + (col & 127);
;                         const f32x4 b0 = bc[g & 1][0], b1 = bc[g & 1][1];
;                         const f32x4 v0 = acc[ai][bj][m][0], v1 = acc[ai][bj][m][1];
;                         const float L2E = 1.4426950408889634f;
;                         if (isq) {
;                             const float s = 0.08838834764831845f;
;                             u32x4 o; o[0] = cvt_pk_bf16(v0[0] * s * __builtin_amdgcn_exp2f(b0[0] * L2E), v0[1] * s * __builtin_amdgcn_exp2f(b0[1] * L2E));
;                             o[1] = cvt_pk_bf16(v0[2] * s * __builtin_amdgcn_exp2f(b0[2] * L2E), v0[3] * s * __builtin_amdgcn_exp2f(b0[3] * L2E));
;                             o[2] = cvt_pk_bf16(v1[0] * s * __builtin_amdgcn_exp2f(b1[0] * L2E), v1[1] * s * __builtin_amdgcn_exp2f(b1[1] * L2E));
;                             o[3] = cvt_pk_bf16(v1[2] * s * __builtin_amdgcn_exp2f(b1[2] * L2E), v1[3] * s * __builtin_amdgcn_exp2f(b1[3] * L2E));
;                             __builtin_nontemporal_store(o, (u32x4*)(d0 + hoff));
;                         } else {
;                             u32x4 o;
;                             o[0] = cvt_pk_bf16(v0[0] * __builtin_amdgcn_exp2f(-b0[0] * L2E), v0[1] * __builtin_amdgcn_exp2f(-b0[1] * L2E));
;                             o[1] = cvt_pk_bf16(v0[2] * __builtin_amdgcn_exp2f(-b0[2] * L2E), v0[3] * __builtin_amdgcn_exp2f(-b0[3] * L2E));
;                             o[2] = cvt_pk_bf16(v1[0] * __builtin_amdgcn_exp2f(-b1[0] * L2E), v1[1] * __builtin_amdgcn_exp2f(-b1[1] * L2E));
;                             o[3] = cvt_pk_bf16(v1[2] * __builtin_amdgcn_exp2f(-b1[2] * L2E), v1[3] * __builtin_amdgcn_exp2f(-b1[3] * L2E));
;                             __builtin_nontemporal_store(o, (u32x4*)(d0 + hoff));
.LBB0_373:
	v_mul_f32_e32 v128, s33, v131
	v_exp_f32_e32 v130, v128
	v_mov_b32_e32 v151, v169
	v_mov_b32_e32 v149, v169
	v_lshl_add_u64 v[128:129], s[42:43], 0, v[150:151]
	v_mul_f32_e32 v130, v155, v130
	v_cvt_pk_bf16_f32 v147, v154, v130
	v_lshl_add_u64 v[128:129], v[128:129], 0, v[148:149]
	global_store_dwordx4 v[128:129], v[144:147], off nt
	global_load_dwordx4 v[128:131], v[152:153], off offset:528
	s_nop 0
	global_load_dwordx4 v[136:139], v[152:153], off offset:512
	s_and_b64 vcc, exec, s[8:9]
	s_mov_b64 s[54:55], -1
	s_cbranch_vccnz .LBB0_375
	s_waitcnt vmcnt(3)
	v_mul_f32_e32 v144, 0xbfb8aa3b, v140
	v_mul_f32_e32 v145, 0xbfb8aa3b, v141
	v_exp_f32_e32 v144, v144
	v_exp_f32_e32 v145, v145
	s_mov_b64 s[54:55], 0
	v_mov_b32_e32 v153, v91
	v_pk_mul_f32 v[144:145], v[92:93], v[144:145]
	s_nop 0
	v_cvt_pk_bf16_f32 v144, v144, v145
	v_mul_f32_e32 v145, 0xbfb8aa3b, v142
	v_exp_f32_e32 v146, v145
	v_mul_f32_e32 v145, 0xbfb8aa3b, v143
	v_exp_f32_e32 v147, v145
	s_nop 0
	v_pk_mul_f32 v[146:147], v[94:95], v[146:147]
	s_nop 0
	v_cvt_pk_bf16_f32 v145, v146, v147
	v_mul_f32_e32 v146, 0xbfb8aa3b, v132
	v_mul_f32_e32 v147, 0xbfb8aa3b, v133
	v_exp_f32_e32 v146, v146
	v_exp_f32_e32 v147, v147
	s_nop 0
	v_pk_mul_f32 v[146:147], v[88:89], v[146:147]
	s_nop 0
	v_cvt_pk_bf16_f32 v146, v146, v147
	v_mul_f32_e32 v147, 0xbfb8aa3b, v134
	v_exp_f32_e32 v147, v147
	s_nop 0
	v_mul_f32_e32 v152, v90, v147
.LBB0_375:
	s_andn2_b64 vcc, exec, s[54:55]
	s_mov_b32 s33, 0xbfb8aa3b
	s_cbranch_vccnz .LBB0_377
	s_waitcnt vmcnt(3)
	v_mul_f32_e32 v140, 0x3fb8aa3b, v140
	v_mul_f32_e32 v141, 0x3fb8aa3b, v141
	v_exp_f32_e32 v140, v140
	v_exp_f32_e32 v141, v141
	v_pk_mul_f32 v[144:145], v[92:93], s[34:35] op_sel_hi:[1,0]
	v_mul_f32_e32 v132, 0x3fb8aa3b, v132
	v_mul_f32_e32 v133, 0x3fb8aa3b, v133
	v_pk_mul_f32 v[140:141], v[144:145], v[140:141]
	v_exp_f32_e32 v132, v132
	v_cvt_pk_bf16_f32 v144, v140, v141
	v_mul_f32_e32 v140, 0x3fb8aa3b, v142
	v_mul_f32_e32 v141, 0x3fb8aa3b, v143
	v_exp_f32_e32 v140, v140
	v_exp_f32_e32 v141, v141
	v_exp_f32_e32 v133, v133
	v_pk_mul_f32 v[142:143], v[94:95], s[34:35] op_sel_hi:[1,0]
	s_mov_b32 s33, 0x3fb8aa3b
	v_pk_mul_f32 v[140:141], v[142:143], v[140:141]
	s_nop 0
	v_cvt_pk_bf16_f32 v145, v140, v141
	v_pk_mul_f32 v[140:141], v[88:89], s[34:35] op_sel_hi:[1,0]
	s_nop 0
	v_pk_mul_f32 v[132:133], v[140:141], v[132:133]
	s_nop 0
	v_cvt_pk_bf16_f32 v146, v132, v133
	v_mul_f32_e32 v133, 0x3fb8aa3b, v134
	v_exp_f32_e32 v190, v133
	v_mul_f32_e32 v132, 0x3db504f3, v90
	v_mov_b32_e32 v133, v91
	v_pk_mul_f32 v[152:153], v[132:133], v[190:191]
.LBB0_377:
	s_waitcnt vmcnt(3)
	v_mul_f32_e32 v132, s33, v135
	v_exp_f32_e32 v132, v132
	v_or_b32_e32 v133, 0x1000, v156
	v_mov_b32_e32 v151, v169
	v_lshlrev_b32_e32 v150, 1, v133
	v_mul_f32_e32 v132, v153, v132
	v_cvt_pk_bf16_f32 v147, v152, v132
	v_lshl_add_u64 v[132:133], s[10:11], 0, v[150:151]
	v_mov_b32_e32 v149, v169
	v_lshl_add_u64 v[132:133], v[132:133], 0, v[148:149]
	global_store_dwordx4 v[132:133], v[144:147], off nt
	v_or_b32_e32 v132, 48, v192
	v_ashrrev_i32_e32 v133, 31, v132
	v_lshlrev_b64 v[132:133], 11, v[132:133]
	v_lshl_add_u64 v[132:133], s[22:23], 0, v[132:133]
	v_lshl_add_u64 v[152:153], v[168:169], 2, v[132:133]
	global_load_dwordx4 v[132:135], v[152:153], off offset:16
	global_load_dwordx4 v[140:143], v[152:153], off
	s_waitcnt vmcnt(3)
	s_and_b64 vcc, exec, s[8:9]
	s_mov_b64 s[54:55], -1
	s_cbranch_vccnz .LBB0_379
	v_mul_f32_e32 v144, 0xbfb8aa3b, v136
	v_mul_f32_e32 v145, 0xbfb8aa3b, v137
	v_exp_f32_e32 v144, v144
	v_exp_f32_e32 v145, v145
	s_mov_b64 s[54:55], 0
	v_mov_b32_e32 v155, v83
	v_pk_mul_f32 v[144:145], v[84:85], v[144:145]
	s_nop 0
	v_cvt_pk_bf16_f32 v144, v144, v145
	v_mul_f32_e32 v145, 0xbfb8aa3b, v138
	v_exp_f32_e32 v146, v145
	v_mul_f32_e32 v145, 0xbfb8aa3b, v139
	v_exp_f32_e32 v147, v145
	s_nop 0
	v_pk_mul_f32 v[146:147], v[86:87], v[146:147]
	s_nop 0
	v_cvt_pk_bf16_f32 v145, v146, v147
	v_mul_f32_e32 v146, 0xbfb8aa3b, v128
	v_mul_f32_e32 v147, 0xbfb8aa3b, v129
	v_exp_f32_e32 v146, v146
	v_exp_f32_e32 v147, v147
	s_nop 0
	v_pk_mul_f32 v[146:147], v[80:81], v[146:147]
	s_nop 0
	v_cvt_pk_bf16_f32 v146, v146, v147
	v_mul_f32_e32 v147, 0xbfb8aa3b, v130
	v_exp_f32_e32 v147, v147
	s_nop 0
	v_mul_f32_e32 v154, v82, v147

;     __device__ __forceinline__ void operator()(const f32x4 (&acc)[2][2][4][2], const Unit& u, int wr, int wc, int fr, int fq) const {
;     ...
;             BC_LOAD(0, 0);
; #pragma unroll
;             for (int g = 0; g < 16; ++g) {
;                 const int ai = g >> 3, m = (g >> 1) & 3, bj = g & 1;
;                 const int r = row0 + ai * HALF + m * 16;
;                 if (g + 1 < 16) BC_LOAD((g + 1) & 1, g + 1);
;                 {
;                     {
;                         const int col = cb + bj * HALF + lc;
;                         const size_t hoff = ((size_t)((r >> 11) * 4 + (col >> 7)) * SEQ + (r & (SEQ - 1))) * 128 + (col & 127);
;                         const f32x4 b0 = bc[g & 1][0], b1 = bc[g & 1][1];
;                         const f32x4 v0 = acc[ai][bj][m][0], v1 = acc[ai][bj][m][1];
;                         const float L2E = 1.4426950408889634f;
;                         if (isq) {
;                             const float s = 0.08838834764831845f;
;                             u32x4 o; o[0] = cvt_pk_bf16(v0[0] * s * __builtin_amdgcn_exp2f(b0[0] * L2E), v0[1] * s * __builtin_amdgcn_exp2f(b0[1] * L2E));
;                             o[1] = cvt_pk_bf16(v0[2] * s * __builtin_amdgcn_exp2f(b0[2] * L2E), v0[3] * s * __builtin_amdgcn_exp2f(b0[3] * L2E));
;                             o[2] = cvt_pk_bf16(v1[0] * s * __builtin_amdgcn_exp2f(b1[0] * L2E), v1[1] * s * __builtin_amdgcn_exp2f(b1[1] * L2E));
;                             o[3] = cvt_pk_bf16(v1[2] * s * __builtin_amdgcn_exp2f(b1[2] * L2E), v1[3] * s * __builtin_amdgcn_exp2f(b1[3] * L2E));
;                             __builtin_nontemporal_store(o, (u32x4*)(d0 + hoff));
;                         } else {
;                             u32x4 o;
;                             o[0] = cvt_pk_bf16(v0[0] * __builtin_amdgcn_exp2f(-b0[0] * L2E), v0[1] * __builtin_amdgcn_exp2f(-b0[1] * L2E));
;                             o[1] = cvt_pk_bf16(v0[2] * __builtin_amdgcn_exp2f(-b0[2] * L2E), v0[3] * __builtin_amdgcn_exp2f(-b0[3] * L2E));
;                             o[2] = cvt_pk_bf16(v1[0] * __builtin_amdgcn_exp2f(-b1[0] * L2E), v1[1] * __builtin_amdgcn_exp2f(-b1[1] * L2E));
;                             o[3] = cvt_pk_bf16(v1[2] * __builtin_amdgcn_exp2f(-b1[2] * L2E), v1[3] * __builtin_amdgcn_exp2f(-b1[3] * L2E));
;                             __builtin_nontemporal_store(o, (u32x4*)(d0 + hoff));
.LBB0_381:
	v_mul_f32_e32 v128, s33, v131
	v_exp_f32_e32 v130, v128
	v_mov_b32_e32 v151, v169
	v_mov_b32_e32 v149, v169
	v_lshl_add_u64 v[128:129], s[42:43], 0, v[150:151]
	v_mul_f32_e32 v130, v155, v130
	v_cvt_pk_bf16_f32 v147, v154, v130
	v_lshl_add_u64 v[128:129], v[128:129], 0, v[148:149]
	global_store_dwordx4 v[128:129], v[144:147], off nt
	global_load_dwordx4 v[128:131], v[152:153], off offset:528
	s_nop 0
	global_load_dwordx4 v[136:139], v[152:153], off offset:512
	s_and_b64 vcc, exec, s[8:9]
	s_mov_b64 s[54:55], -1
	s_cbranch_vccnz .LBB0_383
	s_waitcnt vmcnt(3)
	v_mul_f32_e32 v144, 0xbfb8aa3b, v140
	v_mul_f32_e32 v145, 0xbfb8aa3b, v141
	v_exp_f32_e32 v144, v144
	v_exp_f32_e32 v145, v145
	s_mov_b64 s[54:55], 0
	v_mov_b32_e32 v151, v75
	v_pk_mul_f32 v[144:145], v[76:77], v[144:145]
	s_nop 0
	v_cvt_pk_bf16_f32 v144, v144, v145
	v_mul_f32_e32 v145, 0xbfb8aa3b, v142
	v_exp_f32_e32 v146, v145
	v_mul_f32_e32 v145, 0xbfb8aa3b, v143
	v_exp_f32_e32 v147, v145
	s_nop 0
	v_pk_mul_f32 v[146:147], v[78:79], v[146:147]
	s_nop 0
	v_cvt_pk_bf16_f32 v145, v146, v147
	v_mul_f32_e32 v146, 0xbfb8aa3b, v132
	v_mul_f32_e32 v147, 0xbfb8aa3b, v133
	v_exp_f32_e32 v146, v146
	v_exp_f32_e32 v147, v147
	s_nop 0
	v_pk_mul_f32 v[146:147], v[72:73], v[146:147]
	s_nop 0
	v_cvt_pk_bf16_f32 v146, v146, v147
	v_mul_f32_e32 v147, 0xbfb8aa3b, v134
	v_exp_f32_e32 v147, v147
	s_nop 0
	v_mul_f32_e32 v150, v74, v147
.LBB0_383:
	s_andn2_b64 vcc, exec, s[54:55]
	s_mov_b32 s33, 0xbfb8aa3b
	s_cbranch_vccnz .LBB0_385
	s_waitcnt vmcnt(3)
	v_mul_f32_e32 v140, 0x3fb8aa3b, v140
	v_mul_f32_e32 v141, 0x3fb8aa3b, v141
	v_exp_f32_e32 v140, v140
	v_exp_f32_e32 v141, v141
	v_pk_mul_f32 v[144:145], v[76:77], s[34:35] op_sel_hi:[1,0]
	v_mul_f32_e32 v132, 0x3fb8aa3b, v132
	v_mul_f32_e32 v133, 0x3fb8aa3b, v133
	v_pk_mul_f32 v[140:141], v[144:145], v[140:141]
	v_exp_f32_e32 v132, v132
	v_cvt_pk_bf16_f32 v144, v140, v141
	v_mul_f32_e32 v140, 0x3fb8aa3b, v142
	v_mul_f32_e32 v141, 0x3fb8aa3b, v143
	v_exp_f32_e32 v140, v140
	v_exp_f32_e32 v141, v141
	v_exp_f32_e32 v133, v133
	v_pk_mul_f32 v[142:143], v[78:79], s[34:35] op_sel_hi:[1,0]
	s_mov_b32 s33, 0x3fb8aa3b
	v_pk_mul_f32 v[140:141], v[142:143], v[140:141]
	s_nop 0
	v_cvt_pk_bf16_f32 v145, v140, v141
	v_pk_mul_f32 v[140:141], v[72:73], s[34:35] op_sel_hi:[1,0]
	s_nop 0
	v_pk_mul_f32 v[132:133], v[140:141], v[132:133]
	s_nop 0
	v_cvt_pk_bf16_f32 v146, v132, v133
	v_mul_f32_e32 v133, 0x3fb8aa3b, v134
	v_exp_f32_e32 v190, v133
	v_mul_f32_e32 v132, 0x3db504f3, v74
	v_mov_b32_e32 v133, v75
	v_pk_mul_f32 v[150:151], v[132:133], v[190:191]
.LBB0_385:
	s_waitcnt vmcnt(3)
	v_mul_f32_e32 v132, s33, v135
	v_exp_f32_e32 v132, v132
	v_or_b32_e32 v133, 0x1800, v156
	v_mov_b32_e32 v153, v169
	v_lshlrev_b32_e32 v152, 1, v133
	v_mul_f32_e32 v132, v151, v132
	v_cvt_pk_bf16_f32 v147, v150, v132
	v_lshl_add_u64 v[132:133], s[10:11], 0, v[152:153]
	v_mov_b32_e32 v149, v169
	v_add_u32_e32 v150, 0x80, v192
	v_lshl_add_u64 v[132:133], v[132:133], 0, v[148:149]
	v_ashrrev_i32_e32 v151, 31, v150
	global_store_dwordx4 v[132:133], v[144:147], off nt
	v_lshlrev_b64 v[132:133], 11, v[150:151]
	v_lshl_add_u64 v[132:133], s[22:23], 0, v[132:133]
	v_lshl_add_u64 v[154:155], v[168:169], 2, v[132:133]
	global_load_dwordx4 v[132:135], v[154:155], off offset:16
	global_load_dwordx4 v[140:143], v[154:155], off
	s_waitcnt vmcnt(3)
	s_and_b64 vcc, exec, s[8:9]
	s_mov_b64 s[10:11], -1
	s_cbranch_vccnz .LBB0_387
	v_mul_f32_e32 v144, 0xbfb8aa3b, v136
	v_mul_f32_e32 v145, 0xbfb8aa3b, v137
	v_exp_f32_e32 v144, v144
	v_exp_f32_e32 v145, v145
	s_mov_b64 s[10:11], 0
	v_mov_b32_e32 v157, v67
	v_pk_mul_f32 v[144:145], v[68:69], v[144:145]
	s_nop 0
	v_cvt_pk_bf16_f32 v144, v144, v145
	v_mul_f32_e32 v145, 0xbfb8aa3b, v138
	v_exp_f32_e32 v146, v145
	v_mul_f32_e32 v145, 0xbfb8aa3b, v139
	v_exp_f32_e32 v147, v145
	s_nop 0
	v_pk_mul_f32 v[146:147], v[70:71], v[146:147]
	s_nop 0
	v_cvt_pk_bf16_f32 v145, v146, v147
	v_mul_f32_e32 v146, 0xbfb8aa3b, v128
	v_mul_f32_e32 v147, 0xbfb8aa3b, v129
	v_exp_f32_e32 v146, v146
	v_exp_f32_e32 v147, v147
	s_nop 0
	v_pk_mul_f32 v[146:147], v[64:65], v[146:147]
	s_nop 0
	v_cvt_pk_bf16_f32 v146, v146, v147
	v_mul_f32_e32 v147, 0xbfb8aa3b, v130
	v_exp_f32_e32 v147, v147
	s_nop 0
	v_mul_f32_e32 v156, v66, v147

;     __device__ __forceinline__ void operator()(const f32x4 (&acc)[2][2][4][2], const Unit& u, int wr, int wc, int fr, int fq) const {
;     ...
;             BC_LOAD(0, 0);
; #pragma unroll
;             for (int g = 0; g < 16; ++g) {
;                 const int ai = g >> 3, m = (g >> 1) & 3, bj = g & 1;
;                 const int r = row0 + ai * HALF + m * 16;
;                 if (g + 1 < 16) BC_LOAD((g + 1) & 1, g + 1);
;                 {
;                     {
;                         const int col = cb + bj * HALF + lc;
;                         const size_t hoff = ((size_t)((r >> 11) * 4 + (col >> 7)) * SEQ + (r & (SEQ - 1))) * 128 + (col & 127);
;                         const f32x4 b0 = bc[g & 1][0], b1 = bc[g & 1][1];
;                         const f32x4 v0 = acc[ai][bj][m][0], v1 = acc[ai][bj][m][1];
;                         const float L2E = 1.4426950408889634f;
;                         if (isq) {
;                             const float s = 0.08838834764831845f;
;                             u32x4 o; o[0] = cvt_pk_bf16(v0[0] * s * __builtin_amdgcn_exp2f(b0[0] * L2E), v0[1] * s * __builtin_amdgcn_exp2f(b0[1] * L2E));
;                             o[1] = cvt_pk_bf16(v0[2] * s * __builtin_amdgcn_exp2f(b0[2] * L2E), v0[3] * s * __builtin_amdgcn_exp2f(b0[3] * L2E));
;                             o[2] = cvt_pk_bf16(v1[0] * s * __builtin_amdgcn_exp2f(b1[0] * L2E), v1[1] * s * __builtin_amdgcn_exp2f(b1[1] * L2E));
;                             o[3] = cvt_pk_bf16(v1[2] * s * __builtin_amdgcn_exp2f(b1[2] * L2E), v1[3] * s * __builtin_amdgcn_exp2f(b1[3] * L2E));
;                             __builtin_nontemporal_store(o, (u32x4*)(d0 + hoff));
;                         } else {
;                             u32x4 o;
;                             o[0] = cvt_pk_bf16(v0[0] * __builtin_amdgcn_exp2f(-b0[0] * L2E), v0[1] * __builtin_amdgcn_exp2f(-b0[1] * L2E));
;                             o[1] = cvt_pk_bf16(v0[2] * __builtin_amdgcn_exp2f(-b0[2] * L2E), v0[3] * __builtin_amdgcn_exp2f(-b0[3] * L2E));
;                             o[2] = cvt_pk_bf16(v1[0] * __builtin_amdgcn_exp2f(-b1[0] * L2E), v1[1] * __builtin_amdgcn_exp2f(-b1[1] * L2E));
;                             o[3] = cvt_pk_bf16(v1[2] * __builtin_amdgcn_exp2f(-b1[2] * L2E), v1[3] * __builtin_amdgcn_exp2f(-b1[3] * L2E));
;                             __builtin_nontemporal_store(o, (u32x4*)(d0 + hoff));
.LBB0_389:
	v_mul_f32_e32 v128, s10, v131
	v_exp_f32_e32 v130, v128
	v_mov_b32_e32 v153, v169
	v_mov_b32_e32 v149, v169
	v_lshl_add_u64 v[128:129], s[42:43], 0, v[152:153]
	v_mul_f32_e32 v130, v157, v130
	v_cvt_pk_bf16_f32 v147, v156, v130
	v_lshl_add_u64 v[128:129], v[128:129], 0, v[148:149]
	global_store_dwordx4 v[128:129], v[144:147], off nt
	global_load_dwordx4 v[128:131], v[154:155], off offset:528
	s_nop 0
	global_load_dwordx4 v[136:139], v[154:155], off offset:512
	s_and_b64 vcc, exec, s[8:9]
	s_mov_b64 s[10:11], -1
	s_cbranch_vccnz .LBB0_391
	s_waitcnt vmcnt(3)
	v_mul_f32_e32 v144, 0xbfb8aa3b, v140
	v_mul_f32_e32 v145, 0xbfb8aa3b, v141
	v_exp_f32_e32 v144, v144
	v_exp_f32_e32 v145, v145
	s_mov_b64 s[10:11], 0
	v_mov_b32_e32 v153, v59
	v_pk_mul_f32 v[144:145], v[60:61], v[144:145]
	s_nop 0
	v_cvt_pk_bf16_f32 v144, v144, v145
	v_mul_f32_e32 v145, 0xbfb8aa3b, v142
	v_exp_f32_e32 v146, v145
	v_mul_f32_e32 v145, 0xbfb8aa3b, v143
	v_exp_f32_e32 v147, v145
	s_nop 0
	v_pk_mul_f32 v[146:147], v[62:63], v[146:147]
	s_nop 0
	v_cvt_pk_bf16_f32 v145, v146, v147
	v_mul_f32_e32 v146, 0xbfb8aa3b, v132
	v_mul_f32_e32 v147, 0xbfb8aa3b, v133
	v_exp_f32_e32 v146, v146
	v_exp_f32_e32 v147, v147
	s_nop 0
	v_pk_mul_f32 v[146:147], v[56:57], v[146:147]
	s_nop 0
	v_cvt_pk_bf16_f32 v146, v146, v147
	v_mul_f32_e32 v147, 0xbfb8aa3b, v134
	v_exp_f32_e32 v147, v147
	s_nop 0
	v_mul_f32_e32 v152, v58, v147
.LBB0_391:
	s_andn2_b64 vcc, exec, s[10:11]
	s_mov_b32 s10, 0xbfb8aa3b
	s_cbranch_vccnz .LBB0_393
	s_waitcnt vmcnt(3)
	v_mul_f32_e32 v140, 0x3fb8aa3b, v140
	v_mul_f32_e32 v141, 0x3fb8aa3b, v141
	v_exp_f32_e32 v140, v140
	v_exp_f32_e32 v141, v141
	v_pk_mul_f32 v[144:145], v[60:61], s[34:35] op_sel_hi:[1,0]
	v_mul_f32_e32 v132, 0x3fb8aa3b, v132
	v_mul_f32_e32 v133, 0x3fb8aa3b, v133
	v_pk_mul_f32 v[140:141], v[144:145], v[140:141]
	v_exp_f32_e32 v132, v132
	v_cvt_pk_bf16_f32 v144, v140, v141
	v_mul_f32_e32 v140, 0x3fb8aa3b, v142
	v_mul_f32_e32 v141, 0x3fb8aa3b, v143
	v_exp_f32_e32 v140, v140
	v_exp_f32_e32 v141, v141
	v_exp_f32_e32 v133, v133
	v_pk_mul_f32 v[142:143], v[62:63], s[34:35] op_sel_hi:[1,0]
	s_mov_b32 s10, 0x3fb8aa3b
	v_pk_mul_f32 v[140:141], v[142:143], v[140:141]
	s_nop 0
	v_cvt_pk_bf16_f32 v145, v140, v141
	v_pk_mul_f32 v[140:141], v[56:57], s[34:35] op_sel_hi:[1,0]
	s_nop 0
	v_pk_mul_f32 v[132:133], v[140:141], v[132:133]
	s_nop 0
	v_cvt_pk_bf16_f32 v146, v132, v133
	v_mul_f32_e32 v133, 0x3fb8aa3b, v134
	v_exp_f32_e32 v190, v133
	v_mul_f32_e32 v132, 0x3db504f3, v58
	v_mov_b32_e32 v133, v59
	v_pk_mul_f32 v[152:153], v[132:133], v[190:191]
.LBB0_393:
	s_waitcnt vmcnt(3)
	v_mul_f32_e32 v133, s10, v135
	v_ashrrev_i32_e32 v132, 9, v150
	v_exp_f32_e32 v134, v133
	v_and_b32_e32 v151, -4, v132
	v_add_u32_e32 v132, s17, v151
	v_ashrrev_i32_e32 v133, 31, v132
	v_lshlrev_b32_e32 v135, 7, v150
	v_and_b32_e32 v193, 0x3e780, v135
	v_mul_f32_e32 v134, v153, v134
	v_lshlrev_b64 v[132:133], 19, v[132:133]
	v_cvt_pk_bf16_f32 v147, v152, v134
	v_lshl_add_u64 v[152:153], s[2:3], 0, v[132:133]
	v_lshlrev_b32_e32 v156, 1, v193
	v_mov_b32_e32 v157, v169
	v_lshl_add_u64 v[132:133], v[152:153], 0, v[156:157]
	v_mov_b32_e32 v149, v169
	v_lshl_add_u64 v[132:133], v[132:133], 0, v[148:149]
	global_store_dwordx4 v[132:133], v[144:147], off nt
	v_or_b32_e32 v132, 16, v150
	v_ashrrev_i32_e32 v133, 31, v132
	v_lshlrev_b64 v[132:133], 11, v[132:133]
	v_lshl_add_u64 v[132:133], s[22:23], 0, v[132:133]
	v_lshl_add_u64 v[158:159], v[168:169], 2, v[132:133]
	global_load_dwordx4 v[132:135], v[158:159], off offset:16
	global_load_dwordx4 v[140:143], v[158:159], off
	s_waitcnt vmcnt(3)
	s_and_b64 vcc, exec, s[8:9]
	s_mov_b64 s[10:11], -1
	s_cbranch_vccnz .LBB0_395
	v_mul_f32_e32 v144, 0xbfb8aa3b, v136
	v_mul_f32_e32 v145, 0xbfb8aa3b, v137
	v_exp_f32_e32 v144, v144
	v_exp_f32_e32 v145, v145
	s_mov_b64 s[10:11], 0
	v_mov_b32_e32 v155, v51
	v_pk_mul_f32 v[144:145], v[52:53], v[144:145]
	s_nop 0
	v_cvt_pk_bf16_f32 v144, v144, v145
	v_mul_f32_e32 v145, 0xbfb8aa3b, v138
	v_exp_f32_e32 v146, v145
	v_mul_f32_e32 v145, 0xbfb8aa3b, v139
	v_exp_f32_e32 v147, v145
	s_nop 0
	v_pk_mul_f32 v[146:147], v[54:55], v[146:147]
	s_nop 0
	v_cvt_pk_bf16_f32 v145, v146, v147
	v_mul_f32_e32 v146, 0xbfb8aa3b, v128
	v_mul_f32_e32 v147, 0xbfb8aa3b, v129
	v_exp_f32_e32 v146, v146
	v_exp_f32_e32 v147, v147
	s_nop 0
	v_pk_mul_f32 v[146:147], v[48:49], v[146:147]
	s_nop 0
	v_cvt_pk_bf16_f32 v146, v146, v147
	v_mul_f32_e32 v147, 0xbfb8aa3b, v130
	v_exp_f32_e32 v147, v147
	s_nop 0
	v_mul_f32_e32 v154, v50, v147

;     __device__ __forceinline__ void operator()(const f32x4 (&acc)[2][2][4][2], const Unit& u, int wr, int wc, int fr, int fq) const {
;     ...
;             BC_LOAD(0, 0);
; #pragma unroll
;             for (int g = 0; g < 16; ++g) {
;                 const int ai = g >> 3, m = (g >> 1) & 3, bj = g & 1;
;                 const int r = row0 + ai * HALF + m * 16;
;                 if (g + 1 < 16) BC_LOAD((g + 1) & 1, g + 1);
;                 {
;                     {
;                         const int col = cb + bj * HALF + lc;
;                         const size_t hoff = ((size_t)((r >> 11) * 4 + (col >> 7)) * SEQ + (r & (SEQ - 1))) * 128 + (col & 127);
;                         const f32x4 b0 = bc[g & 1][0], b1 = bc[g & 1][1];
;                         const f32x4 v0 = acc[ai][bj][m][0], v1 = acc[ai][bj][m][1];
;                         const float L2E = 1.4426950408889634f;
;                         if (isq) {
;                             const float s = 0.08838834764831845f;
;                             u32x4 o; o[0] = cvt_pk_bf16(v0[0] * s * __builtin_amdgcn_exp2f(b0[0] * L2E), v0[1] * s * __builtin_amdgcn_exp2f(b0[1] * L2E));
;                             o[1] = cvt_pk_bf16(v0[2] * s * __builtin_amdgcn_exp2f(b0[2] * L2E), v0[3] * s * __builtin_amdgcn_exp2f(b0[3] * L2E));
;                             o[2] = cvt_pk_bf16(v1[0] * s * __builtin_amdgcn_exp2f(b1[0] * L2E), v1[1] * s * __builtin_amdgcn_exp2f(b1[1] * L2E));
;                             o[3] = cvt_pk_bf16(v1[2] * s * __builtin_amdgcn_exp2f(b1[2] * L2E), v1[3] * s * __builtin_amdgcn_exp2f(b1[3] * L2E));
;                             __builtin_nontemporal_store(o, (u32x4*)(d0 + hoff));
;                         } else {
;                             u32x4 o;
;                             o[0] = cvt_pk_bf16(v0[0] * __builtin_amdgcn_exp2f(-b0[0] * L2E), v0[1] * __builtin_amdgcn_exp2f(-b0[1] * L2E));
;                             o[1] = cvt_pk_bf16(v0[2] * __builtin_amdgcn_exp2f(-b0[2] * L2E), v0[3] * __builtin_amdgcn_exp2f(-b0[3] * L2E));
;                             o[2] = cvt_pk_bf16(v1[0] * __builtin_amdgcn_exp2f(-b1[0] * L2E), v1[1] * __builtin_amdgcn_exp2f(-b1[1] * L2E));
;                             o[3] = cvt_pk_bf16(v1[2] * __builtin_amdgcn_exp2f(-b1[2] * L2E), v1[3] * __builtin_amdgcn_exp2f(-b1[3] * L2E));
;                             __builtin_nontemporal_store(o, (u32x4*)(d0 + hoff));
.LBB0_397:
	v_mul_f32_e32 v128, s10, v131
	v_exp_f32_e32 v130, v128
	v_add_u32_e32 v128, s18, v151
	v_ashrrev_i32_e32 v129, 31, v128
	v_lshlrev_b64 v[128:129], 19, v[128:129]
	v_mul_f32_e32 v130, v155, v130
	v_cvt_pk_bf16_f32 v147, v154, v130
	v_lshl_add_u64 v[154:155], s[2:3], 0, v[128:129]
	v_mov_b32_e32 v157, v169
	v_lshl_add_u64 v[128:129], v[154:155], 0, v[156:157]
	v_mov_b32_e32 v149, v169
	v_lshl_add_u64 v[128:129], v[128:129], 0, v[148:149]
	global_store_dwordx4 v[128:129], v[144:147], off nt
	global_load_dwordx4 v[128:131], v[158:159], off offset:528
	s_nop 0
	global_load_dwordx4 v[136:139], v[158:159], off offset:512
	s_and_b64 vcc, exec, s[8:9]
	s_mov_b64 s[2:3], -1
	s_cbranch_vccnz .LBB0_399
	s_waitcnt vmcnt(3)
	v_mul_f32_e32 v144, 0xbfb8aa3b, v140
	v_mul_f32_e32 v145, 0xbfb8aa3b, v141
	v_exp_f32_e32 v144, v144
	v_exp_f32_e32 v145, v145
	s_mov_b64 s[2:3], 0
	v_mov_b32_e32 v159, v43
	v_pk_mul_f32 v[144:145], v[44:45], v[144:145]
	s_nop 0
	v_cvt_pk_bf16_f32 v144, v144, v145
	v_mul_f32_e32 v145, 0xbfb8aa3b, v142
	v_exp_f32_e32 v146, v145
	v_mul_f32_e32 v145, 0xbfb8aa3b, v143
	v_exp_f32_e32 v147, v145
	s_nop 0
	v_pk_mul_f32 v[146:147], v[46:47], v[146:147]
	s_nop 0
	v_cvt_pk_bf16_f32 v145, v146, v147
	v_mul_f32_e32 v146, 0xbfb8aa3b, v132
	v_mul_f32_e32 v147, 0xbfb8aa3b, v133
	v_exp_f32_e32 v146, v146
	v_exp_f32_e32 v147, v147
	s_nop 0
	v_pk_mul_f32 v[146:147], v[40:41], v[146:147]
	s_nop 0
	v_cvt_pk_bf16_f32 v146, v146, v147
	v_mul_f32_e32 v147, 0xbfb8aa3b, v134
	v_exp_f32_e32 v147, v147
	s_nop 0
	v_mul_f32_e32 v158, v42, v147
.LBB0_399:
	s_andn2_b64 vcc, exec, s[2:3]
	s_mov_b32 s2, 0xbfb8aa3b
	s_cbranch_vccnz .LBB0_401
	s_waitcnt vmcnt(3)
	v_mul_f32_e32 v140, 0x3fb8aa3b, v140
	v_mul_f32_e32 v141, 0x3fb8aa3b, v141
	v_exp_f32_e32 v140, v140
	v_exp_f32_e32 v141, v141
	v_pk_mul_f32 v[144:145], v[44:45], s[34:35] op_sel_hi:[1,0]
	v_mul_f32_e32 v132, 0x3fb8aa3b, v132
	v_mul_f32_e32 v133, 0x3fb8aa3b, v133
	v_pk_mul_f32 v[140:141], v[144:145], v[140:141]
	v_exp_f32_e32 v132, v132
	v_cvt_pk_bf16_f32 v144, v140, v141
	v_mul_f32_e32 v140, 0x3fb8aa3b, v142
	v_mul_f32_e32 v141, 0x3fb8aa3b, v143
	v_exp_f32_e32 v140, v140
	v_exp_f32_e32 v141, v141
	v_exp_f32_e32 v133, v133
	v_pk_mul_f32 v[142:143], v[46:47], s[34:35] op_sel_hi:[1,0]
	v_mul_f32_e32 v134, 0x3fb8aa3b, v134
	v_pk_mul_f32 v[140:141], v[142:143], v[140:141]
	v_exp_f32_e32 v190, v134
	v_cvt_pk_bf16_f32 v145, v140, v141
	v_pk_mul_f32 v[140:141], v[40:41], s[34:35] op_sel_hi:[1,0]
	s_mov_b32 s2, 0x3fb8aa3b
	v_pk_mul_f32 v[132:133], v[140:141], v[132:133]
	s_nop 0
	v_cvt_pk_bf16_f32 v146, v132, v133
	v_mul_f32_e32 v132, 0x3db504f3, v42
	v_mov_b32_e32 v133, v43
	v_pk_mul_f32 v[158:159], v[132:133], v[190:191]
.LBB0_401:
	s_waitcnt vmcnt(3)
	v_mul_f32_e32 v132, s2, v135
	v_exp_f32_e32 v132, v132
	v_or_b32_e32 v133, 0x800, v193
	v_mov_b32_e32 v157, v169
	v_lshlrev_b32_e32 v156, 1, v133
	v_mul_f32_e32 v132, v159, v132
	v_cvt_pk_bf16_f32 v147, v158, v132
	v_lshl_add_u64 v[132:133], v[152:153], 0, v[156:157]
	v_mov_b32_e32 v149, v169
	v_lshl_add_u64 v[132:133], v[132:133], 0, v[148:149]
	global_store_dwordx4 v[132:133], v[144:147], off nt
	v_or_b32_e32 v132, 32, v150
	v_ashrrev_i32_e32 v133, 31, v132
	v_lshlrev_b64 v[132:133], 11, v[132:133]
	v_lshl_add_u64 v[132:133], s[22:23], 0, v[132:133]
	v_lshl_add_u64 v[158:159], v[168:169], 2, v[132:133]
	global_load_dwordx4 v[132:135], v[158:159], off offset:16
	global_load_dwordx4 v[140:143], v[158:159], off
	s_waitcnt vmcnt(3)
	s_and_b64 vcc, exec, s[8:9]
	s_mov_b64 s[2:3], -1
	s_cbranch_vccnz .LBB0_403
	v_mul_f32_e32 v144, 0xbfb8aa3b, v136
	v_mul_f32_e32 v145, 0xbfb8aa3b, v137
	v_exp_f32_e32 v144, v144
	v_exp_f32_e32 v145, v145
	s_mov_b64 s[2:3], 0
	v_mov_b32_e32 v195, v35
	v_pk_mul_f32 v[144:145], v[36:37], v[144:145]
	s_nop 0
	v_cvt_pk_bf16_f32 v144, v144, v145
	v_mul_f32_e32 v145, 0xbfb8aa3b, v138
	v_exp_f32_e32 v146, v145
	v_mul_f32_e32 v145, 0xbfb8aa3b, v139
	v_exp_f32_e32 v147, v145
	s_nop 0
	v_pk_mul_f32 v[146:147], v[38:39], v[146:147]
	s_nop 0
	v_cvt_pk_bf16_f32 v145, v146, v147
	v_mul_f32_e32 v146, 0xbfb8aa3b, v128
	v_mul_f32_e32 v147, 0xbfb8aa3b, v129
	v_exp_f32_e32 v146, v146
	v_exp_f32_e32 v147, v147
	s_nop 0
	v_pk_mul_f32 v[146:147], v[32:33], v[146:147]
	s_nop 0
	v_cvt_pk_bf16_f32 v146, v146, v147
	v_mul_f32_e32 v147, 0xbfb8aa3b, v130
	v_exp_f32_e32 v147, v147
	s_nop 0
	v_mul_f32_e32 v194, v34, v147

;     __device__ __forceinline__ void operator()(const f32x4 (&acc)[2][2][4][2], const Unit& u, int wr, int wc, int fr, int fq) const {
;     ...
;             BC_LOAD(0, 0);
; #pragma unroll
;             for (int g = 0; g < 16; ++g) {
;                 const int ai = g >> 3, m = (g >> 1) & 3, bj = g & 1;
;                 const int r = row0 + ai * HALF + m * 16;
;                 if (g + 1 < 16) BC_LOAD((g + 1) & 1, g + 1);
;                 {
;                     {
;                         const int col = cb + bj * HALF + lc;
;                         const size_t hoff = ((size_t)((r >> 11) * 4 + (col >> 7)) * SEQ + (r & (SEQ - 1))) * 128 + (col & 127);
;                         const f32x4 b0 = bc[g & 1][0], b1 = bc[g & 1][1];
;                         const f32x4 v0 = acc[ai][bj][m][0], v1 = acc[ai][bj][m][1];
;                         const float L2E = 1.4426950408889634f;
;                         if (isq) {
;                             const float s = 0.08838834764831845f;
;                             u32x4 o; o[0] = cvt_pk_bf16(v0[0] * s * __builtin_amdgcn_exp2f(b0[0] * L2E), v0[1] * s * __builtin_amdgcn_exp2f(b0[1] * L2E));
;                             o[1] = cvt_pk_bf16(v0[2] * s * __builtin_amdgcn_exp2f(b0[2] * L2E), v0[3] * s * __builtin_amdgcn_exp2f(b0[3] * L2E));
;                             o[2] = cvt_pk_bf16(v1[0] * s * __builtin_amdgcn_exp2f(b1[0] * L2E), v1[1] * s * __builtin_amdgcn_exp2f(b1[1] * L2E));
;                             o[3] = cvt_pk_bf16(v1[2] * s * __builtin_amdgcn_exp2f(b1[2] * L2E), v1[3] * s * __builtin_amdgcn_exp2f(b1[3] * L2E));
;                             __builtin_nontemporal_store(o, (u32x4*)(d0 + hoff));
;                         } else {
;                             u32x4 o;
;                             o[0] = cvt_pk_bf16(v0[0] * __builtin_amdgcn_exp2f(-b0[0] * L2E), v0[1] * __builtin_amdgcn_exp2f(-b0[1] * L2E));
;                             o[1] = cvt_pk_bf16(v0[2] * __builtin_amdgcn_exp2f(-b0[2] * L2E), v0[3] * __builtin_amdgcn_exp2f(-b0[3] * L2E));
;                             o[2] = cvt_pk_bf16(v1[0] * __builtin_amdgcn_exp2f(-b1[0] * L2E), v1[1] * __builtin_amdgcn_exp2f(-b1[1] * L2E));
;                             o[3] = cvt_pk_bf16(v1[2] * __builtin_amdgcn_exp2f(-b1[2] * L2E), v1[3] * __builtin_amdgcn_exp2f(-b1[3] * L2E));
;                             __builtin_nontemporal_store(o, (u32x4*)(d0 + hoff));
.LBB0_405:
	v_mul_f32_e32 v128, s2, v131
	v_exp_f32_e32 v130, v128
	v_mov_b32_e32 v157, v169
	v_mov_b32_e32 v149, v169
	v_lshl_add_u64 v[128:129], v[154:155], 0, v[156:157]
	v_mul_f32_e32 v130, v195, v130
	v_cvt_pk_bf16_f32 v147, v194, v130
	v_lshl_add_u64 v[128:129], v[128:129], 0, v[148:149]
	global_store_dwordx4 v[128:129], v[144:147], off nt
	global_load_dwordx4 v[128:131], v[158:159], off offset:528
	s_nop 0
	global_load_dwordx4 v[136:139], v[158:159], off offset:512
	s_and_b64 vcc, exec, s[8:9]
	s_mov_b64 s[2:3], -1
	s_cbranch_vccnz .LBB0_407
	s_waitcnt vmcnt(3)
	v_mul_f32_e32 v144, 0xbfb8aa3b, v140
	v_mul_f32_e32 v145, 0xbfb8aa3b, v141
	v_exp_f32_e32 v144, v144
	v_exp_f32_e32 v145, v145
	s_mov_b64 s[2:3], 0
	v_mov_b32_e32 v159, v27
	v_pk_mul_f32 v[144:145], v[28:29], v[144:145]
	s_nop 0
	v_cvt_pk_bf16_f32 v144, v144, v145
	v_mul_f32_e32 v145, 0xbfb8aa3b, v142
	v_exp_f32_e32 v146, v145
	v_mul_f32_e32 v145, 0xbfb8aa3b, v143
	v_exp_f32_e32 v147, v145
	s_nop 0
	v_pk_mul_f32 v[146:147], v[30:31], v[146:147]
	s_nop 0
	v_cvt_pk_bf16_f32 v145, v146, v147
	v_mul_f32_e32 v146, 0xbfb8aa3b, v132
	v_mul_f32_e32 v147, 0xbfb8aa3b, v133
	v_exp_f32_e32 v146, v146
	v_exp_f32_e32 v147, v147
	s_nop 0
	v_pk_mul_f32 v[146:147], v[24:25], v[146:147]
	s_nop 0
	v_cvt_pk_bf16_f32 v146, v146, v147
	v_mul_f32_e32 v147, 0xbfb8aa3b, v134
	v_exp_f32_e32 v147, v147
	s_nop 0
	v_mul_f32_e32 v158, v26, v147
.LBB0_407:
	s_andn2_b64 vcc, exec, s[2:3]
	s_mov_b32 s2, 0xbfb8aa3b
	s_cbranch_vccnz .LBB0_409
	s_waitcnt vmcnt(3)
	v_mul_f32_e32 v140, 0x3fb8aa3b, v140
	v_mul_f32_e32 v141, 0x3fb8aa3b, v141
	v_exp_f32_e32 v140, v140
	v_exp_f32_e32 v141, v141
	v_pk_mul_f32 v[144:145], v[28:29], s[34:35] op_sel_hi:[1,0]
	v_mul_f32_e32 v132, 0x3fb8aa3b, v132
	v_mul_f32_e32 v133, 0x3fb8aa3b, v133
	v_pk_mul_f32 v[140:141], v[144:145], v[140:141]
	v_exp_f32_e32 v132, v132
	v_cvt_pk_bf16_f32 v144, v140, v141
	v_mul_f32_e32 v140, 0x3fb8aa3b, v142
	v_mul_f32_e32 v141, 0x3fb8aa3b, v143
	v_exp_f32_e32 v140, v140
	v_exp_f32_e32 v141, v141
	v_exp_f32_e32 v133, v133
	v_pk_mul_f32 v[142:143], v[30:31], s[34:35] op_sel_hi:[1,0]
	v_mul_f32_e32 v134, 0x3fb8aa3b, v134
	v_pk_mul_f32 v[140:141], v[142:143], v[140:141]
	v_exp_f32_e32 v190, v134
	v_cvt_pk_bf16_f32 v145, v140, v141
	v_pk_mul_f32 v[140:141], v[24:25], s[34:35] op_sel_hi:[1,0]
	s_mov_b32 s2, 0x3fb8aa3b
	v_pk_mul_f32 v[132:133], v[140:141], v[132:133]
	s_nop 0
	v_cvt_pk_bf16_f32 v146, v132, v133
	v_mul_f32_e32 v132, 0x3db504f3, v26
	v_mov_b32_e32 v133, v27
	v_pk_mul_f32 v[158:159], v[132:133], v[190:191]
.LBB0_409:
	s_waitcnt vmcnt(3)
	v_mul_f32_e32 v132, s2, v135
	v_exp_f32_e32 v132, v132
	v_or_b32_e32 v133, 0x1000, v193
	v_mov_b32_e32 v157, v169
	v_lshlrev_b32_e32 v156, 1, v133
	v_mul_f32_e32 v132, v159, v132
	v_cvt_pk_bf16_f32 v147, v158, v132
	v_lshl_add_u64 v[132:133], v[152:153], 0, v[156:157]
	v_mov_b32_e32 v149, v169
	v_lshl_add_u64 v[132:133], v[132:133], 0, v[148:149]
	global_store_dwordx4 v[132:133], v[144:147], off nt
	v_or_b32_e32 v132, 48, v150
	v_ashrrev_i32_e32 v133, 31, v132
	v_lshlrev_b64 v[132:133], 11, v[132:133]
	v_lshl_add_u64 v[132:133], s[22:23], 0, v[132:133]
	v_lshl_add_u64 v[150:151], v[168:169], 2, v[132:133]
	global_load_dwordx4 v[132:135], v[150:151], off offset:16
	global_load_dwordx4 v[140:143], v[150:151], off
	s_waitcnt vmcnt(3)
	s_and_b64 vcc, exec, s[8:9]
	s_mov_b64 s[2:3], -1
	s_cbranch_vccnz .LBB0_411
	v_mul_f32_e32 v144, 0xbfb8aa3b, v136
	v_mul_f32_e32 v145, 0xbfb8aa3b, v137
	v_exp_f32_e32 v144, v144
	v_exp_f32_e32 v145, v145
	s_mov_b64 s[2:3], 0
	v_mov_b32_e32 v159, v19
	v_pk_mul_f32 v[144:145], v[20:21], v[144:145]
	s_nop 0
	v_cvt_pk_bf16_f32 v144, v144, v145
	v_mul_f32_e32 v145, 0xbfb8aa3b, v138
	v_exp_f32_e32 v146, v145
	v_mul_f32_e32 v145, 0xbfb8aa3b, v139
	v_exp_f32_e32 v147, v145
	s_nop 0
	v_pk_mul_f32 v[146:147], v[22:23], v[146:147]
	s_nop 0
	v_cvt_pk_bf16_f32 v145, v146, v147
	v_mul_f32_e32 v146, 0xbfb8aa3b, v128
	v_mul_f32_e32 v147, 0xbfb8aa3b, v129
	v_exp_f32_e32 v146, v146
	v_exp_f32_e32 v147, v147
	s_nop 0
	v_pk_mul_f32 v[146:147], v[16:17], v[146:147]
	s_nop 0
	v_cvt_pk_bf16_f32 v146, v146, v147
	v_mul_f32_e32 v147, 0xbfb8aa3b, v130
	v_exp_f32_e32 v147, v147
	s_nop 0
	v_mul_f32_e32 v158, v18, v147

;     __device__ __forceinline__ void operator()(const f32x4 (&acc)[2][2][4][2], const Unit& u, int wr, int wc, int fr, int fq) const {
;     ...
;             BC_LOAD(0, 0);
; #pragma unroll
;             for (int g = 0; g < 16; ++g) {
;                 const int ai = g >> 3, m = (g >> 1) & 3, bj = g & 1;
;                 const int r = row0 + ai * HALF + m * 16;
;                 if (g + 1 < 16) BC_LOAD((g + 1) & 1, g + 1);
;                 {
;                     {
;                         const int col = cb + bj * HALF + lc;
;                         const size_t hoff = ((size_t)((r >> 11) * 4 + (col >> 7)) * SEQ + (r & (SEQ - 1))) * 128 + (col & 127);
;                         const f32x4 b0 = bc[g & 1][0], b1 = bc[g & 1][1];
;                         const f32x4 v0 = acc[ai][bj][m][0], v1 = acc[ai][bj][m][1];
;                         const float L2E = 1.4426950408889634f;
;                         if (isq) {
;                             const float s = 0.08838834764831845f;
;                             u32x4 o; o[0] = cvt_pk_bf16(v0[0] * s * __builtin_amdgcn_exp2f(b0[0] * L2E), v0[1] * s * __builtin_amdgcn_exp2f(b0[1] * L2E));
;                             o[1] = cvt_pk_bf16(v0[2] * s * __builtin_amdgcn_exp2f(b0[2] * L2E), v0[3] * s * __builtin_amdgcn_exp2f(b0[3] * L2E));
;                             o[2] = cvt_pk_bf16(v1[0] * s * __builtin_amdgcn_exp2f(b1[0] * L2E), v1[1] * s * __builtin_amdgcn_exp2f(b1[1] * L2E));
;                             o[3] = cvt_pk_bf16(v1[2] * s * __builtin_amdgcn_exp2f(b1[2] * L2E), v1[3] * s * __builtin_amdgcn_exp2f(b1[3] * L2E));
;                             __builtin_nontemporal_store(o, (u32x4*)(d0 + hoff));
;                         } else {
;                             u32x4 o;
;                             o[0] = cvt_pk_bf16(v0[0] * __builtin_amdgcn_exp2f(-b0[0] * L2E), v0[1] * __builtin_amdgcn_exp2f(-b0[1] * L2E));
;                             o[1] = cvt_pk_bf16(v0[2] * __builtin_amdgcn_exp2f(-b0[2] * L2E), v0[3] * __builtin_amdgcn_exp2f(-b0[3] * L2E));
;                             o[2] = cvt_pk_bf16(v1[0] * __builtin_amdgcn_exp2f(-b1[0] * L2E), v1[1] * __builtin_amdgcn_exp2f(-b1[1] * L2E));
;                             o[3] = cvt_pk_bf16(v1[2] * __builtin_amdgcn_exp2f(-b1[2] * L2E), v1[3] * __builtin_amdgcn_exp2f(-b1[3] * L2E));
;                             __builtin_nontemporal_store(o, (u32x4*)(d0 + hoff));
.LBB0_413:
	v_mul_f32_e32 v128, s2, v131
	v_exp_f32_e32 v130, v128
	v_mov_b32_e32 v157, v169
	v_mov_b32_e32 v149, v169
	v_lshl_add_u64 v[128:129], v[154:155], 0, v[156:157]
	v_mul_f32_e32 v130, v159, v130
	v_cvt_pk_bf16_f32 v147, v158, v130
	v_lshl_add_u64 v[128:129], v[128:129], 0, v[148:149]
	global_store_dwordx4 v[128:129], v[144:147], off nt
	global_load_dwordx4 v[128:131], v[150:151], off offset:528
	s_nop 0
	global_load_dwordx4 v[136:139], v[150:151], off offset:512
	s_and_b64 vcc, exec, s[8:9]
	s_mov_b64 s[2:3], -1
	s_cbranch_vccnz .LBB0_415
	s_waitcnt vmcnt(3)
	v_mul_f32_e32 v144, 0xbfb8aa3b, v140
	v_mul_f32_e32 v145, 0xbfb8aa3b, v141
	v_exp_f32_e32 v144, v144
	v_exp_f32_e32 v145, v145
	s_mov_b64 s[2:3], 0
	v_mov_b32_e32 v151, v11
	v_pk_mul_f32 v[144:145], v[12:13], v[144:145]
	s_nop 0
	v_cvt_pk_bf16_f32 v144, v144, v145
	v_mul_f32_e32 v145, 0xbfb8aa3b, v142
	v_exp_f32_e32 v146, v145
	v_mul_f32_e32 v145, 0xbfb8aa3b, v143
	v_exp_f32_e32 v147, v145
	s_nop 0
	v_pk_mul_f32 v[146:147], v[14:15], v[146:147]
	s_nop 0
	v_cvt_pk_bf16_f32 v145, v146, v147
	v_mul_f32_e32 v146, 0xbfb8aa3b, v132
	v_mul_f32_e32 v147, 0xbfb8aa3b, v133
	v_exp_f32_e32 v146, v146
	v_exp_f32_e32 v147, v147
	s_nop 0
	v_pk_mul_f32 v[146:147], v[8:9], v[146:147]
	s_nop 0
	v_cvt_pk_bf16_f32 v146, v146, v147
	v_mul_f32_e32 v147, 0xbfb8aa3b, v134
	v_exp_f32_e32 v147, v147
	s_nop 0
	v_mul_f32_e32 v150, v10, v147
.LBB0_415:
	s_andn2_b64 vcc, exec, s[2:3]
	s_mov_b32 s2, 0xbfb8aa3b
	s_cbranch_vccnz .LBB0_417
	s_waitcnt vmcnt(3)
	v_mul_f32_e32 v140, 0x3fb8aa3b, v140
	v_mul_f32_e32 v141, 0x3fb8aa3b, v141
	v_exp_f32_e32 v140, v140
	v_exp_f32_e32 v141, v141
	v_pk_mul_f32 v[144:145], v[12:13], s[34:35] op_sel_hi:[1,0]
	v_mul_f32_e32 v132, 0x3fb8aa3b, v132
	v_mul_f32_e32 v133, 0x3fb8aa3b, v133
	v_pk_mul_f32 v[140:141], v[144:145], v[140:141]
	v_exp_f32_e32 v132, v132
	v_cvt_pk_bf16_f32 v144, v140, v141
	v_mul_f32_e32 v140, 0x3fb8aa3b, v142
	v_mul_f32_e32 v141, 0x3fb8aa3b, v143
	v_exp_f32_e32 v140, v140
	v_exp_f32_e32 v141, v141
	v_exp_f32_e32 v133, v133
	v_pk_mul_f32 v[142:143], v[14:15], s[34:35] op_sel_hi:[1,0]
	v_mul_f32_e32 v134, 0x3fb8aa3b, v134
	v_pk_mul_f32 v[140:141], v[142:143], v[140:141]
	v_exp_f32_e32 v190, v134
	v_cvt_pk_bf16_f32 v145, v140, v141
	v_pk_mul_f32 v[140:141], v[8:9], s[34:35] op_sel_hi:[1,0]
	s_mov_b32 s2, 0x3fb8aa3b
	v_pk_mul_f32 v[132:133], v[140:141], v[132:133]
	s_nop 0
	v_cvt_pk_bf16_f32 v146, v132, v133
	v_mul_f32_e32 v132, 0x3db504f3, v10
	v_mov_b32_e32 v133, v11
	v_pk_mul_f32 v[150:151], v[132:133], v[190:191]
.LBB0_417:
	s_waitcnt vmcnt(3)
	v_mul_f32_e32 v132, s2, v135
	v_exp_f32_e32 v134, v132
	v_or_b32_e32 v132, 0x1800, v193
	v_lshlrev_b32_e32 v168, 1, v132
	v_lshl_add_u64 v[132:133], v[152:153], 0, v[168:169]
	v_mul_f32_e32 v134, v151, v134
	v_mov_b32_e32 v149, v169
	v_cvt_pk_bf16_f32 v147, v150, v134
	v_lshl_add_u64 v[132:133], v[132:133], 0, v[148:149]
	s_and_b64 vcc, exec, s[8:9]
	s_mov_b64 s[2:3], -1
	global_store_dwordx4 v[132:133], v[144:147], off nt
	s_waitcnt vmcnt(1)
	s_cbranch_vccnz .LBB0_419
	v_mul_f32_e32 v132, 0xbfb8aa3b, v136
	v_mul_f32_e32 v133, 0xbfb8aa3b, v137
	v_exp_f32_e32 v132, v132
	v_exp_f32_e32 v133, v133
	v_mul_f32_e32 v134, 0xbfb8aa3b, v138
	v_mul_f32_e32 v135, 0xbfb8aa3b, v139
	v_exp_f32_e32 v134, v134
	v_pk_mul_f32 v[132:133], v[4:5], v[132:133]
	v_exp_f32_e32 v135, v135
	v_cvt_pk_bf16_f32 v132, v132, v133
	v_mul_f32_e32 v133, 0xbfb8aa3b, v128
	v_exp_f32_e32 v140, v133
	v_mul_f32_e32 v133, 0xbfb8aa3b, v129
	v_exp_f32_e32 v141, v133
	v_mul_f32_e32 v133, 0xbfb8aa3b, v130
	v_exp_f32_e32 v142, v133
	v_pk_mul_f32 v[134:135], v[6:7], v[134:135]
	s_mov_b64 s[2:3], 0
	v_cvt_pk_bf16_f32 v133, v134, v135
	v_pk_mul_f32 v[134:135], v[0:1], v[140:141]
	v_mul_f32_e32 v140, v2, v142
	v_cvt_pk_bf16_f32 v134, v134, v135
	v_mov_b32_e32 v141, v3

; #define ROPE_LOAD(buf, g) do { const int _pos = (row0 + ((g) >> 2) * HALF + ((g) & 3) * 16) & (SEQ - 1); const float* _rp = rope + _pos * 32 + 8 * (fq & 1); \
;                 rc[buf][0] = *(const f32x4*)_rp; rc[buf][1] = *(const f32x4*)(_rp + 4); rc[buf][2] = *(const f32x4*)(_rp + 16); rc[buf][3] = *(const f32x4*)(_rp + 20); } while (0)
;     __device__ __forceinline__ void operator()(const f32x4 (&acc)[2][2][4][2], const Unit& u, int wr, int wc, int fr, int fq) const {
;     ...
;                 if (wc == 0 && g + 1 < 8) ROPE_LOAD((g + 1) & 1, g + 1);
; #pragma unroll
;                 for (int bj = 0; bj < 2; ++bj) {
;                     float v[8] = {acc[ai][bj][m][0][0], acc[ai][bj][m][0][1], acc[ai][bj][m][0][2], acc[ai][bj][m][0][3],
;                                   acc[ai][bj][m][1][0], acc[ai][bj][m][1][1], acc[ai][bj][m][1][2], acc[ai][bj][m][1][3]};
;                     if (wc == 0) {
;                         const f32x4 c0 = rc[g & 1][0], c1 = rc[g & 1][1], s0 = rc[g & 1][2], s1 = rc[g & 1][3];
;                         const float cs[8] = {c0[0], c0[1], c0[2], c0[3], c1[0], c1[1], c1[2], c1[3]}, sn[8] = {s0[0], s0[1], s0[2], s0[3], s1[0], s1[1], s1[2], s1[3]};
; #pragma unroll
;                         for (int i = 0; i < 8; ++i) {
;                             const float pv = __shfl_xor(v[i], 32);
;                             v[i] = (fq < 2) ? (v[i] * cs[i] - pv * sn[i]) : (v[i] * cs[i] + pv * sn[i]);
;                         }
;                     }
.LBB0_438:
	v_and_b32_e32 v190, 64, v211
	v_xor_b32_e32 v168, 32, v211
	v_add_u32_e32 v190, 64, v190
	v_cmp_lt_i32_e32 vcc, v168, v190
	s_nop 1
	v_cndmask_b32_e32 v168, v211, v168, vcc
	v_lshlrev_b32_e32 v168, 2, v168
	ds_bpermute_b32 v194, v168, v124
	ds_bpermute_b32 v195, v168, v125
	ds_bpermute_b32 v196, v168, v126
	ds_bpermute_b32 v197, v168, v127
	ds_bpermute_b32 v198, v168, v120
	ds_bpermute_b32 v199, v168, v121
	ds_bpermute_b32 v200, v168, v122
	ds_bpermute_b32 v201, v168, v123
	s_waitcnt vmcnt(4) lgkmcnt(0)
	v_pk_mul_f32 v[194:195], v[156:157], v[194:195]
	v_pk_mul_f32 v[196:197], v[158:159], v[196:197]
	v_pk_mul_f32 v[198:199], v[152:153], v[198:199]
	v_cndmask_b32_e64 v195, v195, -v195, s[0:1]
	v_pk_mul_f32 v[200:201], v[154:155], v[200:201]
	v_cndmask_b32_e64 v194, v194, -v194, s[0:1]
	v_cndmask_b32_e64 v197, v197, -v197, s[0:1]
	v_cndmask_b32_e64 v196, v196, -v196, s[0:1]
	v_cndmask_b32_e64 v199, v199, -v199, s[0:1]
	v_cndmask_b32_e64 v198, v198, -v198, s[0:1]
	v_cndmask_b32_e64 v201, v201, -v201, s[0:1]
	v_cndmask_b32_e64 v200, v200, -v200, s[0:1]
	v_pk_fma_f32 v[122:123], v[122:123], v[150:151], v[200:201]
	v_pk_fma_f32 v[120:121], v[120:121], v[148:149], v[198:199]
	v_pk_fma_f32 v[126:127], v[126:127], v[146:147], v[196:197]
	v_pk_fma_f32 v[124:125], v[124:125], v[144:145], v[194:195]
	s_branch .LBB0_429
.LBB0_439:
	v_and_b32_e32 v121, 64, v211
	v_xor_b32_e32 v120, 32, v211
	v_add_u32_e32 v121, 64, v121
	v_cmp_lt_i32_e32 vcc, v120, v121
	s_nop 1
	v_cndmask_b32_e32 v120, v211, v120, vcc
	v_lshlrev_b32_e32 v127, 2, v120
	ds_bpermute_b32 v120, v127, v116
	ds_bpermute_b32 v121, v127, v117
	ds_bpermute_b32 v122, v127, v118
	ds_bpermute_b32 v123, v127, v119
	ds_bpermute_b32 v124, v127, v112
	ds_bpermute_b32 v125, v127, v113
	ds_bpermute_b32 v126, v127, v114
	ds_bpermute_b32 v127, v127, v115
	s_waitcnt lgkmcnt(0)
	v_pk_mul_f32 v[120:121], v[156:157], v[120:121]
	v_pk_mul_f32 v[122:123], v[158:159], v[122:123]
	v_pk_mul_f32 v[124:125], v[152:153], v[124:125]
	v_cndmask_b32_e64 v121, v121, -v121, s[0:1]
	v_pk_mul_f32 v[126:127], v[154:155], v[126:127]
	v_cndmask_b32_e64 v120, v120, -v120, s[0:1]
	v_cndmask_b32_e64 v123, v123, -v123, s[0:1]
	v_cndmask_b32_e64 v122, v122, -v122, s[0:1]
	v_cndmask_b32_e64 v125, v125, -v125, s[0:1]
	v_cndmask_b32_e64 v124, v124, -v124, s[0:1]
	v_cndmask_b32_e64 v127, v127, -v127, s[0:1]
	v_cndmask_b32_e64 v126, v126, -v126, s[0:1]
	v_pk_fma_f32 v[114:115], v[114:115], v[150:151], v[126:127]
	v_pk_fma_f32 v[112:113], v[112:113], v[148:149], v[124:125]
	v_pk_fma_f32 v[118:119], v[118:119], v[146:147], v[122:123]
	v_pk_fma_f32 v[116:117], v[116:117], v[144:145], v[120:121]
	s_and_b64 vcc, exec, s[54:55]
	s_cbranch_vccnz .LBB0_435

; #define ROPE_LOAD(buf, g) do { const int _pos = (row0 + ((g) >> 2) * HALF + ((g) & 3) * 16) & (SEQ - 1); const float* _rp = rope + _pos * 32 + 8 * (fq & 1); \
;                 rc[buf][0] = *(const f32x4*)_rp; rc[buf][1] = *(const f32x4*)(_rp + 4); rc[buf][2] = *(const f32x4*)(_rp + 16); rc[buf][3] = *(const f32x4*)(_rp + 20); } while (0)
;     __device__ __forceinline__ void operator()(const f32x4 (&acc)[2][2][4][2], const Unit& u, int wr, int wc, int fr, int fq) const {
;     ...
;                 if (wc == 0 && g + 1 < 8) ROPE_LOAD((g + 1) & 1, g + 1);
; #pragma unroll
;                 for (int bj = 0; bj < 2; ++bj) {
;                     float v[8] = {acc[ai][bj][m][0][0], acc[ai][bj][m][0][1], acc[ai][bj][m][0][2], acc[ai][bj][m][0][3],
;                                   acc[ai][bj][m][1][0], acc[ai][bj][m][1][1], acc[ai][bj][m][1][2], acc[ai][bj][m][1][3]};
;                     if (wc == 0) {
;                         const f32x4 c0 = rc[g & 1][0], c1 = rc[g & 1][1], s0 = rc[g & 1][2], s1 = rc[g & 1][3];
;                         const float cs[8] = {c0[0], c0[1], c0[2], c0[3], c1[0], c1[1], c1[2], c1[3]}, sn[8] = {s0[0], s0[1], s0[2], s0[3], s1[0], s1[1], s1[2], s1[3]};
; #pragma unroll
;                         for (int i = 0; i < 8; ++i) {
;                             const float pv = __shfl_xor(v[i], 32);
;                             v[i] = (fq < 2) ? (v[i] * cs[i] - pv * sn[i]) : (v[i] * cs[i] + pv * sn[i]);
;                         }
;                     }
.LBB0_447:
	v_and_b32_e32 v113, 64, v211
	v_xor_b32_e32 v112, 32, v211
	v_add_u32_e32 v113, 64, v113
	v_cmp_lt_i32_e32 vcc, v112, v113
	s_nop 1
	v_cndmask_b32_e32 v112, v211, v112, vcc
	v_lshlrev_b32_e32 v119, 2, v112
	ds_bpermute_b32 v112, v119, v108
	ds_bpermute_b32 v113, v119, v109
	ds_bpermute_b32 v114, v119, v110
	ds_bpermute_b32 v115, v119, v111
	ds_bpermute_b32 v116, v119, v104
	ds_bpermute_b32 v117, v119, v105
	ds_bpermute_b32 v118, v119, v106
	ds_bpermute_b32 v119, v119, v107
	s_waitcnt vmcnt(6) lgkmcnt(0)
	v_pk_mul_f32 v[112:113], v[140:141], v[112:113]
	v_pk_mul_f32 v[114:115], v[142:143], v[114:115]
	v_pk_mul_f32 v[116:117], v[136:137], v[116:117]
	v_cndmask_b32_e64 v113, v113, -v113, s[0:1]
	v_pk_mul_f32 v[118:119], v[138:139], v[118:119]
	v_cndmask_b32_e64 v112, v112, -v112, s[0:1]
	v_cndmask_b32_e64 v115, v115, -v115, s[0:1]
	v_cndmask_b32_e64 v114, v114, -v114, s[0:1]
	v_cndmask_b32_e64 v117, v117, -v117, s[0:1]
	v_cndmask_b32_e64 v116, v116, -v116, s[0:1]
	v_cndmask_b32_e64 v119, v119, -v119, s[0:1]
	v_cndmask_b32_e64 v118, v118, -v118, s[0:1]
	v_pk_fma_f32 v[106:107], v[106:107], v[134:135], v[118:119]
	v_pk_fma_f32 v[104:105], v[104:105], v[132:133], v[116:117]
	v_pk_fma_f32 v[110:111], v[110:111], v[130:131], v[114:115]
	v_pk_fma_f32 v[108:109], v[108:109], v[128:129], v[112:113]
	s_and_b64 vcc, exec, s[54:55]
	s_cbranch_vccnz .LBB0_445

; #define ROPE_LOAD(buf, g) do { const int _pos = (row0 + ((g) >> 2) * HALF + ((g) & 3) * 16) & (SEQ - 1); const float* _rp = rope + _pos * 32 + 8 * (fq & 1); \
;                 rc[buf][0] = *(const f32x4*)_rp; rc[buf][1] = *(const f32x4*)(_rp + 4); rc[buf][2] = *(const f32x4*)(_rp + 16); rc[buf][3] = *(const f32x4*)(_rp + 20); } while (0)
;     __device__ __forceinline__ void operator()(const f32x4 (&acc)[2][2][4][2], const Unit& u, int wr, int wc, int fr, int fq) const {
;     ...
;                 if (wc == 0 && g + 1 < 8) ROPE_LOAD((g + 1) & 1, g + 1);
; #pragma unroll
;                 for (int bj = 0; bj < 2; ++bj) {
;                     float v[8] = {acc[ai][bj][m][0][0], acc[ai][bj][m][0][1], acc[ai][bj][m][0][2], acc[ai][bj][m][0][3],
;                                   acc[ai][bj][m][1][0], acc[ai][bj][m][1][1], acc[ai][bj][m][1][2], acc[ai][bj][m][1][3]};
;                     if (wc == 0) {
;                         const f32x4 c0 = rc[g & 1][0], c1 = rc[g & 1][1], s0 = rc[g & 1][2], s1 = rc[g & 1][3];
;                         const float cs[8] = {c0[0], c0[1], c0[2], c0[3], c1[0], c1[1], c1[2], c1[3]}, sn[8] = {s0[0], s0[1], s0[2], s0[3], s1[0], s1[1], s1[2], s1[3]};
; #pragma unroll
;                         for (int i = 0; i < 8; ++i) {
;                             const float pv = __shfl_xor(v[i], 32);
;                             v[i] = (fq < 2) ? (v[i] * cs[i] - pv * sn[i]) : (v[i] * cs[i] + pv * sn[i]);
;                         }
;                     }
.LBB0_453:
	v_and_b32_e32 v105, 64, v211
	v_xor_b32_e32 v104, 32, v211
	v_add_u32_e32 v105, 64, v105
	v_cmp_lt_i32_e32 vcc, v104, v105
	s_nop 1
	v_cndmask_b32_e32 v104, v211, v104, vcc
	v_lshlrev_b32_e32 v111, 2, v104
	ds_bpermute_b32 v104, v111, v100
	ds_bpermute_b32 v105, v111, v101
	ds_bpermute_b32 v106, v111, v102
	ds_bpermute_b32 v107, v111, v103
	ds_bpermute_b32 v108, v111, v96
	ds_bpermute_b32 v109, v111, v97
	ds_bpermute_b32 v110, v111, v98
	ds_bpermute_b32 v111, v111, v99
	s_waitcnt lgkmcnt(0)
	v_pk_mul_f32 v[104:105], v[140:141], v[104:105]
	v_pk_mul_f32 v[106:107], v[142:143], v[106:107]
	v_pk_mul_f32 v[108:109], v[136:137], v[108:109]
	v_cndmask_b32_e64 v105, v105, -v105, s[0:1]
	v_pk_mul_f32 v[110:111], v[138:139], v[110:111]
	v_cndmask_b32_e64 v104, v104, -v104, s[0:1]
	v_cndmask_b32_e64 v107, v107, -v107, s[0:1]
	v_cndmask_b32_e64 v106, v106, -v106, s[0:1]
	v_cndmask_b32_e64 v109, v109, -v109, s[0:1]
	v_cndmask_b32_e64 v108, v108, -v108, s[0:1]
	v_cndmask_b32_e64 v111, v111, -v111, s[0:1]
	v_cndmask_b32_e64 v110, v110, -v110, s[0:1]
	v_pk_fma_f32 v[98:99], v[98:99], v[134:135], v[110:111]
	v_pk_fma_f32 v[96:97], v[96:97], v[132:133], v[108:109]
	v_pk_fma_f32 v[102:103], v[102:103], v[130:131], v[106:107]
	v_pk_fma_f32 v[100:101], v[100:101], v[128:129], v[104:105]
	s_and_b64 vcc, exec, s[54:55]
	s_cbranch_vccnz .LBB0_452

; #define ROPE_LOAD(buf, g) do { const int _pos = (row0 + ((g) >> 2) * HALF + ((g) & 3) * 16) & (SEQ - 1); const float* _rp = rope + _pos * 32 + 8 * (fq & 1); \
;                 rc[buf][0] = *(const f32x4*)_rp; rc[buf][1] = *(const f32x4*)(_rp + 4); rc[buf][2] = *(const f32x4*)(_rp + 16); rc[buf][3] = *(const f32x4*)(_rp + 20); } while (0)
;     __device__ __forceinline__ void operator()(const f32x4 (&acc)[2][2][4][2], const Unit& u, int wr, int wc, int fr, int fq) const {
;     ...
;                 if (wc == 0 && g + 1 < 8) ROPE_LOAD((g + 1) & 1, g + 1);
; #pragma unroll
;                 for (int bj = 0; bj < 2; ++bj) {
;                     float v[8] = {acc[ai][bj][m][0][0], acc[ai][bj][m][0][1], acc[ai][bj][m][0][2], acc[ai][bj][m][0][3],
;                                   acc[ai][bj][m][1][0], acc[ai][bj][m][1][1], acc[ai][bj][m][1][2], acc[ai][bj][m][1][3]};
;                     if (wc == 0) {
;                         const f32x4 c0 = rc[g & 1][0], c1 = rc[g & 1][1], s0 = rc[g & 1][2], s1 = rc[g & 1][3];
;                         const float cs[8] = {c0[0], c0[1], c0[2], c0[3], c1[0], c1[1], c1[2], c1[3]}, sn[8] = {s0[0], s0[1], s0[2], s0[3], s1[0], s1[1], s1[2], s1[3]};
; #pragma unroll
;                         for (int i = 0; i < 8; ++i) {
;                             const float pv = __shfl_xor(v[i], 32);
;                             v[i] = (fq < 2) ? (v[i] * cs[i] - pv * sn[i]) : (v[i] * cs[i] + pv * sn[i]);
;                         }
;                     }
.LBB0_461:
	v_and_b32_e32 v97, 64, v211
	v_xor_b32_e32 v96, 32, v211
	v_add_u32_e32 v97, 64, v97
	v_cmp_lt_i32_e32 vcc, v96, v97
	s_nop 1
	v_cndmask_b32_e32 v96, v211, v96, vcc
	v_lshlrev_b32_e32 v103, 2, v96
	ds_bpermute_b32 v96, v103, v92
	ds_bpermute_b32 v97, v103, v93
	ds_bpermute_b32 v98, v103, v94
	ds_bpermute_b32 v99, v103, v95
	ds_bpermute_b32 v100, v103, v88
	ds_bpermute_b32 v101, v103, v89
	ds_bpermute_b32 v102, v103, v90
	ds_bpermute_b32 v103, v103, v91
	s_waitcnt vmcnt(6) lgkmcnt(0)
	v_pk_mul_f32 v[96:97], v[156:157], v[96:97]
	v_pk_mul_f32 v[98:99], v[158:159], v[98:99]
	v_pk_mul_f32 v[100:101], v[152:153], v[100:101]
	v_cndmask_b32_e64 v97, v97, -v97, s[0:1]
	v_pk_mul_f32 v[102:103], v[154:155], v[102:103]
	v_cndmask_b32_e64 v96, v96, -v96, s[0:1]
	v_cndmask_b32_e64 v99, v99, -v99, s[0:1]
	v_cndmask_b32_e64 v98, v98, -v98, s[0:1]
	v_cndmask_b32_e64 v101, v101, -v101, s[0:1]
	v_cndmask_b32_e64 v100, v100, -v100, s[0:1]
	v_cndmask_b32_e64 v103, v103, -v103, s[0:1]
	v_cndmask_b32_e64 v102, v102, -v102, s[0:1]
	v_pk_fma_f32 v[90:91], v[90:91], v[150:151], v[102:103]
	v_pk_fma_f32 v[88:89], v[88:89], v[148:149], v[100:101]
	v_pk_fma_f32 v[94:95], v[94:95], v[146:147], v[98:99]
	v_pk_fma_f32 v[92:93], v[92:93], v[144:145], v[96:97]
	s_and_b64 vcc, exec, s[54:55]
	s_cbranch_vccnz .LBB0_459

; #define ROPE_LOAD(buf, g) do { const int _pos = (row0 + ((g) >> 2) * HALF + ((g) & 3) * 16) & (SEQ - 1); const float* _rp = rope + _pos * 32 + 8 * (fq & 1); \
;                 rc[buf][0] = *(const f32x4*)_rp; rc[buf][1] = *(const f32x4*)(_rp + 4); rc[buf][2] = *(const f32x4*)(_rp + 16); rc[buf][3] = *(const f32x4*)(_rp + 20); } while (0)
;     __device__ __forceinline__ void operator()(const f32x4 (&acc)[2][2][4][2], const Unit& u, int wr, int wc, int fr, int fq) const {
;     ...
;                 if (wc == 0 && g + 1 < 8) ROPE_LOAD((g + 1) & 1, g + 1);
; #pragma unroll
;                 for (int bj = 0; bj < 2; ++bj) {
;                     float v[8] = {acc[ai][bj][m][0][0], acc[ai][bj][m][0][1], acc[ai][bj][m][0][2], acc[ai][bj][m][0][3],
;                                   acc[ai][bj][m][1][0], acc[ai][bj][m][1][1], acc[ai][bj][m][1][2], acc[ai][bj][m][1][3]};
;                     if (wc == 0) {
;                         const f32x4 c0 = rc[g & 1][0], c1 = rc[g & 1][1], s0 = rc[g & 1][2], s1 = rc[g & 1][3];
;                         const float cs[8] = {c0[0], c0[1], c0[2], c0[3], c1[0], c1[1], c1[2], c1[3]}, sn[8] = {s0[0], s0[1], s0[2], s0[3], s1[0], s1[1], s1[2], s1[3]};
; #pragma unroll
;                         for (int i = 0; i < 8; ++i) {
;                             const float pv = __shfl_xor(v[i], 32);
;                             v[i] = (fq < 2) ? (v[i] * cs[i] - pv * sn[i]) : (v[i] * cs[i] + pv * sn[i]);
;                         }
;                     }
.LBB0_467:
	v_and_b32_e32 v89, 64, v211
	v_xor_b32_e32 v88, 32, v211
	v_add_u32_e32 v89, 64, v89
	v_cmp_lt_i32_e32 vcc, v88, v89
	s_nop 1
	v_cndmask_b32_e32 v88, v211, v88, vcc
	v_lshlrev_b32_e32 v95, 2, v88
	ds_bpermute_b32 v88, v95, v84
	ds_bpermute_b32 v89, v95, v85
	ds_bpermute_b32 v90, v95, v86
	ds_bpermute_b32 v91, v95, v87
	ds_bpermute_b32 v92, v95, v80
	ds_bpermute_b32 v93, v95, v81
	ds_bpermute_b32 v94, v95, v82
	ds_bpermute_b32 v95, v95, v83
	s_waitcnt lgkmcnt(0)
	v_pk_mul_f32 v[88:89], v[156:157], v[88:89]
	v_pk_mul_f32 v[90:91], v[158:159], v[90:91]
	v_pk_mul_f32 v[92:93], v[152:153], v[92:93]
	v_cndmask_b32_e64 v89, v89, -v89, s[0:1]
	v_pk_mul_f32 v[94:95], v[154:155], v[94:95]
	v_cndmask_b32_e64 v88, v88, -v88, s[0:1]
	v_cndmask_b32_e64 v91, v91, -v91, s[0:1]
	v_cndmask_b32_e64 v90, v90, -v90, s[0:1]
	v_cndmask_b32_e64 v93, v93, -v93, s[0:1]
	v_cndmask_b32_e64 v92, v92, -v92, s[0:1]
	v_cndmask_b32_e64 v95, v95, -v95, s[0:1]
	v_cndmask_b32_e64 v94, v94, -v94, s[0:1]
	v_pk_fma_f32 v[82:83], v[82:83], v[150:151], v[94:95]
	v_pk_fma_f32 v[80:81], v[80:81], v[148:149], v[92:93]
	v_pk_fma_f32 v[86:87], v[86:87], v[146:147], v[90:91]
	v_pk_fma_f32 v[84:85], v[84:85], v[144:145], v[88:89]
	s_and_b64 vcc, exec, s[54:55]
	s_cbranch_vccnz .LBB0_466

; #define ROPE_LOAD(buf, g) do { const int _pos = (row0 + ((g) >> 2) * HALF + ((g) & 3) * 16) & (SEQ - 1); const float* _rp = rope + _pos * 32 + 8 * (fq & 1); \
;                 rc[buf][0] = *(const f32x4*)_rp; rc[buf][1] = *(const f32x4*)(_rp + 4); rc[buf][2] = *(const f32x4*)(_rp + 16); rc[buf][3] = *(const f32x4*)(_rp + 20); } while (0)
;     __device__ __forceinline__ void operator()(const f32x4 (&acc)[2][2][4][2], const Unit& u, int wr, int wc, int fr, int fq) const {
;     ...
;                 if (wc == 0 && g + 1 < 8) ROPE_LOAD((g + 1) & 1, g + 1);
; #pragma unroll
;                 for (int bj = 0; bj < 2; ++bj) {
;                     float v[8] = {acc[ai][bj][m][0][0], acc[ai][bj][m][0][1], acc[ai][bj][m][0][2], acc[ai][bj][m][0][3],
;                                   acc[ai][bj][m][1][0], acc[ai][bj][m][1][1], acc[ai][bj][m][1][2], acc[ai][bj][m][1][3]};
;                     if (wc == 0) {
;                         const f32x4 c0 = rc[g & 1][0], c1 = rc[g & 1][1], s0 = rc[g & 1][2], s1 = rc[g & 1][3];
;                         const float cs[8] = {c0[0], c0[1], c0[2], c0[3], c1[0], c1[1], c1[2], c1[3]}, sn[8] = {s0[0], s0[1], s0[2], s0[3], s1[0], s1[1], s1[2], s1[3]};
; #pragma unroll
;                         for (int i = 0; i < 8; ++i) {
;                             const float pv = __shfl_xor(v[i], 32);
;                             v[i] = (fq < 2) ? (v[i] * cs[i] - pv * sn[i]) : (v[i] * cs[i] + pv * sn[i]);
;                         }
;                     }
.LBB0_475:
	v_and_b32_e32 v81, 64, v211
	v_xor_b32_e32 v80, 32, v211
	v_add_u32_e32 v81, 64, v81
	v_cmp_lt_i32_e32 vcc, v80, v81
	s_nop 1
	v_cndmask_b32_e32 v80, v211, v80, vcc
	v_lshlrev_b32_e32 v87, 2, v80
	ds_bpermute_b32 v80, v87, v76
	ds_bpermute_b32 v81, v87, v77
	ds_bpermute_b32 v82, v87, v78
	ds_bpermute_b32 v83, v87, v79
	ds_bpermute_b32 v84, v87, v72
	ds_bpermute_b32 v85, v87, v73
	ds_bpermute_b32 v86, v87, v74
	ds_bpermute_b32 v87, v87, v75
	s_waitcnt vmcnt(6) lgkmcnt(0)
	v_pk_mul_f32 v[80:81], v[140:141], v[80:81]
	v_pk_mul_f32 v[82:83], v[142:143], v[82:83]
	v_pk_mul_f32 v[84:85], v[136:137], v[84:85]
	v_cndmask_b32_e64 v81, v81, -v81, s[0:1]
	v_pk_mul_f32 v[86:87], v[138:139], v[86:87]
	v_cndmask_b32_e64 v80, v80, -v80, s[0:1]
	v_cndmask_b32_e64 v83, v83, -v83, s[0:1]
	v_cndmask_b32_e64 v82, v82, -v82, s[0:1]
	v_cndmask_b32_e64 v85, v85, -v85, s[0:1]
	v_cndmask_b32_e64 v84, v84, -v84, s[0:1]
	v_cndmask_b32_e64 v87, v87, -v87, s[0:1]
	v_cndmask_b32_e64 v86, v86, -v86, s[0:1]
	v_pk_fma_f32 v[74:75], v[74:75], v[134:135], v[86:87]
	v_pk_fma_f32 v[72:73], v[72:73], v[132:133], v[84:85]
	v_pk_fma_f32 v[78:79], v[78:79], v[130:131], v[82:83]
	v_pk_fma_f32 v[76:77], v[76:77], v[128:129], v[80:81]
	s_and_b64 vcc, exec, s[54:55]
	s_cbranch_vccnz .LBB0_473

; #define ROPE_LOAD(buf, g) do { const int _pos = (row0 + ((g) >> 2) * HALF + ((g) & 3) * 16) & (SEQ - 1); const float* _rp = rope + _pos * 32 + 8 * (fq & 1); \
;                 rc[buf][0] = *(const f32x4*)_rp; rc[buf][1] = *(const f32x4*)(_rp + 4); rc[buf][2] = *(const f32x4*)(_rp + 16); rc[buf][3] = *(const f32x4*)(_rp + 20); } while (0)
;     __device__ __forceinline__ void operator()(const f32x4 (&acc)[2][2][4][2], const Unit& u, int wr, int wc, int fr, int fq) const {
;     ...
;                 if (wc == 0 && g + 1 < 8) ROPE_LOAD((g + 1) & 1, g + 1);
; #pragma unroll
;                 for (int bj = 0; bj < 2; ++bj) {
;                     float v[8] = {acc[ai][bj][m][0][0], acc[ai][bj][m][0][1], acc[ai][bj][m][0][2], acc[ai][bj][m][0][3],
;                                   acc[ai][bj][m][1][0], acc[ai][bj][m][1][1], acc[ai][bj][m][1][2], acc[ai][bj][m][1][3]};
;                     if (wc == 0) {
;                         const f32x4 c0 = rc[g & 1][0], c1 = rc[g & 1][1], s0 = rc[g & 1][2], s1 = rc[g & 1][3];
;                         const float cs[8] = {c0[0], c0[1], c0[2], c0[3], c1[0], c1[1], c1[2], c1[3]}, sn[8] = {s0[0], s0[1], s0[2], s0[3], s1[0], s1[1], s1[2], s1[3]};
; #pragma unroll
;                         for (int i = 0; i < 8; ++i) {
;                             const float pv = __shfl_xor(v[i], 32);
;                             v[i] = (fq < 2) ? (v[i] * cs[i] - pv * sn[i]) : (v[i] * cs[i] + pv * sn[i]);
;                         }
;                     }
.LBB0_481:
	v_and_b32_e32 v73, 64, v211
	v_xor_b32_e32 v72, 32, v211
	v_add_u32_e32 v73, 64, v73
	v_cmp_lt_i32_e32 vcc, v72, v73
	s_nop 1
	v_cndmask_b32_e32 v72, v211, v72, vcc
	v_lshlrev_b32_e32 v79, 2, v72
	ds_bpermute_b32 v72, v79, v68
	ds_bpermute_b32 v73, v79, v69
	ds_bpermute_b32 v74, v79, v70
	ds_bpermute_b32 v75, v79, v71
	ds_bpermute_b32 v76, v79, v64
	ds_bpermute_b32 v77, v79, v65
	ds_bpermute_b32 v78, v79, v66
	ds_bpermute_b32 v79, v79, v67
	s_waitcnt lgkmcnt(0)
	v_pk_mul_f32 v[72:73], v[140:141], v[72:73]
	v_pk_mul_f32 v[74:75], v[142:143], v[74:75]
	v_pk_mul_f32 v[76:77], v[136:137], v[76:77]
	v_cndmask_b32_e64 v73, v73, -v73, s[0:1]
	v_pk_mul_f32 v[78:79], v[138:139], v[78:79]
	v_cndmask_b32_e64 v72, v72, -v72, s[0:1]
	v_cndmask_b32_e64 v75, v75, -v75, s[0:1]
	v_cndmask_b32_e64 v74, v74, -v74, s[0:1]
	v_cndmask_b32_e64 v77, v77, -v77, s[0:1]
	v_cndmask_b32_e64 v76, v76, -v76, s[0:1]
	v_cndmask_b32_e64 v79, v79, -v79, s[0:1]
	v_cndmask_b32_e64 v78, v78, -v78, s[0:1]
	v_pk_fma_f32 v[66:67], v[66:67], v[134:135], v[78:79]
	v_pk_fma_f32 v[64:65], v[64:65], v[132:133], v[76:77]
	v_pk_fma_f32 v[70:71], v[70:71], v[130:131], v[74:75]
	v_pk_fma_f32 v[68:69], v[68:69], v[128:129], v[72:73]
	s_and_b64 vcc, exec, s[54:55]
	s_cbranch_vccnz .LBB0_480

; #define ROPE_LOAD(buf, g) do { const int _pos = (row0 + ((g) >> 2) * HALF + ((g) & 3) * 16) & (SEQ - 1); const float* _rp = rope + _pos * 32 + 8 * (fq & 1); \
;                 rc[buf][0] = *(const f32x4*)_rp; rc[buf][1] = *(const f32x4*)(_rp + 4); rc[buf][2] = *(const f32x4*)(_rp + 16); rc[buf][3] = *(const f32x4*)(_rp + 20); } while (0)
;     __device__ __forceinline__ void operator()(const f32x4 (&acc)[2][2][4][2], const Unit& u, int wr, int wc, int fr, int fq) const {
;     ...
;                 if (wc == 0 && g + 1 < 8) ROPE_LOAD((g + 1) & 1, g + 1);
; #pragma unroll
;                 for (int bj = 0; bj < 2; ++bj) {
;                     float v[8] = {acc[ai][bj][m][0][0], acc[ai][bj][m][0][1], acc[ai][bj][m][0][2], acc[ai][bj][m][0][3],
;                                   acc[ai][bj][m][1][0], acc[ai][bj][m][1][1], acc[ai][bj][m][1][2], acc[ai][bj][m][1][3]};
;                     if (wc == 0) {
;                         const f32x4 c0 = rc[g & 1][0], c1 = rc[g & 1][1], s0 = rc[g & 1][2], s1 = rc[g & 1][3];
;                         const float cs[8] = {c0[0], c0[1], c0[2], c0[3], c1[0], c1[1], c1[2], c1[3]}, sn[8] = {s0[0], s0[1], s0[2], s0[3], s1[0], s1[1], s1[2], s1[3]};
; #pragma unroll
;                         for (int i = 0; i < 8; ++i) {
;                             const float pv = __shfl_xor(v[i], 32);
;                             v[i] = (fq < 2) ? (v[i] * cs[i] - pv * sn[i]) : (v[i] * cs[i] + pv * sn[i]);
;                         }
;                     }
.LBB0_489:
	v_and_b32_e32 v65, 64, v211
	v_xor_b32_e32 v64, 32, v211
	v_add_u32_e32 v65, 64, v65
	v_cmp_lt_i32_e32 vcc, v64, v65
	s_nop 1
	v_cndmask_b32_e32 v64, v211, v64, vcc
	v_lshlrev_b32_e32 v71, 2, v64
	ds_bpermute_b32 v64, v71, v60
	ds_bpermute_b32 v65, v71, v61
	ds_bpermute_b32 v66, v71, v62
	ds_bpermute_b32 v67, v71, v63
	ds_bpermute_b32 v68, v71, v56
	ds_bpermute_b32 v69, v71, v57
	ds_bpermute_b32 v70, v71, v58
	ds_bpermute_b32 v71, v71, v59
	s_waitcnt vmcnt(6) lgkmcnt(0)
	v_pk_mul_f32 v[64:65], v[156:157], v[64:65]
	v_pk_mul_f32 v[66:67], v[158:159], v[66:67]
	v_pk_mul_f32 v[68:69], v[152:153], v[68:69]
	v_cndmask_b32_e64 v65, v65, -v65, s[0:1]
	v_pk_mul_f32 v[70:71], v[154:155], v[70:71]
	v_cndmask_b32_e64 v64, v64, -v64, s[0:1]
	v_cndmask_b32_e64 v67, v67, -v67, s[0:1]
	v_cndmask_b32_e64 v66, v66, -v66, s[0:1]
	v_cndmask_b32_e64 v69, v69, -v69, s[0:1]
	v_cndmask_b32_e64 v68, v68, -v68, s[0:1]
	v_cndmask_b32_e64 v71, v71, -v71, s[0:1]
	v_cndmask_b32_e64 v70, v70, -v70, s[0:1]
	v_pk_fma_f32 v[58:59], v[58:59], v[150:151], v[70:71]
	v_pk_fma_f32 v[56:57], v[56:57], v[148:149], v[68:69]
	v_pk_fma_f32 v[62:63], v[62:63], v[146:147], v[66:67]
	v_pk_fma_f32 v[60:61], v[60:61], v[144:145], v[64:65]
	s_and_b64 vcc, exec, s[54:55]
	s_cbranch_vccnz .LBB0_487

; #define ROPE_LOAD(buf, g) do { const int _pos = (row0 + ((g) >> 2) * HALF + ((g) & 3) * 16) & (SEQ - 1); const float* _rp = rope + _pos * 32 + 8 * (fq & 1); \
;                 rc[buf][0] = *(const f32x4*)_rp; rc[buf][1] = *(const f32x4*)(_rp + 4); rc[buf][2] = *(const f32x4*)(_rp + 16); rc[buf][3] = *(const f32x4*)(_rp + 20); } while (0)
;     __device__ __forceinline__ void operator()(const f32x4 (&acc)[2][2][4][2], const Unit& u, int wr, int wc, int fr, int fq) const {
;     ...
;                 if (wc == 0 && g + 1 < 8) ROPE_LOAD((g + 1) & 1, g + 1);
; #pragma unroll
;                 for (int bj = 0; bj < 2; ++bj) {
;                     float v[8] = {acc[ai][bj][m][0][0], acc[ai][bj][m][0][1], acc[ai][bj][m][0][2], acc[ai][bj][m][0][3],
;                                   acc[ai][bj][m][1][0], acc[ai][bj][m][1][1], acc[ai][bj][m][1][2], acc[ai][bj][m][1][3]};
;                     if (wc == 0) {
;                         const f32x4 c0 = rc[g & 1][0], c1 = rc[g & 1][1], s0 = rc[g & 1][2], s1 = rc[g & 1][3];
;                         const float cs[8] = {c0[0], c0[1], c0[2], c0[3], c1[0], c1[1], c1[2], c1[3]}, sn[8] = {s0[0], s0[1], s0[2], s0[3], s1[0], s1[1], s1[2], s1[3]};
; #pragma unroll
;                         for (int i = 0; i < 8; ++i) {
;                             const float pv = __shfl_xor(v[i], 32);
;                             v[i] = (fq < 2) ? (v[i] * cs[i] - pv * sn[i]) : (v[i] * cs[i] + pv * sn[i]);
;                         }
;                     }
.LBB0_495:
	v_and_b32_e32 v59, 64, v211
	v_xor_b32_e32 v58, 32, v211
	v_add_u32_e32 v59, 64, v59
	v_cmp_lt_i32_e32 vcc, v58, v59
	s_nop 1
	v_cndmask_b32_e32 v58, v211, v58, vcc
	v_lshlrev_b32_e32 v79, 2, v58
	ds_bpermute_b32 v58, v79, v52
	ds_bpermute_b32 v59, v79, v53
	ds_bpermute_b32 v60, v79, v54
	ds_bpermute_b32 v61, v79, v55
	ds_bpermute_b32 v62, v79, v48
	ds_bpermute_b32 v63, v79, v49
	ds_bpermute_b32 v78, v79, v50
	ds_bpermute_b32 v79, v79, v51
	s_waitcnt lgkmcnt(0)
	v_pk_mul_f32 v[58:59], v[156:157], v[58:59]
	v_pk_mul_f32 v[60:61], v[158:159], v[60:61]
	v_pk_mul_f32 v[62:63], v[152:153], v[62:63]
	v_cndmask_b32_e64 v59, v59, -v59, s[0:1]
	v_pk_mul_f32 v[78:79], v[154:155], v[78:79]
	v_cndmask_b32_e64 v58, v58, -v58, s[0:1]
	v_cndmask_b32_e64 v61, v61, -v61, s[0:1]
	v_cndmask_b32_e64 v60, v60, -v60, s[0:1]
	v_cndmask_b32_e64 v63, v63, -v63, s[0:1]
	v_cndmask_b32_e64 v62, v62, -v62, s[0:1]
	v_cndmask_b32_e64 v79, v79, -v79, s[0:1]
	v_cndmask_b32_e64 v78, v78, -v78, s[0:1]
	v_pk_fma_f32 v[50:51], v[50:51], v[150:151], v[78:79]
	v_pk_fma_f32 v[48:49], v[48:49], v[148:149], v[62:63]
	v_pk_fma_f32 v[54:55], v[54:55], v[146:147], v[60:61]
	v_pk_fma_f32 v[52:53], v[52:53], v[144:145], v[58:59]
	s_and_b64 vcc, exec, s[54:55]
	s_cbranch_vccnz .LBB0_494

; #define ROPE_LOAD(buf, g) do { const int _pos = (row0 + ((g) >> 2) * HALF + ((g) & 3) * 16) & (SEQ - 1); const float* _rp = rope + _pos * 32 + 8 * (fq & 1); \
;                 rc[buf][0] = *(const f32x4*)_rp; rc[buf][1] = *(const f32x4*)(_rp + 4); rc[buf][2] = *(const f32x4*)(_rp + 16); rc[buf][3] = *(const f32x4*)(_rp + 20); } while (0)
;     __device__ __forceinline__ void operator()(const f32x4 (&acc)[2][2][4][2], const Unit& u, int wr, int wc, int fr, int fq) const {
;     ...
;                 if (wc == 0 && g + 1 < 8) ROPE_LOAD((g + 1) & 1, g + 1);
; #pragma unroll
;                 for (int bj = 0; bj < 2; ++bj) {
;                     float v[8] = {acc[ai][bj][m][0][0], acc[ai][bj][m][0][1], acc[ai][bj][m][0][2], acc[ai][bj][m][0][3],
;                                   acc[ai][bj][m][1][0], acc[ai][bj][m][1][1], acc[ai][bj][m][1][2], acc[ai][bj][m][1][3]};
;                     if (wc == 0) {
;                         const f32x4 c0 = rc[g & 1][0], c1 = rc[g & 1][1], s0 = rc[g & 1][2], s1 = rc[g & 1][3];
;                         const float cs[8] = {c0[0], c0[1], c0[2], c0[3], c1[0], c1[1], c1[2], c1[3]}, sn[8] = {s0[0], s0[1], s0[2], s0[3], s1[0], s1[1], s1[2], s1[3]};
; #pragma unroll
;                         for (int i = 0; i < 8; ++i) {
;                             const float pv = __shfl_xor(v[i], 32);
;                             v[i] = (fq < 2) ? (v[i] * cs[i] - pv * sn[i]) : (v[i] * cs[i] + pv * sn[i]);
;                         }
;                     }
.LBB0_503:
	v_and_b32_e32 v51, 64, v211
	v_xor_b32_e32 v50, 32, v211
	v_add_u32_e32 v51, 64, v51
	v_cmp_lt_i32_e32 vcc, v50, v51
	s_nop 1
	v_cndmask_b32_e32 v50, v211, v50, vcc
	v_lshlrev_b32_e32 v75, 2, v50
	ds_bpermute_b32 v50, v75, v44
	ds_bpermute_b32 v51, v75, v45
	ds_bpermute_b32 v52, v75, v46
	ds_bpermute_b32 v53, v75, v47
	ds_bpermute_b32 v54, v75, v40
	ds_bpermute_b32 v55, v75, v41
	ds_bpermute_b32 v74, v75, v42
	ds_bpermute_b32 v75, v75, v43
	s_waitcnt vmcnt(6) lgkmcnt(0)
	v_pk_mul_f32 v[50:51], v[140:141], v[50:51]
	v_pk_mul_f32 v[52:53], v[142:143], v[52:53]
	v_pk_mul_f32 v[54:55], v[136:137], v[54:55]
	v_cndmask_b32_e64 v51, v51, -v51, s[0:1]
	v_pk_mul_f32 v[74:75], v[138:139], v[74:75]
	v_cndmask_b32_e64 v50, v50, -v50, s[0:1]
	v_cndmask_b32_e64 v53, v53, -v53, s[0:1]
	v_cndmask_b32_e64 v52, v52, -v52, s[0:1]
	v_cndmask_b32_e64 v55, v55, -v55, s[0:1]
	v_cndmask_b32_e64 v54, v54, -v54, s[0:1]
	v_cndmask_b32_e64 v75, v75, -v75, s[0:1]
	v_cndmask_b32_e64 v74, v74, -v74, s[0:1]
	v_pk_fma_f32 v[42:43], v[42:43], v[134:135], v[74:75]
	v_pk_fma_f32 v[40:41], v[40:41], v[132:133], v[54:55]
	v_pk_fma_f32 v[46:47], v[46:47], v[130:131], v[52:53]
	v_pk_fma_f32 v[44:45], v[44:45], v[128:129], v[50:51]
	s_and_b64 vcc, exec, s[54:55]
	s_cbranch_vccnz .LBB0_501

; #define ROPE_LOAD(buf, g) do { const int _pos = (row0 + ((g) >> 2) * HALF + ((g) & 3) * 16) & (SEQ - 1); const float* _rp = rope + _pos * 32 + 8 * (fq & 1); \
;                 rc[buf][0] = *(const f32x4*)_rp; rc[buf][1] = *(const f32x4*)(_rp + 4); rc[buf][2] = *(const f32x4*)(_rp + 16); rc[buf][3] = *(const f32x4*)(_rp + 20); } while (0)
;     __device__ __forceinline__ void operator()(const f32x4 (&acc)[2][2][4][2], const Unit& u, int wr, int wc, int fr, int fq) const {
;     ...
;                 if (wc == 0 && g + 1 < 8) ROPE_LOAD((g + 1) & 1, g + 1);
; #pragma unroll
;                 for (int bj = 0; bj < 2; ++bj) {
;                     float v[8] = {acc[ai][bj][m][0][0], acc[ai][bj][m][0][1], acc[ai][bj][m][0][2], acc[ai][bj][m][0][3],
;                                   acc[ai][bj][m][1][0], acc[ai][bj][m][1][1], acc[ai][bj][m][1][2], acc[ai][bj][m][1][3]};
;                     if (wc == 0) {
;                         const f32x4 c0 = rc[g & 1][0], c1 = rc[g & 1][1], s0 = rc[g & 1][2], s1 = rc[g & 1][3];
;                         const float cs[8] = {c0[0], c0[1], c0[2], c0[3], c1[0], c1[1], c1[2], c1[3]}, sn[8] = {s0[0], s0[1], s0[2], s0[3], s1[0], s1[1], s1[2], s1[3]};
; #pragma unroll
;                         for (int i = 0; i < 8; ++i) {
;                             const float pv = __shfl_xor(v[i], 32);
;                             v[i] = (fq < 2) ? (v[i] * cs[i] - pv * sn[i]) : (v[i] * cs[i] + pv * sn[i]);
;                         }
;                     }
.LBB0_509:
	v_and_b32_e32 v41, 64, v211
	v_xor_b32_e32 v40, 32, v211
	v_add_u32_e32 v41, 64, v41
	v_cmp_lt_i32_e32 vcc, v40, v41
	s_nop 1
	v_cndmask_b32_e32 v40, v211, v40, vcc
	v_lshlrev_b32_e32 v47, 2, v40
	ds_bpermute_b32 v40, v47, v36
	ds_bpermute_b32 v41, v47, v37
	ds_bpermute_b32 v42, v47, v38
	ds_bpermute_b32 v43, v47, v39
	ds_bpermute_b32 v44, v47, v32
	ds_bpermute_b32 v45, v47, v33
	ds_bpermute_b32 v46, v47, v34
	ds_bpermute_b32 v47, v47, v35
	s_waitcnt lgkmcnt(0)
	v_pk_mul_f32 v[40:41], v[140:141], v[40:41]
	v_pk_mul_f32 v[42:43], v[142:143], v[42:43]
	v_pk_mul_f32 v[44:45], v[136:137], v[44:45]
	v_cndmask_b32_e64 v41, v41, -v41, s[0:1]
	v_pk_mul_f32 v[46:47], v[138:139], v[46:47]
	v_cndmask_b32_e64 v40, v40, -v40, s[0:1]
	v_cndmask_b32_e64 v43, v43, -v43, s[0:1]
	v_cndmask_b32_e64 v42, v42, -v42, s[0:1]
	v_cndmask_b32_e64 v45, v45, -v45, s[0:1]
	v_cndmask_b32_e64 v44, v44, -v44, s[0:1]
	v_cndmask_b32_e64 v47, v47, -v47, s[0:1]
	v_cndmask_b32_e64 v46, v46, -v46, s[0:1]
	v_pk_fma_f32 v[34:35], v[34:35], v[134:135], v[46:47]
	v_pk_fma_f32 v[32:33], v[32:33], v[132:133], v[44:45]
	v_pk_fma_f32 v[38:39], v[38:39], v[130:131], v[42:43]
	v_pk_fma_f32 v[36:37], v[36:37], v[128:129], v[40:41]
	s_and_b64 vcc, exec, s[54:55]
	s_cbranch_vccnz .LBB0_508

; #define ROPE_LOAD(buf, g) do { const int _pos = (row0 + ((g) >> 2) * HALF + ((g) & 3) * 16) & (SEQ - 1); const float* _rp = rope + _pos * 32 + 8 * (fq & 1); \
;                 rc[buf][0] = *(const f32x4*)_rp; rc[buf][1] = *(const f32x4*)(_rp + 4); rc[buf][2] = *(const f32x4*)(_rp + 16); rc[buf][3] = *(const f32x4*)(_rp + 20); } while (0)
;     __device__ __forceinline__ void operator()(const f32x4 (&acc)[2][2][4][2], const Unit& u, int wr, int wc, int fr, int fq) const {
;     ...
;                 if (wc == 0 && g + 1 < 8) ROPE_LOAD((g + 1) & 1, g + 1);
; #pragma unroll
;                 for (int bj = 0; bj < 2; ++bj) {
;                     float v[8] = {acc[ai][bj][m][0][0], acc[ai][bj][m][0][1], acc[ai][bj][m][0][2], acc[ai][bj][m][0][3],
;                                   acc[ai][bj][m][1][0], acc[ai][bj][m][1][1], acc[ai][bj][m][1][2], acc[ai][bj][m][1][3]};
;                     if (wc == 0) {
;                         const f32x4 c0 = rc[g & 1][0], c1 = rc[g & 1][1], s0 = rc[g & 1][2], s1 = rc[g & 1][3];
;                         const float cs[8] = {c0[0], c0[1], c0[2], c0[3], c1[0], c1[1], c1[2], c1[3]}, sn[8] = {s0[0], s0[1], s0[2], s0[3], s1[0], s1[1], s1[2], s1[3]};
; #pragma unroll
;                         for (int i = 0; i < 8; ++i) {
;                             const float pv = __shfl_xor(v[i], 32);
;                             v[i] = (fq < 2) ? (v[i] * cs[i] - pv * sn[i]) : (v[i] * cs[i] + pv * sn[i]);
;                         }
;                     }
.LBB0_517:
	v_and_b32_e32 v33, 64, v211
	v_xor_b32_e32 v32, 32, v211
	v_add_u32_e32 v33, 64, v33
	v_cmp_lt_i32_e32 vcc, v32, v33
	s_nop 1
	v_cndmask_b32_e32 v32, v211, v32, vcc
	v_lshlrev_b32_e32 v39, 2, v32
	ds_bpermute_b32 v32, v39, v28
	ds_bpermute_b32 v33, v39, v29
	ds_bpermute_b32 v34, v39, v30
	ds_bpermute_b32 v35, v39, v31
	ds_bpermute_b32 v36, v39, v24
	ds_bpermute_b32 v37, v39, v25
	ds_bpermute_b32 v38, v39, v26
	ds_bpermute_b32 v39, v39, v27
	s_waitcnt vmcnt(6) lgkmcnt(0)
	v_pk_mul_f32 v[32:33], v[156:157], v[32:33]
	v_pk_mul_f32 v[34:35], v[158:159], v[34:35]
	v_pk_mul_f32 v[36:37], v[152:153], v[36:37]
	v_cndmask_b32_e64 v33, v33, -v33, s[0:1]
	v_pk_mul_f32 v[38:39], v[154:155], v[38:39]
	v_cndmask_b32_e64 v32, v32, -v32, s[0:1]
	v_cndmask_b32_e64 v35, v35, -v35, s[0:1]
	v_cndmask_b32_e64 v34, v34, -v34, s[0:1]
	v_cndmask_b32_e64 v37, v37, -v37, s[0:1]
	v_cndmask_b32_e64 v36, v36, -v36, s[0:1]
	v_cndmask_b32_e64 v39, v39, -v39, s[0:1]
	v_cndmask_b32_e64 v38, v38, -v38, s[0:1]
	v_pk_fma_f32 v[26:27], v[26:27], v[150:151], v[38:39]
	v_pk_fma_f32 v[24:25], v[24:25], v[148:149], v[36:37]
	v_pk_fma_f32 v[30:31], v[30:31], v[146:147], v[34:35]
	v_pk_fma_f32 v[28:29], v[28:29], v[144:145], v[32:33]
	s_and_b64 vcc, exec, s[54:55]
	s_cbranch_vccnz .LBB0_515

; #define ROPE_LOAD(buf, g) do { const int _pos = (row0 + ((g) >> 2) * HALF + ((g) & 3) * 16) & (SEQ - 1); const float* _rp = rope + _pos * 32 + 8 * (fq & 1); \
;                 rc[buf][0] = *(const f32x4*)_rp; rc[buf][1] = *(const f32x4*)(_rp + 4); rc[buf][2] = *(const f32x4*)(_rp + 16); rc[buf][3] = *(const f32x4*)(_rp + 20); } while (0)
;     __device__ __forceinline__ void operator()(const f32x4 (&acc)[2][2][4][2], const Unit& u, int wr, int wc, int fr, int fq) const {
;     ...
;                 if (wc == 0 && g + 1 < 8) ROPE_LOAD((g + 1) & 1, g + 1);
; #pragma unroll
;                 for (int bj = 0; bj < 2; ++bj) {
;                     float v[8] = {acc[ai][bj][m][0][0], acc[ai][bj][m][0][1], acc[ai][bj][m][0][2], acc[ai][bj][m][0][3],
;                                   acc[ai][bj][m][1][0], acc[ai][bj][m][1][1], acc[ai][bj][m][1][2], acc[ai][bj][m][1][3]};
;                     if (wc == 0) {
;                         const f32x4 c0 = rc[g & 1][0], c1 = rc[g & 1][1], s0 = rc[g & 1][2], s1 = rc[g & 1][3];
;                         const float cs[8] = {c0[0], c0[1], c0[2], c0[3], c1[0], c1[1], c1[2], c1[3]}, sn[8] = {s0[0], s0[1], s0[2], s0[3], s1[0], s1[1], s1[2], s1[3]};
; #pragma unroll
;                         for (int i = 0; i < 8; ++i) {
;                             const float pv = __shfl_xor(v[i], 32);
;                             v[i] = (fq < 2) ? (v[i] * cs[i] - pv * sn[i]) : (v[i] * cs[i] + pv * sn[i]);
;                         }
;                     }
.LBB0_523:
	v_and_b32_e32 v25, 64, v211
	v_xor_b32_e32 v24, 32, v211
	v_add_u32_e32 v25, 64, v25
	v_cmp_lt_i32_e32 vcc, v24, v25
	s_nop 1
	v_cndmask_b32_e32 v24, v211, v24, vcc
	v_lshlrev_b32_e32 v31, 2, v24
	ds_bpermute_b32 v24, v31, v20
	ds_bpermute_b32 v25, v31, v21
	ds_bpermute_b32 v26, v31, v22
	ds_bpermute_b32 v27, v31, v23
	ds_bpermute_b32 v28, v31, v16
	ds_bpermute_b32 v29, v31, v17
	ds_bpermute_b32 v30, v31, v18
	ds_bpermute_b32 v31, v31, v19
	s_waitcnt lgkmcnt(0)
	v_pk_mul_f32 v[24:25], v[156:157], v[24:25]
	v_pk_mul_f32 v[26:27], v[158:159], v[26:27]
	v_pk_mul_f32 v[28:29], v[152:153], v[28:29]
	v_cndmask_b32_e64 v25, v25, -v25, s[0:1]
	v_pk_mul_f32 v[30:31], v[154:155], v[30:31]
	v_cndmask_b32_e64 v24, v24, -v24, s[0:1]
	v_cndmask_b32_e64 v27, v27, -v27, s[0:1]
	v_cndmask_b32_e64 v26, v26, -v26, s[0:1]
	v_cndmask_b32_e64 v29, v29, -v29, s[0:1]
	v_cndmask_b32_e64 v28, v28, -v28, s[0:1]
	v_cndmask_b32_e64 v31, v31, -v31, s[0:1]
	v_cndmask_b32_e64 v30, v30, -v30, s[0:1]
	v_pk_fma_f32 v[18:19], v[18:19], v[150:151], v[30:31]
	v_pk_fma_f32 v[16:17], v[16:17], v[148:149], v[28:29]
	v_pk_fma_f32 v[22:23], v[22:23], v[146:147], v[26:27]
	v_pk_fma_f32 v[20:21], v[20:21], v[144:145], v[24:25]
	s_and_b64 vcc, exec, s[54:55]
	s_cbranch_vccnz .LBB0_522

; #define ROPE_LOAD(buf, g) do { const int _pos = (row0 + ((g) >> 2) * HALF + ((g) & 3) * 16) & (SEQ - 1); const float* _rp = rope + _pos * 32 + 8 * (fq & 1); \
;                 rc[buf][0] = *(const f32x4*)_rp; rc[buf][1] = *(const f32x4*)(_rp + 4); rc[buf][2] = *(const f32x4*)(_rp + 16); rc[buf][3] = *(const f32x4*)(_rp + 20); } while (0)
;     __device__ __forceinline__ void operator()(const f32x4 (&acc)[2][2][4][2], const Unit& u, int wr, int wc, int fr, int fq) const {
;     ...
;                 if (wc == 0 && g + 1 < 8) ROPE_LOAD((g + 1) & 1, g + 1);
; #pragma unroll
;                 for (int bj = 0; bj < 2; ++bj) {
;                     float v[8] = {acc[ai][bj][m][0][0], acc[ai][bj][m][0][1], acc[ai][bj][m][0][2], acc[ai][bj][m][0][3],
;                                   acc[ai][bj][m][1][0], acc[ai][bj][m][1][1], acc[ai][bj][m][1][2], acc[ai][bj][m][1][3]};
;                     if (wc == 0) {
;                         const f32x4 c0 = rc[g & 1][0], c1 = rc[g & 1][1], s0 = rc[g & 1][2], s1 = rc[g & 1][3];
;                         const float cs[8] = {c0[0], c0[1], c0[2], c0[3], c1[0], c1[1], c1[2], c1[3]}, sn[8] = {s0[0], s0[1], s0[2], s0[3], s1[0], s1[1], s1[2], s1[3]};
; #pragma unroll
;                         for (int i = 0; i < 8; ++i) {
;                             const float pv = __shfl_xor(v[i], 32);
;                             v[i] = (fq < 2) ? (v[i] * cs[i] - pv * sn[i]) : (v[i] * cs[i] + pv * sn[i]);
;                         }
;                     }
.LBB0_529:
	v_and_b32_e32 v17, 64, v211
	v_xor_b32_e32 v16, 32, v211
	v_add_u32_e32 v17, 64, v17
	v_cmp_lt_i32_e32 vcc, v16, v17
	s_nop 1
	v_cndmask_b32_e32 v16, v211, v16, vcc
	v_lshlrev_b32_e32 v23, 2, v16
	ds_bpermute_b32 v16, v23, v12
	ds_bpermute_b32 v17, v23, v13
	ds_bpermute_b32 v18, v23, v14
	ds_bpermute_b32 v19, v23, v15
	ds_bpermute_b32 v20, v23, v8
	ds_bpermute_b32 v21, v23, v9
	ds_bpermute_b32 v22, v23, v10
	ds_bpermute_b32 v23, v23, v11
	s_waitcnt vmcnt(2) lgkmcnt(0)
	v_pk_mul_f32 v[16:17], v[140:141], v[16:17]
	v_pk_mul_f32 v[18:19], v[142:143], v[18:19]
	v_pk_mul_f32 v[20:21], v[136:137], v[20:21]
	v_cndmask_b32_e64 v17, v17, -v17, s[0:1]
	v_pk_mul_f32 v[22:23], v[138:139], v[22:23]
	v_cndmask_b32_e64 v16, v16, -v16, s[0:1]
	v_cndmask_b32_e64 v19, v19, -v19, s[0:1]
	v_cndmask_b32_e64 v18, v18, -v18, s[0:1]
	v_cndmask_b32_e64 v21, v21, -v21, s[0:1]
	v_cndmask_b32_e64 v20, v20, -v20, s[0:1]
	v_cndmask_b32_e64 v23, v23, -v23, s[0:1]
	v_cndmask_b32_e64 v22, v22, -v22, s[0:1]
	v_pk_fma_f32 v[10:11], v[10:11], v[134:135], v[22:23]
	v_pk_fma_f32 v[8:9], v[8:9], v[132:133], v[20:21]
	v_pk_fma_f32 v[14:15], v[14:15], v[130:131], v[18:19]
	v_pk_fma_f32 v[12:13], v[12:13], v[128:129], v[16:17]
	s_and_b64 vcc, exec, s[54:55]
	s_cbranch_vccnz .LBB0_528

; #define ROPE_LOAD(buf, g) do { const int _pos = (row0 + ((g) >> 2) * HALF + ((g) & 3) * 16) & (SEQ - 1); const float* _rp = rope + _pos * 32 + 8 * (fq & 1); \
;                 rc[buf][0] = *(const f32x4*)_rp; rc[buf][1] = *(const f32x4*)(_rp + 4); rc[buf][2] = *(const f32x4*)(_rp + 16); rc[buf][3] = *(const f32x4*)(_rp + 20); } while (0)
;     __device__ __forceinline__ void operator()(const f32x4 (&acc)[2][2][4][2], const Unit& u, int wr, int wc, int fr, int fq) const {
;     ...
;                 if (wc == 0 && g + 1 < 8) ROPE_LOAD((g + 1) & 1, g + 1);
; #pragma unroll
;                 for (int bj = 0; bj < 2; ++bj) {
;                     float v[8] = {acc[ai][bj][m][0][0], acc[ai][bj][m][0][1], acc[ai][bj][m][0][2], acc[ai][bj][m][0][3],
;                                   acc[ai][bj][m][1][0], acc[ai][bj][m][1][1], acc[ai][bj][m][1][2], acc[ai][bj][m][1][3]};
;                     if (wc == 0) {
;                         const f32x4 c0 = rc[g & 1][0], c1 = rc[g & 1][1], s0 = rc[g & 1][2], s1 = rc[g & 1][3];
;                         const float cs[8] = {c0[0], c0[1], c0[2], c0[3], c1[0], c1[1], c1[2], c1[3]}, sn[8] = {s0[0], s0[1], s0[2], s0[3], s1[0], s1[1], s1[2], s1[3]};
; #pragma unroll
;                         for (int i = 0; i < 8; ++i) {
;                             const float pv = __shfl_xor(v[i], 32);
;                             v[i] = (fq < 2) ? (v[i] * cs[i] - pv * sn[i]) : (v[i] * cs[i] + pv * sn[i]);
;                         }
;                     }
.LBB0_535:
	v_and_b32_e32 v9, 64, v211
	v_xor_b32_e32 v8, 32, v211
	v_add_u32_e32 v9, 64, v9
	v_cmp_lt_i32_e32 vcc, v8, v9
	s_nop 1
	v_cndmask_b32_e32 v8, v211, v8, vcc
	v_lshlrev_b32_e32 v15, 2, v8
	ds_bpermute_b32 v8, v15, v4
	ds_bpermute_b32 v9, v15, v5
	ds_bpermute_b32 v10, v15, v6
	ds_bpermute_b32 v11, v15, v7
	ds_bpermute_b32 v12, v15, v0
	ds_bpermute_b32 v13, v15, v1
	ds_bpermute_b32 v14, v15, v2
	ds_bpermute_b32 v15, v15, v3
	s_waitcnt lgkmcnt(0)
	v_pk_mul_f32 v[8:9], v[140:141], v[8:9]
	v_pk_mul_f32 v[10:11], v[142:143], v[10:11]
	v_pk_mul_f32 v[12:13], v[136:137], v[12:13]
	v_cndmask_b32_e64 v9, v9, -v9, s[0:1]
	v_pk_mul_f32 v[14:15], v[138:139], v[14:15]
	v_cndmask_b32_e64 v8, v8, -v8, s[0:1]
	v_cndmask_b32_e64 v11, v11, -v11, s[0:1]
	v_cndmask_b32_e64 v10, v10, -v10, s[0:1]
	v_cndmask_b32_e64 v13, v13, -v13, s[0:1]
	v_cndmask_b32_e64 v12, v12, -v12, s[0:1]
	v_cndmask_b32_e64 v15, v15, -v15, s[0:1]
	v_cndmask_b32_e64 v14, v14, -v14, s[0:1]
	v_pk_fma_f32 v[2:3], v[2:3], v[134:135], v[14:15]
	v_pk_fma_f32 v[0:1], v[0:1], v[132:133], v[12:13]
	v_pk_fma_f32 v[6:7], v[6:7], v[130:131], v[10:11]
	v_pk_fma_f32 v[4:5], v[4:5], v[128:129], v[8:9]
	s_and_b64 vcc, exec, s[54:55]
	s_cbranch_vccnz .LBB0_534

;     __device__ __forceinline__ void operator()(const f32x4 (&acc)[2][2][4][2], const Unit& u, int wr, int wc, int fr, int fq) const {
;     ...
;             BC_LOAD(0, 0);
; #pragma unroll
;             for (int g = 0; g < 16; ++g) {
;                 const int ai = g >> 3, m = (g >> 1) & 3, bj = g & 1;
;                 const int r = row0 + ai * HALF + m * 16;
;                 if (g + 1 < 16) BC_LOAD((g + 1) & 1, g + 1);
;                 {
;                     {
;                         const int col = cb + bj * HALF + lc;
;                         const size_t hoff = ((size_t)((r >> 11) * 4 + (col >> 7)) * SEQ + (r & (SEQ - 1))) * 128 + (col & 127);
;                         const f32x4 b0 = bc[g & 1][0], b1 = bc[g & 1][1];
;                         const f32x4 v0 = acc[ai][bj][m][0], v1 = acc[ai][bj][m][1];
;                         const float L2E = 1.4426950408889634f;
;                         if (isq) {
;                             const float s = 0.08838834764831845f;
;                             u32x4 o; o[0] = cvt_pk_bf16(v0[0] * s * __builtin_amdgcn_exp2f(b0[0] * L2E), v0[1] * s * __builtin_amdgcn_exp2f(b0[1] * L2E));
;                             o[1] = cvt_pk_bf16(v0[2] * s * __builtin_amdgcn_exp2f(b0[2] * L2E), v0[3] * s * __builtin_amdgcn_exp2f(b0[3] * L2E));
;                             o[2] = cvt_pk_bf16(v1[0] * s * __builtin_amdgcn_exp2f(b1[0] * L2E), v1[1] * s * __builtin_amdgcn_exp2f(b1[1] * L2E));
;                             o[3] = cvt_pk_bf16(v1[2] * s * __builtin_amdgcn_exp2f(b1[2] * L2E), v1[3] * s * __builtin_amdgcn_exp2f(b1[3] * L2E));
;                             __builtin_nontemporal_store(o, (u32x4*)(d0 + hoff));
;                         } else {
;                             u32x4 o;
;                             o[0] = cvt_pk_bf16(v0[0] * __builtin_amdgcn_exp2f(-b0[0] * L2E), v0[1] * __builtin_amdgcn_exp2f(-b0[1] * L2E));
;                             o[1] = cvt_pk_bf16(v0[2] * __builtin_amdgcn_exp2f(-b0[2] * L2E), v0[3] * __builtin_amdgcn_exp2f(-b0[3] * L2E));
;                             o[2] = cvt_pk_bf16(v1[0] * __builtin_amdgcn_exp2f(-b1[0] * L2E), v1[1] * __builtin_amdgcn_exp2f(-b1[1] * L2E));
;                             o[3] = cvt_pk_bf16(v1[2] * __builtin_amdgcn_exp2f(-b1[2] * L2E), v1[3] * __builtin_amdgcn_exp2f(-b1[3] * L2E));
;                             __builtin_nontemporal_store(o, (u32x4*)(d0 + hoff));
.LBB0_1413:
	s_and_b64 vcc, exec, s[2:3]
	s_cbranch_vccz .LBB0_1628
	s_cmp_gt_u32 s76, 13
	s_cselect_b64 s[42:43], -1, 0
	s_cmp_lt_u32 s76, 14
	s_cselect_b64 s[2:3], -1, 0
	s_and_b64 s[8:9], s[2:3], exec
	s_cselect_b32 s10, -12, -14
	v_ashrrev_i32_e32 v193, 31, v192
	s_add_i32 s10, s10, s76
	v_lshlrev_b64 v[128:129], 11, v[192:193]
	v_lshl_or_b32 v168, s10, 8, v170
	v_lshl_add_u64 v[128:129], s[22:23], 0, v[128:129]
	v_lshl_add_u64 v[136:137], v[168:169], 2, v[128:129]
	global_load_dwordx4 v[132:135], v[136:137], off offset:16
	global_load_dwordx4 v[144:147], v[136:137], off
	global_load_dwordx4 v[128:131], v[136:137], off offset:528
	s_nop 0
	global_load_dwordx4 v[136:139], v[136:137], off offset:512
	s_mov_b64 s[8:9], -1
	s_and_b64 vcc, exec, s[42:43]
	s_cbranch_vccz .LBB0_1416
	s_waitcnt vmcnt(2)
	v_mul_f32_e32 v140, 0xbfb8aa3b, v144
	v_mul_f32_e32 v141, 0xbfb8aa3b, v145
	v_exp_f32_e32 v140, v140
	v_exp_f32_e32 v141, v141
	v_mul_f32_e32 v142, 0xbfb8aa3b, v146
	v_mul_f32_e32 v143, 0xbfb8aa3b, v147
	v_exp_f32_e32 v142, v142
	v_pk_mul_f32 v[140:141], v[124:125], v[140:141]
	v_exp_f32_e32 v143, v143
	v_cvt_pk_bf16_f32 v140, v140, v141
	v_mul_f32_e32 v141, 0xbfb8aa3b, v132
	v_exp_f32_e32 v148, v141
	v_mul_f32_e32 v141, 0xbfb8aa3b, v133
	v_exp_f32_e32 v149, v141
	v_mul_f32_e32 v141, 0xbfb8aa3b, v134
	v_exp_f32_e32 v150, v141
	v_pk_mul_f32 v[142:143], v[126:127], v[142:143]
	s_mov_b64 s[8:9], 0
	v_cvt_pk_bf16_f32 v141, v142, v143
	v_pk_mul_f32 v[142:143], v[120:121], v[148:149]
	v_mul_f32_e32 v148, v122, v150
	v_cvt_pk_bf16_f32 v142, v142, v143
	v_mov_b32_e32 v149, v123
.LBB0_1416:
	s_andn2_b64 vcc, exec, s[8:9]
	s_mov_b32 s8, 0xbfb8aa3b
	s_cbranch_vccnz .LBB0_1418
	s_waitcnt vmcnt(2)
	v_mul_f32_e32 v140, 0x3fb8aa3b, v144
	v_mul_f32_e32 v141, 0x3fb8aa3b, v145
	v_exp_f32_e32 v140, v140
	v_exp_f32_e32 v141, v141
	v_pk_mul_f32 v[142:143], v[124:125], s[34:35] op_sel_hi:[1,0]
	v_mul_f32_e32 v132, 0x3fb8aa3b, v132
	v_mul_f32_e32 v133, 0x3fb8aa3b, v133
	v_pk_mul_f32 v[140:141], v[142:143], v[140:141]
	v_exp_f32_e32 v132, v132
	v_cvt_pk_bf16_f32 v140, v140, v141
	v_mul_f32_e32 v141, 0x3fb8aa3b, v146
	v_exp_f32_e32 v142, v141
	v_mul_f32_e32 v141, 0x3fb8aa3b, v147
	v_exp_f32_e32 v143, v141
	v_exp_f32_e32 v133, v133
	v_pk_mul_f32 v[144:145], v[126:127], s[34:35] op_sel_hi:[1,0]
	v_mul_f32_e32 v134, 0x3fb8aa3b, v134
	v_pk_mul_f32 v[142:143], v[144:145], v[142:143]
	v_exp_f32_e32 v190, v134
	v_cvt_pk_bf16_f32 v141, v142, v143
	v_pk_mul_f32 v[142:143], v[120:121], s[34:35] op_sel_hi:[1,0]
	s_mov_b32 s8, 0x3fb8aa3b
	v_pk_mul_f32 v[132:133], v[142:143], v[132:133]
	s_nop 0
	v_cvt_pk_bf16_f32 v142, v132, v133
	v_mul_f32_e32 v132, 0x3db504f3, v122
	v_mov_b32_e32 v133, v123
	v_pk_mul_f32 v[148:149], v[132:133], v[190:191]
.LBB0_1418:
	s_and_b64 s[2:3], s[2:3], exec
	s_cselect_b32 s2, s72, 0x47188000
	v_readlane_b32 s80, v252, 28
	v_readlane_b32 s81, v252, 29
	s_add_u32 s2, s80, s2
	s_addc_u32 s3, s81, 0
	s_ashr_i32 s9, s15, 9
	s_and_b32 s33, s9, -4
	s_lshl_b32 s17, s10, 1
	s_waitcnt vmcnt(2)
	v_mul_f32_e32 v132, s8, v135
	s_add_i32 s10, s33, s17
	v_exp_f32_e32 v132, v132
	s_ashr_i32 s11, s10, 31
	v_lshlrev_b32_e32 v133, 7, v192
	s_lshl_b64 s[8:9], s[10:11], 19
	v_and_b32_e32 v156, 0x3e780, v133
	s_add_u32 s10, s2, s8
	v_mul_f32_e32 v132, v149, v132
	s_addc_u32 s11, s3, s9
	v_lshlrev_b32_e32 v150, 1, v156
	v_mov_b32_e32 v151, v169
	v_cvt_pk_bf16_f32 v143, v148, v132
	v_lshl_add_u64 v[132:133], s[10:11], 0, v[150:151]
	v_lshlrev_b32_e32 v148, 1, v170
	v_mov_b32_e32 v149, v169
	v_lshl_add_u64 v[132:133], v[132:133], 0, v[148:149]
	global_store_dwordx4 v[132:133], v[140:143], off nt
	v_or_b32_e32 v132, 16, v192
	v_ashrrev_i32_e32 v133, 31, v132
	v_lshlrev_b64 v[132:133], 11, v[132:133]
	v_lshl_add_u64 v[132:133], s[22:23], 0, v[132:133]
	v_lshl_add_u64 v[152:153], v[168:169], 2, v[132:133]
	global_load_dwordx4 v[132:135], v[152:153], off offset:16
	global_load_dwordx4 v[140:143], v[152:153], off
	s_waitcnt vmcnt(3)
	v_cndmask_b32_e64 v144, 0, 1, s[42:43]
	v_cmp_ne_u32_e64 s[8:9], 1, v144
	s_andn2_b64 vcc, exec, s[42:43]
	s_mov_b64 s[42:43], -1
	v_readlane_b32 s82, v252, 30
	v_readlane_b32 s83, v252, 31
	s_cbranch_vccnz .LBB0_1420
	v_mul_f32_e32 v144, 0xbfb8aa3b, v136
	v_mul_f32_e32 v145, 0xbfb8aa3b, v137
	v_exp_f32_e32 v144, v144
	v_exp_f32_e32 v145, v145
	v_mul_f32_e32 v146, 0xbfb8aa3b, v138
	v_mul_f32_e32 v147, 0xbfb8aa3b, v139
	v_exp_f32_e32 v146, v146
	v_pk_mul_f32 v[144:145], v[116:117], v[144:145]
	v_exp_f32_e32 v147, v147
	v_cvt_pk_bf16_f32 v144, v144, v145
	v_mul_f32_e32 v145, 0xbfb8aa3b, v128
	v_exp_f32_e32 v154, v145
	v_mul_f32_e32 v145, 0xbfb8aa3b, v129
	v_exp_f32_e32 v155, v145
	v_mul_f32_e32 v145, 0xbfb8aa3b, v130
	v_exp_f32_e32 v149, v145
	v_pk_mul_f32 v[146:147], v[118:119], v[146:147]
	s_mov_b64 s[42:43], 0
	v_cvt_pk_bf16_f32 v145, v146, v147
	v_pk_mul_f32 v[146:147], v[112:113], v[154:155]
	v_mul_f32_e32 v154, v114, v149
	v_cvt_pk_bf16_f32 v146, v146, v147
	v_mov_b32_e32 v155, v115

;     __device__ __forceinline__ void operator()(const f32x4 (&acc)[2][2][4][2], const Unit& u, int wr, int wc, int fr, int fq) const {
;     ...
;             BC_LOAD(0, 0);
; #pragma unroll
;             for (int g = 0; g < 16; ++g) {
;                 const int ai = g >> 3, m = (g >> 1) & 3, bj = g & 1;
;                 const int r = row0 + ai * HALF + m * 16;
;                 if (g + 1 < 16) BC_LOAD((g + 1) & 1, g + 1);
;                 {
;                     {
;                         const int col = cb + bj * HALF + lc;
;                         const size_t hoff = ((size_t)((r >> 11) * 4 + (col >> 7)) * SEQ + (r & (SEQ - 1))) * 128 + (col & 127);
;                         const f32x4 b0 = bc[g & 1][0], b1 = bc[g & 1][1];
;                         const f32x4 v0 = acc[ai][bj][m][0], v1 = acc[ai][bj][m][1];
;                         const float L2E = 1.4426950408889634f;
;                         if (isq) {
;                             const float s = 0.08838834764831845f;
;                             u32x4 o; o[0] = cvt_pk_bf16(v0[0] * s * __builtin_amdgcn_exp2f(b0[0] * L2E), v0[1] * s * __builtin_amdgcn_exp2f(b0[1] * L2E));
;                             o[1] = cvt_pk_bf16(v0[2] * s * __builtin_amdgcn_exp2f(b0[2] * L2E), v0[3] * s * __builtin_amdgcn_exp2f(b0[3] * L2E));
;                             o[2] = cvt_pk_bf16(v1[0] * s * __builtin_amdgcn_exp2f(b1[0] * L2E), v1[1] * s * __builtin_amdgcn_exp2f(b1[1] * L2E));
;                             o[3] = cvt_pk_bf16(v1[2] * s * __builtin_amdgcn_exp2f(b1[2] * L2E), v1[3] * s * __builtin_amdgcn_exp2f(b1[3] * L2E));
;                             __builtin_nontemporal_store(o, (u32x4*)(d0 + hoff));
;                         } else {
;                             u32x4 o;
;                             o[0] = cvt_pk_bf16(v0[0] * __builtin_amdgcn_exp2f(-b0[0] * L2E), v0[1] * __builtin_amdgcn_exp2f(-b0[1] * L2E));
;                             o[1] = cvt_pk_bf16(v0[2] * __builtin_amdgcn_exp2f(-b0[2] * L2E), v0[3] * __builtin_amdgcn_exp2f(-b0[3] * L2E));
;                             o[2] = cvt_pk_bf16(v1[0] * __builtin_amdgcn_exp2f(-b1[0] * L2E), v1[1] * __builtin_amdgcn_exp2f(-b1[1] * L2E));
;                             o[3] = cvt_pk_bf16(v1[2] * __builtin_amdgcn_exp2f(-b1[2] * L2E), v1[3] * __builtin_amdgcn_exp2f(-b1[3] * L2E));
;                             __builtin_nontemporal_store(o, (u32x4*)(d0 + hoff));
.LBB0_1422:
	v_mul_f32_e32 v128, s18, v131
	s_or_b32 s18, s17, 1
	v_exp_f32_e32 v128, v128
	s_add_i32 s42, s33, s18
	s_ashr_i32 s43, s42, 31
	s_lshl_b64 s[42:43], s[42:43], 19
	s_add_u32 s42, s2, s42
	v_mul_f32_e32 v128, v155, v128
	s_addc_u32 s43, s3, s43
	v_mov_b32_e32 v151, v169
	v_cvt_pk_bf16_f32 v147, v154, v128
	v_lshl_add_u64 v[128:129], s[42:43], 0, v[150:151]
	v_mov_b32_e32 v149, v169
	v_lshl_add_u64 v[128:129], v[128:129], 0, v[148:149]
	global_store_dwordx4 v[128:129], v[144:147], off nt
	global_load_dwordx4 v[128:131], v[152:153], off offset:528
	s_nop 0
	global_load_dwordx4 v[136:139], v[152:153], off offset:512
	s_and_b64 vcc, exec, s[8:9]
	s_mov_b64 s[48:49], -1
	s_cbranch_vccnz .LBB0_1424
	s_waitcnt vmcnt(3)
	v_mul_f32_e32 v144, 0xbfb8aa3b, v140
	v_mul_f32_e32 v145, 0xbfb8aa3b, v141
	v_exp_f32_e32 v144, v144
	v_exp_f32_e32 v145, v145
	v_mul_f32_e32 v146, 0xbfb8aa3b, v142
	v_mul_f32_e32 v147, 0xbfb8aa3b, v143
	v_exp_f32_e32 v146, v146
	v_pk_mul_f32 v[144:145], v[108:109], v[144:145]
	v_exp_f32_e32 v147, v147
	v_cvt_pk_bf16_f32 v144, v144, v145
	v_mul_f32_e32 v145, 0xbfb8aa3b, v132
	v_exp_f32_e32 v150, v145
	v_mul_f32_e32 v145, 0xbfb8aa3b, v133
	v_exp_f32_e32 v151, v145
	v_mul_f32_e32 v145, 0xbfb8aa3b, v134
	v_exp_f32_e32 v149, v145
	v_pk_mul_f32 v[146:147], v[110:111], v[146:147]
	s_mov_b64 s[48:49], 0
	v_cvt_pk_bf16_f32 v145, v146, v147
	v_pk_mul_f32 v[146:147], v[104:105], v[150:151]
	v_mul_f32_e32 v152, v106, v149
	v_cvt_pk_bf16_f32 v146, v146, v147
	v_mov_b32_e32 v153, v107
.LBB0_1424:
	s_andn2_b64 vcc, exec, s[48:49]
	s_mov_b32 s33, 0xbfb8aa3b
	s_cbranch_vccnz .LBB0_1426
	s_waitcnt vmcnt(3)
	v_mul_f32_e32 v140, 0x3fb8aa3b, v140
	v_mul_f32_e32 v141, 0x3fb8aa3b, v141
	v_exp_f32_e32 v140, v140
	v_exp_f32_e32 v141, v141
	v_pk_mul_f32 v[144:145], v[108:109], s[34:35] op_sel_hi:[1,0]
	v_mul_f32_e32 v132, 0x3fb8aa3b, v132
	v_mul_f32_e32 v133, 0x3fb8aa3b, v133
	v_pk_mul_f32 v[140:141], v[144:145], v[140:141]
	v_exp_f32_e32 v132, v132
	v_cvt_pk_bf16_f32 v144, v140, v141
	v_mul_f32_e32 v140, 0x3fb8aa3b, v142
	v_mul_f32_e32 v141, 0x3fb8aa3b, v143
	v_exp_f32_e32 v140, v140
	v_exp_f32_e32 v141, v141
	v_exp_f32_e32 v133, v133
	v_pk_mul_f32 v[142:143], v[110:111], s[34:35] op_sel_hi:[1,0]
	v_mul_f32_e32 v134, 0x3fb8aa3b, v134
	v_pk_mul_f32 v[140:141], v[142:143], v[140:141]
	v_exp_f32_e32 v190, v134
	v_cvt_pk_bf16_f32 v145, v140, v141
	v_pk_mul_f32 v[140:141], v[104:105], s[34:35] op_sel_hi:[1,0]
	s_mov_b32 s33, 0x3fb8aa3b
	v_pk_mul_f32 v[132:133], v[140:141], v[132:133]
	s_nop 0
	v_cvt_pk_bf16_f32 v146, v132, v133
	v_mul_f32_e32 v132, 0x3db504f3, v106
	v_mov_b32_e32 v133, v107
	v_pk_mul_f32 v[152:153], v[132:133], v[190:191]
.LBB0_1426:
	s_waitcnt vmcnt(3)
	v_mul_f32_e32 v132, s33, v135
	v_exp_f32_e32 v132, v132
	v_or_b32_e32 v133, 0x800, v156
	v_mov_b32_e32 v151, v169
	v_lshlrev_b32_e32 v150, 1, v133
	v_mul_f32_e32 v132, v153, v132
	v_cvt_pk_bf16_f32 v147, v152, v132
	v_lshl_add_u64 v[132:133], s[10:11], 0, v[150:151]
	v_mov_b32_e32 v149, v169
	v_lshl_add_u64 v[132:133], v[132:133], 0, v[148:149]
	global_store_dwordx4 v[132:133], v[144:147], off nt
	v_or_b32_e32 v132, 32, v192
	v_ashrrev_i32_e32 v133, 31, v132
	v_lshlrev_b64 v[132:133], 11, v[132:133]
	v_lshl_add_u64 v[132:133], s[22:23], 0, v[132:133]
	v_lshl_add_u64 v[152:153], v[168:169], 2, v[132:133]
	global_load_dwordx4 v[132:135], v[152:153], off offset:16
	global_load_dwordx4 v[140:143], v[152:153], off
	s_waitcnt vmcnt(3)
	s_and_b64 vcc, exec, s[8:9]
	s_mov_b64 s[48:49], -1
	s_cbranch_vccnz .LBB0_1428
	v_mul_f32_e32 v144, 0xbfb8aa3b, v136
	v_mul_f32_e32 v145, 0xbfb8aa3b, v137
	v_exp_f32_e32 v144, v144
	v_exp_f32_e32 v145, v145
	v_mul_f32_e32 v146, 0xbfb8aa3b, v138
	v_mul_f32_e32 v147, 0xbfb8aa3b, v139
	v_exp_f32_e32 v146, v146
	v_pk_mul_f32 v[144:145], v[100:101], v[144:145]
	v_exp_f32_e32 v147, v147
	v_cvt_pk_bf16_f32 v144, v144, v145
	v_mul_f32_e32 v145, 0xbfb8aa3b, v128
	v_exp_f32_e32 v154, v145
	v_mul_f32_e32 v145, 0xbfb8aa3b, v129
	v_exp_f32_e32 v155, v145
	v_mul_f32_e32 v145, 0xbfb8aa3b, v130
	v_exp_f32_e32 v149, v145
	v_pk_mul_f32 v[146:147], v[102:103], v[146:147]
	s_mov_b64 s[48:49], 0
	v_cvt_pk_bf16_f32 v145, v146, v147
	v_pk_mul_f32 v[146:147], v[96:97], v[154:155]
	v_mul_f32_e32 v154, v98, v149
	v_cvt_pk_bf16_f32 v146, v146, v147
	v_mov_b32_e32 v155, v99

;     __device__ __forceinline__ void operator()(const f32x4 (&acc)[2][2][4][2], const Unit& u, int wr, int wc, int fr, int fq) const {
;     ...
;             BC_LOAD(0, 0);
; #pragma unroll
;             for (int g = 0; g < 16; ++g) {
;                 const int ai = g >> 3, m = (g >> 1) & 3, bj = g & 1;
;                 const int r = row0 + ai * HALF + m * 16;
;                 if (g + 1 < 16) BC_LOAD((g + 1) & 1, g + 1);
;                 {
;                     {
;                         const int col = cb + bj * HALF + lc;
;                         const size_t hoff = ((size_t)((r >> 11) * 4 + (col >> 7)) * SEQ + (r & (SEQ - 1))) * 128 + (col & 127);
;                         const f32x4 b0 = bc[g & 1][0], b1 = bc[g & 1][1];
;                         const f32x4 v0 = acc[ai][bj][m][0], v1 = acc[ai][bj][m][1];
;                         const float L2E = 1.4426950408889634f;
;                         if (isq) {
;                             const float s = 0.08838834764831845f;
;                             u32x4 o; o[0] = cvt_pk_bf16(v0[0] * s * __builtin_amdgcn_exp2f(b0[0] * L2E), v0[1] * s * __builtin_amdgcn_exp2f(b0[1] * L2E));
;                             o[1] = cvt_pk_bf16(v0[2] * s * __builtin_amdgcn_exp2f(b0[2] * L2E), v0[3] * s * __builtin_amdgcn_exp2f(b0[3] * L2E));
;                             o[2] = cvt_pk_bf16(v1[0] * s * __builtin_amdgcn_exp2f(b1[0] * L2E), v1[1] * s * __builtin_amdgcn_exp2f(b1[1] * L2E));
;                             o[3] = cvt_pk_bf16(v1[2] * s * __builtin_amdgcn_exp2f(b1[2] * L2E), v1[3] * s * __builtin_amdgcn_exp2f(b1[3] * L2E));
;                             __builtin_nontemporal_store(o, (u32x4*)(d0 + hoff));
;                         } else {
;                             u32x4 o;
;                             o[0] = cvt_pk_bf16(v0[0] * __builtin_amdgcn_exp2f(-b0[0] * L2E), v0[1] * __builtin_amdgcn_exp2f(-b0[1] * L2E));
;                             o[1] = cvt_pk_bf16(v0[2] * __builtin_amdgcn_exp2f(-b0[2] * L2E), v0[3] * __builtin_amdgcn_exp2f(-b0[3] * L2E));
;                             o[2] = cvt_pk_bf16(v1[0] * __builtin_amdgcn_exp2f(-b1[0] * L2E), v1[1] * __builtin_amdgcn_exp2f(-b1[1] * L2E));
;                             o[3] = cvt_pk_bf16(v1[2] * __builtin_amdgcn_exp2f(-b1[2] * L2E), v1[3] * __builtin_amdgcn_exp2f(-b1[3] * L2E));
;                             __builtin_nontemporal_store(o, (u32x4*)(d0 + hoff));
.LBB0_1430:
	v_mul_f32_e32 v128, s33, v131
	v_exp_f32_e32 v130, v128
	v_mov_b32_e32 v151, v169
	v_mov_b32_e32 v149, v169
	v_lshl_add_u64 v[128:129], s[42:43], 0, v[150:151]
	v_mul_f32_e32 v130, v155, v130
	v_cvt_pk_bf16_f32 v147, v154, v130
	v_lshl_add_u64 v[128:129], v[128:129], 0, v[148:149]
	global_store_dwordx4 v[128:129], v[144:147], off nt
	global_load_dwordx4 v[128:131], v[152:153], off offset:528
	s_nop 0
	global_load_dwordx4 v[136:139], v[152:153], off offset:512
	s_and_b64 vcc, exec, s[8:9]
	s_mov_b64 s[48:49], -1
	s_cbranch_vccnz .LBB0_1432
	s_waitcnt vmcnt(3)
	v_mul_f32_e32 v144, 0xbfb8aa3b, v140
	v_mul_f32_e32 v145, 0xbfb8aa3b, v141
	v_exp_f32_e32 v144, v144
	v_exp_f32_e32 v145, v145
	v_mul_f32_e32 v146, 0xbfb8aa3b, v142
	v_mul_f32_e32 v147, 0xbfb8aa3b, v143
	v_exp_f32_e32 v146, v146
	v_pk_mul_f32 v[144:145], v[92:93], v[144:145]
	v_exp_f32_e32 v147, v147
	v_cvt_pk_bf16_f32 v144, v144, v145
	v_mul_f32_e32 v145, 0xbfb8aa3b, v132
	v_exp_f32_e32 v150, v145
	v_mul_f32_e32 v145, 0xbfb8aa3b, v133
	v_exp_f32_e32 v151, v145
	v_mul_f32_e32 v145, 0xbfb8aa3b, v134
	v_exp_f32_e32 v149, v145
	v_pk_mul_f32 v[146:147], v[94:95], v[146:147]
	s_mov_b64 s[48:49], 0
	v_cvt_pk_bf16_f32 v145, v146, v147
	v_pk_mul_f32 v[146:147], v[88:89], v[150:151]
	v_mul_f32_e32 v152, v90, v149
	v_cvt_pk_bf16_f32 v146, v146, v147
	v_mov_b32_e32 v153, v91
.LBB0_1432:
	s_andn2_b64 vcc, exec, s[48:49]
	s_mov_b32 s33, 0xbfb8aa3b
	s_cbranch_vccnz .LBB0_1434
	s_waitcnt vmcnt(3)
	v_mul_f32_e32 v140, 0x3fb8aa3b, v140
	v_mul_f32_e32 v141, 0x3fb8aa3b, v141
	v_exp_f32_e32 v140, v140
	v_exp_f32_e32 v141, v141
	v_pk_mul_f32 v[144:145], v[92:93], s[34:35] op_sel_hi:[1,0]
	v_mul_f32_e32 v132, 0x3fb8aa3b, v132
	v_mul_f32_e32 v133, 0x3fb8aa3b, v133
	v_pk_mul_f32 v[140:141], v[144:145], v[140:141]
	v_exp_f32_e32 v132, v132
	v_cvt_pk_bf16_f32 v144, v140, v141
	v_mul_f32_e32 v140, 0x3fb8aa3b, v142
	v_mul_f32_e32 v141, 0x3fb8aa3b, v143
	v_exp_f32_e32 v140, v140
	v_exp_f32_e32 v141, v141
	v_exp_f32_e32 v133, v133
	v_pk_mul_f32 v[142:143], v[94:95], s[34:35] op_sel_hi:[1,0]
	v_mul_f32_e32 v134, 0x3fb8aa3b, v134
	v_pk_mul_f32 v[140:141], v[142:143], v[140:141]
	v_exp_f32_e32 v190, v134
	v_cvt_pk_bf16_f32 v145, v140, v141
	v_pk_mul_f32 v[140:141], v[88:89], s[34:35] op_sel_hi:[1,0]
	s_mov_b32 s33, 0x3fb8aa3b
	v_pk_mul_f32 v[132:133], v[140:141], v[132:133]
	s_nop 0
	v_cvt_pk_bf16_f32 v146, v132, v133
	v_mul_f32_e32 v132, 0x3db504f3, v90
	v_mov_b32_e32 v133, v91
	v_pk_mul_f32 v[152:153], v[132:133], v[190:191]
.LBB0_1434:
	s_waitcnt vmcnt(3)
	v_mul_f32_e32 v132, s33, v135
	v_exp_f32_e32 v132, v132
	v_or_b32_e32 v133, 0x1000, v156
	v_mov_b32_e32 v151, v169
	v_lshlrev_b32_e32 v150, 1, v133
	v_mul_f32_e32 v132, v153, v132
	v_cvt_pk_bf16_f32 v147, v152, v132
	v_lshl_add_u64 v[132:133], s[10:11], 0, v[150:151]
	v_mov_b32_e32 v149, v169
	v_lshl_add_u64 v[132:133], v[132:133], 0, v[148:149]
	global_store_dwordx4 v[132:133], v[144:147], off nt
	v_or_b32_e32 v132, 48, v192
	v_ashrrev_i32_e32 v133, 31, v132
	v_lshlrev_b64 v[132:133], 11, v[132:133]
	v_lshl_add_u64 v[132:133], s[22:23], 0, v[132:133]
	v_lshl_add_u64 v[152:153], v[168:169], 2, v[132:133]
	global_load_dwordx4 v[132:135], v[152:153], off offset:16
	global_load_dwordx4 v[140:143], v[152:153], off
	s_waitcnt vmcnt(3)
	s_and_b64 vcc, exec, s[8:9]
	s_mov_b64 s[48:49], -1
	s_cbranch_vccnz .LBB0_1436
	v_mul_f32_e32 v144, 0xbfb8aa3b, v136
	v_mul_f32_e32 v145, 0xbfb8aa3b, v137
	v_exp_f32_e32 v144, v144
	v_exp_f32_e32 v145, v145
	v_mul_f32_e32 v146, 0xbfb8aa3b, v138
	v_mul_f32_e32 v147, 0xbfb8aa3b, v139
	v_exp_f32_e32 v146, v146
	v_pk_mul_f32 v[144:145], v[84:85], v[144:145]
	v_exp_f32_e32 v147, v147
	v_cvt_pk_bf16_f32 v144, v144, v145
	v_mul_f32_e32 v145, 0xbfb8aa3b, v128
	v_exp_f32_e32 v154, v145
	v_mul_f32_e32 v145, 0xbfb8aa3b, v129
	v_exp_f32_e32 v155, v145
	v_mul_f32_e32 v145, 0xbfb8aa3b, v130
	v_exp_f32_e32 v149, v145
	v_pk_mul_f32 v[146:147], v[86:87], v[146:147]
	s_mov_b64 s[48:49], 0
	v_cvt_pk_bf16_f32 v145, v146, v147
	v_pk_mul_f32 v[146:147], v[80:81], v[154:155]
	v_mul_f32_e32 v154, v82, v149
	v_cvt_pk_bf16_f32 v146, v146, v147
	v_mov_b32_e32 v155, v83

;     __device__ __forceinline__ void operator()(const f32x4 (&acc)[2][2][4][2], const Unit& u, int wr, int wc, int fr, int fq) const {
;     ...
;             BC_LOAD(0, 0);
; #pragma unroll
;             for (int g = 0; g < 16; ++g) {
;                 const int ai = g >> 3, m = (g >> 1) & 3, bj = g & 1;
;                 const int r = row0 + ai * HALF + m * 16;
;                 if (g + 1 < 16) BC_LOAD((g + 1) & 1, g + 1);
;                 {
;                     {
;                         const int col = cb + bj * HALF + lc;
;                         const size_t hoff = ((size_t)((r >> 11) * 4 + (col >> 7)) * SEQ + (r & (SEQ - 1))) * 128 + (col & 127);
;                         const f32x4 b0 = bc[g & 1][0], b1 = bc[g & 1][1];
;                         const f32x4 v0 = acc[ai][bj][m][0], v1 = acc[ai][bj][m][1];
;                         const float L2E = 1.4426950408889634f;
;                         if (isq) {
;                             const float s = 0.08838834764831845f;
;                             u32x4 o; o[0] = cvt_pk_bf16(v0[0] * s * __builtin_amdgcn_exp2f(b0[0] * L2E), v0[1] * s * __builtin_amdgcn_exp2f(b0[1] * L2E));
;                             o[1] = cvt_pk_bf16(v0[2] * s * __builtin_amdgcn_exp2f(b0[2] * L2E), v0[3] * s * __builtin_amdgcn_exp2f(b0[3] * L2E));
;                             o[2] = cvt_pk_bf16(v1[0] * s * __builtin_amdgcn_exp2f(b1[0] * L2E), v1[1] * s * __builtin_amdgcn_exp2f(b1[1] * L2E));
;                             o[3] = cvt_pk_bf16(v1[2] * s * __builtin_amdgcn_exp2f(b1[2] * L2E), v1[3] * s * __builtin_amdgcn_exp2f(b1[3] * L2E));
;                             __builtin_nontemporal_store(o, (u32x4*)(d0 + hoff));
;                         } else {
;                             u32x4 o;
;                             o[0] = cvt_pk_bf16(v0[0] * __builtin_amdgcn_exp2f(-b0[0] * L2E), v0[1] * __builtin_amdgcn_exp2f(-b0[1] * L2E));
;                             o[1] = cvt_pk_bf16(v0[2] * __builtin_amdgcn_exp2f(-b0[2] * L2E), v0[3] * __builtin_amdgcn_exp2f(-b0[3] * L2E));
;                             o[2] = cvt_pk_bf16(v1[0] * __builtin_amdgcn_exp2f(-b1[0] * L2E), v1[1] * __builtin_amdgcn_exp2f(-b1[1] * L2E));
;                             o[3] = cvt_pk_bf16(v1[2] * __builtin_amdgcn_exp2f(-b1[2] * L2E), v1[3] * __builtin_amdgcn_exp2f(-b1[3] * L2E));
;                             __builtin_nontemporal_store(o, (u32x4*)(d0 + hoff));
.LBB0_1438:
	v_mul_f32_e32 v128, s33, v131
	v_exp_f32_e32 v130, v128
	v_mov_b32_e32 v151, v169
	v_mov_b32_e32 v149, v169
	v_lshl_add_u64 v[128:129], s[42:43], 0, v[150:151]
	v_mul_f32_e32 v130, v155, v130
	v_cvt_pk_bf16_f32 v147, v154, v130
	v_lshl_add_u64 v[128:129], v[128:129], 0, v[148:149]
	global_store_dwordx4 v[128:129], v[144:147], off nt
	global_load_dwordx4 v[128:131], v[152:153], off offset:528
	s_nop 0
	global_load_dwordx4 v[136:139], v[152:153], off offset:512
	s_and_b64 vcc, exec, s[8:9]
	s_mov_b64 s[48:49], -1
	s_cbranch_vccnz .LBB0_1440
	s_waitcnt vmcnt(3)
	v_mul_f32_e32 v144, 0xbfb8aa3b, v140
	v_mul_f32_e32 v145, 0xbfb8aa3b, v141
	v_exp_f32_e32 v144, v144
	v_exp_f32_e32 v145, v145
	v_mul_f32_e32 v146, 0xbfb8aa3b, v142
	v_mul_f32_e32 v147, 0xbfb8aa3b, v143
	v_exp_f32_e32 v146, v146
	v_pk_mul_f32 v[144:145], v[76:77], v[144:145]
	v_exp_f32_e32 v147, v147
	v_cvt_pk_bf16_f32 v144, v144, v145
	v_mul_f32_e32 v145, 0xbfb8aa3b, v132
	v_exp_f32_e32 v150, v145
	v_mul_f32_e32 v145, 0xbfb8aa3b, v133
	v_exp_f32_e32 v151, v145
	v_mul_f32_e32 v145, 0xbfb8aa3b, v134
	v_exp_f32_e32 v149, v145
	v_pk_mul_f32 v[146:147], v[78:79], v[146:147]
	s_mov_b64 s[48:49], 0
	v_cvt_pk_bf16_f32 v145, v146, v147
	v_pk_mul_f32 v[146:147], v[72:73], v[150:151]
	v_mul_f32_e32 v150, v74, v149
	v_cvt_pk_bf16_f32 v146, v146, v147
	v_mov_b32_e32 v151, v75
.LBB0_1440:
	s_andn2_b64 vcc, exec, s[48:49]
	s_mov_b32 s33, 0xbfb8aa3b
	s_cbranch_vccnz .LBB0_1442
	s_waitcnt vmcnt(3)
	v_mul_f32_e32 v140, 0x3fb8aa3b, v140
	v_mul_f32_e32 v141, 0x3fb8aa3b, v141
	v_exp_f32_e32 v140, v140
	v_exp_f32_e32 v141, v141
	v_pk_mul_f32 v[144:145], v[76:77], s[34:35] op_sel_hi:[1,0]
	v_mul_f32_e32 v132, 0x3fb8aa3b, v132
	v_mul_f32_e32 v133, 0x3fb8aa3b, v133
	v_pk_mul_f32 v[140:141], v[144:145], v[140:141]
	v_exp_f32_e32 v132, v132
	v_cvt_pk_bf16_f32 v144, v140, v141
	v_mul_f32_e32 v140, 0x3fb8aa3b, v142
	v_mul_f32_e32 v141, 0x3fb8aa3b, v143
	v_exp_f32_e32 v140, v140
	v_exp_f32_e32 v141, v141
	v_exp_f32_e32 v133, v133
	v_pk_mul_f32 v[142:143], v[78:79], s[34:35] op_sel_hi:[1,0]
	v_mul_f32_e32 v134, 0x3fb8aa3b, v134
	v_pk_mul_f32 v[140:141], v[142:143], v[140:141]
	v_exp_f32_e32 v190, v134
	v_cvt_pk_bf16_f32 v145, v140, v141
	v_pk_mul_f32 v[140:141], v[72:73], s[34:35] op_sel_hi:[1,0]
	s_mov_b32 s33, 0x3fb8aa3b
	v_pk_mul_f32 v[132:133], v[140:141], v[132:133]
	s_nop 0
	v_cvt_pk_bf16_f32 v146, v132, v133
	v_mul_f32_e32 v132, 0x3db504f3, v74
	v_mov_b32_e32 v133, v75
	v_pk_mul_f32 v[150:151], v[132:133], v[190:191]
.LBB0_1442:
	s_waitcnt vmcnt(3)
	v_mul_f32_e32 v132, s33, v135
	v_exp_f32_e32 v132, v132
	v_or_b32_e32 v133, 0x1800, v156
	v_mov_b32_e32 v153, v169
	v_lshlrev_b32_e32 v152, 1, v133
	v_mul_f32_e32 v132, v151, v132
	v_cvt_pk_bf16_f32 v147, v150, v132
	v_lshl_add_u64 v[132:133], s[10:11], 0, v[152:153]
	v_mov_b32_e32 v149, v169
	v_add_u32_e32 v150, 0x80, v192
	v_lshl_add_u64 v[132:133], v[132:133], 0, v[148:149]
	v_ashrrev_i32_e32 v151, 31, v150
	global_store_dwordx4 v[132:133], v[144:147], off nt
	v_lshlrev_b64 v[132:133], 11, v[150:151]
	v_lshl_add_u64 v[132:133], s[22:23], 0, v[132:133]
	v_lshl_add_u64 v[154:155], v[168:169], 2, v[132:133]
	global_load_dwordx4 v[132:135], v[154:155], off offset:16
	global_load_dwordx4 v[140:143], v[154:155], off
	s_waitcnt vmcnt(3)
	s_and_b64 vcc, exec, s[8:9]
	s_mov_b64 s[10:11], -1
	s_cbranch_vccnz .LBB0_1444
	v_mul_f32_e32 v144, 0xbfb8aa3b, v136
	v_mul_f32_e32 v145, 0xbfb8aa3b, v137
	v_exp_f32_e32 v144, v144
	v_exp_f32_e32 v145, v145
	v_mul_f32_e32 v146, 0xbfb8aa3b, v138
	v_mul_f32_e32 v147, 0xbfb8aa3b, v139
	v_exp_f32_e32 v146, v146
	v_pk_mul_f32 v[144:145], v[68:69], v[144:145]
	v_exp_f32_e32 v147, v147
	v_cvt_pk_bf16_f32 v144, v144, v145
	v_mul_f32_e32 v145, 0xbfb8aa3b, v128
	v_exp_f32_e32 v156, v145
	v_mul_f32_e32 v145, 0xbfb8aa3b, v129
	v_exp_f32_e32 v157, v145
	v_mul_f32_e32 v145, 0xbfb8aa3b, v130
	v_exp_f32_e32 v149, v145
	v_pk_mul_f32 v[146:147], v[70:71], v[146:147]
	s_mov_b64 s[10:11], 0
	v_cvt_pk_bf16_f32 v145, v146, v147
	v_pk_mul_f32 v[146:147], v[64:65], v[156:157]
	v_mul_f32_e32 v156, v66, v149
	v_cvt_pk_bf16_f32 v146, v146, v147
	v_mov_b32_e32 v157, v67

;     __device__ __forceinline__ void operator()(const f32x4 (&acc)[2][2][4][2], const Unit& u, int wr, int wc, int fr, int fq) const {
;     ...
;             BC_LOAD(0, 0);
; #pragma unroll
;             for (int g = 0; g < 16; ++g) {
;                 const int ai = g >> 3, m = (g >> 1) & 3, bj = g & 1;
;                 const int r = row0 + ai * HALF + m * 16;
;                 if (g + 1 < 16) BC_LOAD((g + 1) & 1, g + 1);
;                 {
;                     {
;                         const int col = cb + bj * HALF + lc;
;                         const size_t hoff = ((size_t)((r >> 11) * 4 + (col >> 7)) * SEQ + (r & (SEQ - 1))) * 128 + (col & 127);
;                         const f32x4 b0 = bc[g & 1][0], b1 = bc[g & 1][1];
;                         const f32x4 v0 = acc[ai][bj][m][0], v1 = acc[ai][bj][m][1];
;                         const float L2E = 1.4426950408889634f;
;                         if (isq) {
;                             const float s = 0.08838834764831845f;
;                             u32x4 o; o[0] = cvt_pk_bf16(v0[0] * s * __builtin_amdgcn_exp2f(b0[0] * L2E), v0[1] * s * __builtin_amdgcn_exp2f(b0[1] * L2E));
;                             o[1] = cvt_pk_bf16(v0[2] * s * __builtin_amdgcn_exp2f(b0[2] * L2E), v0[3] * s * __builtin_amdgcn_exp2f(b0[3] * L2E));
;                             o[2] = cvt_pk_bf16(v1[0] * s * __builtin_amdgcn_exp2f(b1[0] * L2E), v1[1] * s * __builtin_amdgcn_exp2f(b1[1] * L2E));
;                             o[3] = cvt_pk_bf16(v1[2] * s * __builtin_amdgcn_exp2f(b1[2] * L2E), v1[3] * s * __builtin_amdgcn_exp2f(b1[3] * L2E));
;                             __builtin_nontemporal_store(o, (u32x4*)(d0 + hoff));
;                         } else {
;                             u32x4 o;
;                             o[0] = cvt_pk_bf16(v0[0] * __builtin_amdgcn_exp2f(-b0[0] * L2E), v0[1] * __builtin_amdgcn_exp2f(-b0[1] * L2E));
;                             o[1] = cvt_pk_bf16(v0[2] * __builtin_amdgcn_exp2f(-b0[2] * L2E), v0[3] * __builtin_amdgcn_exp2f(-b0[3] * L2E));
;                             o[2] = cvt_pk_bf16(v1[0] * __builtin_amdgcn_exp2f(-b1[0] * L2E), v1[1] * __builtin_amdgcn_exp2f(-b1[1] * L2E));
;                             o[3] = cvt_pk_bf16(v1[2] * __builtin_amdgcn_exp2f(-b1[2] * L2E), v1[3] * __builtin_amdgcn_exp2f(-b1[3] * L2E));
;                             __builtin_nontemporal_store(o, (u32x4*)(d0 + hoff));
.LBB0_1446:
	v_mul_f32_e32 v128, s10, v131
	v_exp_f32_e32 v130, v128
	v_mov_b32_e32 v153, v169
	v_mov_b32_e32 v149, v169
	v_lshl_add_u64 v[128:129], s[42:43], 0, v[152:153]
	v_mul_f32_e32 v130, v157, v130
	v_cvt_pk_bf16_f32 v147, v156, v130
	v_lshl_add_u64 v[128:129], v[128:129], 0, v[148:149]
	global_store_dwordx4 v[128:129], v[144:147], off nt
	global_load_dwordx4 v[128:131], v[154:155], off offset:528
	s_nop 0
	global_load_dwordx4 v[136:139], v[154:155], off offset:512
	s_and_b64 vcc, exec, s[8:9]
	s_mov_b64 s[10:11], -1
	s_cbranch_vccnz .LBB0_1448
	s_waitcnt vmcnt(3)
	v_mul_f32_e32 v144, 0xbfb8aa3b, v140
	v_mul_f32_e32 v145, 0xbfb8aa3b, v141
	v_exp_f32_e32 v144, v144
	v_exp_f32_e32 v145, v145
	v_mul_f32_e32 v146, 0xbfb8aa3b, v142
	v_mul_f32_e32 v147, 0xbfb8aa3b, v143
	v_exp_f32_e32 v146, v146
	v_pk_mul_f32 v[144:145], v[60:61], v[144:145]
	v_exp_f32_e32 v147, v147
	v_cvt_pk_bf16_f32 v144, v144, v145
	v_mul_f32_e32 v145, 0xbfb8aa3b, v132
	v_exp_f32_e32 v152, v145
	v_mul_f32_e32 v145, 0xbfb8aa3b, v133
	v_exp_f32_e32 v153, v145
	v_mul_f32_e32 v145, 0xbfb8aa3b, v134
	v_exp_f32_e32 v149, v145
	v_pk_mul_f32 v[146:147], v[62:63], v[146:147]
	s_mov_b64 s[10:11], 0
	v_cvt_pk_bf16_f32 v145, v146, v147
	v_pk_mul_f32 v[146:147], v[56:57], v[152:153]
	v_mul_f32_e32 v152, v58, v149
	v_cvt_pk_bf16_f32 v146, v146, v147
	v_mov_b32_e32 v153, v59
.LBB0_1448:
	s_andn2_b64 vcc, exec, s[10:11]
	s_mov_b32 s10, 0xbfb8aa3b
	s_cbranch_vccnz .LBB0_1450
	s_waitcnt vmcnt(3)
	v_mul_f32_e32 v140, 0x3fb8aa3b, v140
	v_mul_f32_e32 v141, 0x3fb8aa3b, v141
	v_exp_f32_e32 v140, v140
	v_exp_f32_e32 v141, v141
	v_pk_mul_f32 v[144:145], v[60:61], s[34:35] op_sel_hi:[1,0]
	v_mul_f32_e32 v132, 0x3fb8aa3b, v132
	v_mul_f32_e32 v133, 0x3fb8aa3b, v133
	v_pk_mul_f32 v[140:141], v[144:145], v[140:141]
	v_exp_f32_e32 v132, v132
	v_cvt_pk_bf16_f32 v144, v140, v141
	v_mul_f32_e32 v140, 0x3fb8aa3b, v142
	v_mul_f32_e32 v141, 0x3fb8aa3b, v143
	v_exp_f32_e32 v140, v140
	v_exp_f32_e32 v141, v141
	v_exp_f32_e32 v133, v133
	v_pk_mul_f32 v[142:143], v[62:63], s[34:35] op_sel_hi:[1,0]
	v_mul_f32_e32 v134, 0x3fb8aa3b, v134
	v_pk_mul_f32 v[140:141], v[142:143], v[140:141]
	v_exp_f32_e32 v190, v134
	v_cvt_pk_bf16_f32 v145, v140, v141
	v_pk_mul_f32 v[140:141], v[56:57], s[34:35] op_sel_hi:[1,0]
	s_mov_b32 s10, 0x3fb8aa3b
	v_pk_mul_f32 v[132:133], v[140:141], v[132:133]
	s_nop 0
	v_cvt_pk_bf16_f32 v146, v132, v133
	v_mul_f32_e32 v132, 0x3db504f3, v58
	v_mov_b32_e32 v133, v59
	v_pk_mul_f32 v[152:153], v[132:133], v[190:191]
.LBB0_1450:
	s_waitcnt vmcnt(3)
	v_mul_f32_e32 v133, s10, v135
	v_ashrrev_i32_e32 v132, 9, v150
	v_exp_f32_e32 v134, v133
	v_and_b32_e32 v151, -4, v132
	v_add_u32_e32 v132, s17, v151
	v_ashrrev_i32_e32 v133, 31, v132
	v_lshlrev_b32_e32 v135, 7, v150
	v_and_b32_e32 v193, 0x3e780, v135
	v_mul_f32_e32 v134, v153, v134
	v_lshlrev_b64 v[132:133], 19, v[132:133]
	v_cvt_pk_bf16_f32 v147, v152, v134
	v_lshl_add_u64 v[152:153], s[2:3], 0, v[132:133]
	v_lshlrev_b32_e32 v156, 1, v193
	v_mov_b32_e32 v157, v169
	v_lshl_add_u64 v[132:133], v[152:153], 0, v[156:157]
	v_mov_b32_e32 v149, v169
	v_lshl_add_u64 v[132:133], v[132:133], 0, v[148:149]
	global_store_dwordx4 v[132:133], v[144:147], off nt
	v_or_b32_e32 v132, 16, v150
	v_ashrrev_i32_e32 v133, 31, v132
	v_lshlrev_b64 v[132:133], 11, v[132:133]
	v_lshl_add_u64 v[132:133], s[22:23], 0, v[132:133]
	v_lshl_add_u64 v[158:159], v[168:169], 2, v[132:133]
	global_load_dwordx4 v[132:135], v[158:159], off offset:16
	global_load_dwordx4 v[140:143], v[158:159], off
	s_waitcnt vmcnt(3)
	s_and_b64 vcc, exec, s[8:9]
	s_mov_b64 s[10:11], -1
	s_cbranch_vccnz .LBB0_1452
	v_mul_f32_e32 v144, 0xbfb8aa3b, v136
	v_mul_f32_e32 v145, 0xbfb8aa3b, v137
	v_exp_f32_e32 v144, v144
	v_exp_f32_e32 v145, v145
	v_mul_f32_e32 v146, 0xbfb8aa3b, v138
	v_mul_f32_e32 v147, 0xbfb8aa3b, v139
	v_exp_f32_e32 v146, v146
	v_pk_mul_f32 v[144:145], v[52:53], v[144:145]
	v_exp_f32_e32 v147, v147
	v_cvt_pk_bf16_f32 v144, v144, v145
	v_mul_f32_e32 v145, 0xbfb8aa3b, v128
	v_exp_f32_e32 v154, v145
	v_mul_f32_e32 v145, 0xbfb8aa3b, v129
	v_exp_f32_e32 v155, v145
	v_mul_f32_e32 v145, 0xbfb8aa3b, v130
	v_exp_f32_e32 v149, v145
	v_pk_mul_f32 v[146:147], v[54:55], v[146:147]
	s_mov_b64 s[10:11], 0
	v_cvt_pk_bf16_f32 v145, v146, v147
	v_pk_mul_f32 v[146:147], v[48:49], v[154:155]
	v_mul_f32_e32 v154, v50, v149
	v_cvt_pk_bf16_f32 v146, v146, v147
	v_mov_b32_e32 v155, v51

;     __device__ __forceinline__ void operator()(const f32x4 (&acc)[2][2][4][2], const Unit& u, int wr, int wc, int fr, int fq) const {
;     ...
;             BC_LOAD(0, 0);
; #pragma unroll
;             for (int g = 0; g < 16; ++g) {
;                 const int ai = g >> 3, m = (g >> 1) & 3, bj = g & 1;
;                 const int r = row0 + ai * HALF + m * 16;
;                 if (g + 1 < 16) BC_LOAD((g + 1) & 1, g + 1);
;                 {
;                     {
;                         const int col = cb + bj * HALF + lc;
;                         const size_t hoff = ((size_t)((r >> 11) * 4 + (col >> 7)) * SEQ + (r & (SEQ - 1))) * 128 + (col & 127);
;                         const f32x4 b0 = bc[g & 1][0], b1 = bc[g & 1][1];
;                         const f32x4 v0 = acc[ai][bj][m][0], v1 = acc[ai][bj][m][1];
;                         const float L2E = 1.4426950408889634f;
;                         if (isq) {
;                             const float s = 0.08838834764831845f;
;                             u32x4 o; o[0] = cvt_pk_bf16(v0[0] * s * __builtin_amdgcn_exp2f(b0[0] * L2E), v0[1] * s * __builtin_amdgcn_exp2f(b0[1] * L2E));
;                             o[1] = cvt_pk_bf16(v0[2] * s * __builtin_amdgcn_exp2f(b0[2] * L2E), v0[3] * s * __builtin_amdgcn_exp2f(b0[3] * L2E));
;                             o[2] = cvt_pk_bf16(v1[0] * s * __builtin_amdgcn_exp2f(b1[0] * L2E), v1[1] * s * __builtin_amdgcn_exp2f(b1[1] * L2E));
;                             o[3] = cvt_pk_bf16(v1[2] * s * __builtin_amdgcn_exp2f(b1[2] * L2E), v1[3] * s * __builtin_amdgcn_exp2f(b1[3] * L2E));
;                             __builtin_nontemporal_store(o, (u32x4*)(d0 + hoff));
;                         } else {
;                             u32x4 o;
;                             o[0] = cvt_pk_bf16(v0[0] * __builtin_amdgcn_exp2f(-b0[0] * L2E), v0[1] * __builtin_amdgcn_exp2f(-b0[1] * L2E));
;                             o[1] = cvt_pk_bf16(v0[2] * __builtin_amdgcn_exp2f(-b0[2] * L2E), v0[3] * __builtin_amdgcn_exp2f(-b0[3] * L2E));
;                             o[2] = cvt_pk_bf16(v1[0] * __builtin_amdgcn_exp2f(-b1[0] * L2E), v1[1] * __builtin_amdgcn_exp2f(-b1[1] * L2E));
;                             o[3] = cvt_pk_bf16(v1[2] * __builtin_amdgcn_exp2f(-b1[2] * L2E), v1[3] * __builtin_amdgcn_exp2f(-b1[3] * L2E));
;                             __builtin_nontemporal_store(o, (u32x4*)(d0 + hoff));
.LBB0_1454:
	v_mul_f32_e32 v128, s10, v131
	v_exp_f32_e32 v130, v128
	v_add_u32_e32 v128, s18, v151
	v_ashrrev_i32_e32 v129, 31, v128
	v_lshlrev_b64 v[128:129], 19, v[128:129]
	v_mul_f32_e32 v130, v155, v130
	v_cvt_pk_bf16_f32 v147, v154, v130
	v_lshl_add_u64 v[154:155], s[2:3], 0, v[128:129]
	v_mov_b32_e32 v157, v169
	v_lshl_add_u64 v[128:129], v[154:155], 0, v[156:157]
	v_mov_b32_e32 v149, v169
	v_lshl_add_u64 v[128:129], v[128:129], 0, v[148:149]
	global_store_dwordx4 v[128:129], v[144:147], off nt
	global_load_dwordx4 v[128:131], v[158:159], off offset:528
	s_nop 0
	global_load_dwordx4 v[136:139], v[158:159], off offset:512
	s_and_b64 vcc, exec, s[8:9]
	s_mov_b64 s[2:3], -1
	s_cbranch_vccnz .LBB0_1456
	s_waitcnt vmcnt(3)
	v_mul_f32_e32 v144, 0xbfb8aa3b, v140
	v_mul_f32_e32 v145, 0xbfb8aa3b, v141
	v_exp_f32_e32 v144, v144
	v_exp_f32_e32 v145, v145
	v_mul_f32_e32 v146, 0xbfb8aa3b, v142
	v_mul_f32_e32 v147, 0xbfb8aa3b, v143
	v_exp_f32_e32 v146, v146
	v_pk_mul_f32 v[144:145], v[44:45], v[144:145]
	v_exp_f32_e32 v147, v147
	v_cvt_pk_bf16_f32 v144, v144, v145
	v_mul_f32_e32 v145, 0xbfb8aa3b, v132
	v_exp_f32_e32 v156, v145
	v_mul_f32_e32 v145, 0xbfb8aa3b, v133
	v_exp_f32_e32 v157, v145
	v_mul_f32_e32 v145, 0xbfb8aa3b, v134
	v_exp_f32_e32 v149, v145
	v_pk_mul_f32 v[146:147], v[46:47], v[146:147]
	s_mov_b64 s[2:3], 0
	v_cvt_pk_bf16_f32 v145, v146, v147
	v_pk_mul_f32 v[146:147], v[40:41], v[156:157]
	v_mul_f32_e32 v158, v42, v149
	v_cvt_pk_bf16_f32 v146, v146, v147
	v_mov_b32_e32 v159, v43

;     __device__ __forceinline__ void operator()(const f32x4 (&acc)[2][2][4][2], const Unit& u, int wr, int wc, int fr, int fq) const {
;     ...
;             BC_LOAD(0, 0);
; #pragma unroll
;             for (int g = 0; g < 16; ++g) {
;                 const int ai = g >> 3, m = (g >> 1) & 3, bj = g & 1;
;                 const int r = row0 + ai * HALF + m * 16;
;                 if (g + 1 < 16) BC_LOAD((g + 1) & 1, g + 1);
;                 {
;                     {
;                         const int col = cb + bj * HALF + lc;
;                         const size_t hoff = ((size_t)((r >> 11) * 4 + (col >> 7)) * SEQ + (r & (SEQ - 1))) * 128 + (col & 127);
;                         const f32x4 b0 = bc[g & 1][0], b1 = bc[g & 1][1];
;                         const f32x4 v0 = acc[ai][bj][m][0], v1 = acc[ai][bj][m][1];
;                         const float L2E = 1.4426950408889634f;
;                         if (isq) {
;                             const float s = 0.08838834764831845f;
;                             u32x4 o; o[0] = cvt_pk_bf16(v0[0] * s * __builtin_amdgcn_exp2f(b0[0] * L2E), v0[1] * s * __builtin_amdgcn_exp2f(b0[1] * L2E));
;                             o[1] = cvt_pk_bf16(v0[2] * s * __builtin_amdgcn_exp2f(b0[2] * L2E), v0[3] * s * __builtin_amdgcn_exp2f(b0[3] * L2E));
;                             o[2] = cvt_pk_bf16(v1[0] * s * __builtin_amdgcn_exp2f(b1[0] * L2E), v1[1] * s * __builtin_amdgcn_exp2f(b1[1] * L2E));
;                             o[3] = cvt_pk_bf16(v1[2] * s * __builtin_amdgcn_exp2f(b1[2] * L2E), v1[3] * s * __builtin_amdgcn_exp2f(b1[3] * L2E));
;                             __builtin_nontemporal_store(o, (u32x4*)(d0 + hoff));
;                         } else {
;                             u32x4 o;
;                             o[0] = cvt_pk_bf16(v0[0] * __builtin_amdgcn_exp2f(-b0[0] * L2E), v0[1] * __builtin_amdgcn_exp2f(-b0[1] * L2E));
;                             o[1] = cvt_pk_bf16(v0[2] * __builtin_amdgcn_exp2f(-b0[2] * L2E), v0[3] * __builtin_amdgcn_exp2f(-b0[3] * L2E));
;                             o[2] = cvt_pk_bf16(v1[0] * __builtin_amdgcn_exp2f(-b1[0] * L2E), v1[1] * __builtin_amdgcn_exp2f(-b1[1] * L2E));
;                             o[3] = cvt_pk_bf16(v1[2] * __builtin_amdgcn_exp2f(-b1[2] * L2E), v1[3] * __builtin_amdgcn_exp2f(-b1[3] * L2E));
;                             __builtin_nontemporal_store(o, (u32x4*)(d0 + hoff));
.LBB0_1458:
	s_waitcnt vmcnt(3)
	v_mul_f32_e32 v132, s2, v135
	v_exp_f32_e32 v132, v132
	v_or_b32_e32 v133, 0x800, v193
	v_mov_b32_e32 v157, v169
	v_lshlrev_b32_e32 v156, 1, v133
	v_mul_f32_e32 v132, v159, v132
	v_cvt_pk_bf16_f32 v147, v158, v132
	v_lshl_add_u64 v[132:133], v[152:153], 0, v[156:157]
	v_mov_b32_e32 v149, v169
	v_lshl_add_u64 v[132:133], v[132:133], 0, v[148:149]
	global_store_dwordx4 v[132:133], v[144:147], off nt
	v_or_b32_e32 v132, 32, v150
	v_ashrrev_i32_e32 v133, 31, v132
	v_lshlrev_b64 v[132:133], 11, v[132:133]
	v_lshl_add_u64 v[132:133], s[22:23], 0, v[132:133]
	v_lshl_add_u64 v[158:159], v[168:169], 2, v[132:133]
	global_load_dwordx4 v[132:135], v[158:159], off offset:16
	global_load_dwordx4 v[140:143], v[158:159], off
	s_waitcnt vmcnt(3)
	s_and_b64 vcc, exec, s[8:9]
	s_mov_b64 s[2:3], -1
	s_cbranch_vccnz .LBB0_1460
	v_mul_f32_e32 v144, 0xbfb8aa3b, v136
	v_mul_f32_e32 v145, 0xbfb8aa3b, v137
	v_exp_f32_e32 v144, v144
	v_exp_f32_e32 v145, v145
	v_mul_f32_e32 v146, 0xbfb8aa3b, v138
	v_mul_f32_e32 v147, 0xbfb8aa3b, v139
	v_exp_f32_e32 v146, v146
	v_pk_mul_f32 v[144:145], v[36:37], v[144:145]
	v_exp_f32_e32 v147, v147
	v_cvt_pk_bf16_f32 v144, v144, v145
	v_mul_f32_e32 v145, 0xbfb8aa3b, v128
	v_exp_f32_e32 v194, v145
	v_mul_f32_e32 v145, 0xbfb8aa3b, v129
	v_exp_f32_e32 v195, v145
	v_mul_f32_e32 v145, 0xbfb8aa3b, v130
	v_exp_f32_e32 v149, v145
	v_pk_mul_f32 v[146:147], v[38:39], v[146:147]
	s_mov_b64 s[2:3], 0
	v_cvt_pk_bf16_f32 v145, v146, v147
	v_pk_mul_f32 v[146:147], v[32:33], v[194:195]
	v_mul_f32_e32 v194, v34, v149
	v_cvt_pk_bf16_f32 v146, v146, v147
	v_mov_b32_e32 v195, v35

;     __device__ __forceinline__ void operator()(const f32x4 (&acc)[2][2][4][2], const Unit& u, int wr, int wc, int fr, int fq) const {
;     ...
;             BC_LOAD(0, 0);
; #pragma unroll
;             for (int g = 0; g < 16; ++g) {
;                 const int ai = g >> 3, m = (g >> 1) & 3, bj = g & 1;
;                 const int r = row0 + ai * HALF + m * 16;
;                 if (g + 1 < 16) BC_LOAD((g + 1) & 1, g + 1);
;                 {
;                     {
;                         const int col = cb + bj * HALF + lc;
;                         const size_t hoff = ((size_t)((r >> 11) * 4 + (col >> 7)) * SEQ + (r & (SEQ - 1))) * 128 + (col & 127);
;                         const f32x4 b0 = bc[g & 1][0], b1 = bc[g & 1][1];
;                         const f32x4 v0 = acc[ai][bj][m][0], v1 = acc[ai][bj][m][1];
;                         const float L2E = 1.4426950408889634f;
;                         if (isq) {
;                             const float s = 0.08838834764831845f;
;                             u32x4 o; o[0] = cvt_pk_bf16(v0[0] * s * __builtin_amdgcn_exp2f(b0[0] * L2E), v0[1] * s * __builtin_amdgcn_exp2f(b0[1] * L2E));
;                             o[1] = cvt_pk_bf16(v0[2] * s * __builtin_amdgcn_exp2f(b0[2] * L2E), v0[3] * s * __builtin_amdgcn_exp2f(b0[3] * L2E));
;                             o[2] = cvt_pk_bf16(v1[0] * s * __builtin_amdgcn_exp2f(b1[0] * L2E), v1[1] * s * __builtin_amdgcn_exp2f(b1[1] * L2E));
;                             o[3] = cvt_pk_bf16(v1[2] * s * __builtin_amdgcn_exp2f(b1[2] * L2E), v1[3] * s * __builtin_amdgcn_exp2f(b1[3] * L2E));
;                             __builtin_nontemporal_store(o, (u32x4*)(d0 + hoff));
;                         } else {
;                             u32x4 o;
;                             o[0] = cvt_pk_bf16(v0[0] * __builtin_amdgcn_exp2f(-b0[0] * L2E), v0[1] * __builtin_amdgcn_exp2f(-b0[1] * L2E));
;                             o[1] = cvt_pk_bf16(v0[2] * __builtin_amdgcn_exp2f(-b0[2] * L2E), v0[3] * __builtin_amdgcn_exp2f(-b0[3] * L2E));
;                             o[2] = cvt_pk_bf16(v1[0] * __builtin_amdgcn_exp2f(-b1[0] * L2E), v1[1] * __builtin_amdgcn_exp2f(-b1[1] * L2E));
;                             o[3] = cvt_pk_bf16(v1[2] * __builtin_amdgcn_exp2f(-b1[2] * L2E), v1[3] * __builtin_amdgcn_exp2f(-b1[3] * L2E));
;                             __builtin_nontemporal_store(o, (u32x4*)(d0 + hoff));
.LBB0_1462:
	v_mul_f32_e32 v128, s2, v131
	v_exp_f32_e32 v130, v128
	v_mov_b32_e32 v157, v169
	v_mov_b32_e32 v149, v169
	v_lshl_add_u64 v[128:129], v[154:155], 0, v[156:157]
	v_mul_f32_e32 v130, v195, v130
	v_cvt_pk_bf16_f32 v147, v194, v130
	v_lshl_add_u64 v[128:129], v[128:129], 0, v[148:149]
	global_store_dwordx4 v[128:129], v[144:147], off nt
	global_load_dwordx4 v[128:131], v[158:159], off offset:528
	s_nop 0
	global_load_dwordx4 v[136:139], v[158:159], off offset:512
	s_and_b64 vcc, exec, s[8:9]
	s_mov_b64 s[2:3], -1
	s_cbranch_vccnz .LBB0_1464
	s_waitcnt vmcnt(3)
	v_mul_f32_e32 v144, 0xbfb8aa3b, v140
	v_mul_f32_e32 v145, 0xbfb8aa3b, v141
	v_exp_f32_e32 v144, v144
	v_exp_f32_e32 v145, v145
	v_mul_f32_e32 v146, 0xbfb8aa3b, v142
	v_mul_f32_e32 v147, 0xbfb8aa3b, v143
	v_exp_f32_e32 v146, v146
	v_pk_mul_f32 v[144:145], v[28:29], v[144:145]
	v_exp_f32_e32 v147, v147
	v_cvt_pk_bf16_f32 v144, v144, v145
	v_mul_f32_e32 v145, 0xbfb8aa3b, v132
	v_exp_f32_e32 v156, v145
	v_mul_f32_e32 v145, 0xbfb8aa3b, v133
	v_exp_f32_e32 v157, v145
	v_mul_f32_e32 v145, 0xbfb8aa3b, v134
	v_exp_f32_e32 v149, v145
	v_pk_mul_f32 v[146:147], v[30:31], v[146:147]
	s_mov_b64 s[2:3], 0
	v_cvt_pk_bf16_f32 v145, v146, v147
	v_pk_mul_f32 v[146:147], v[24:25], v[156:157]
	v_mul_f32_e32 v158, v26, v149
	v_cvt_pk_bf16_f32 v146, v146, v147
	v_mov_b32_e32 v159, v27

;     __device__ __forceinline__ void operator()(const f32x4 (&acc)[2][2][4][2], const Unit& u, int wr, int wc, int fr, int fq) const {
;     ...
;             BC_LOAD(0, 0);
; #pragma unroll
;             for (int g = 0; g < 16; ++g) {
;                 const int ai = g >> 3, m = (g >> 1) & 3, bj = g & 1;
;                 const int r = row0 + ai * HALF + m * 16;
;                 if (g + 1 < 16) BC_LOAD((g + 1) & 1, g + 1);
;                 {
;                     {
;                         const int col = cb + bj * HALF + lc;
;                         const size_t hoff = ((size_t)((r >> 11) * 4 + (col >> 7)) * SEQ + (r & (SEQ - 1))) * 128 + (col & 127);
;                         const f32x4 b0 = bc[g & 1][0], b1 = bc[g & 1][1];
;                         const f32x4 v0 = acc[ai][bj][m][0], v1 = acc[ai][bj][m][1];
;                         const float L2E = 1.4426950408889634f;
;                         if (isq) {
;                             const float s = 0.08838834764831845f;
;                             u32x4 o; o[0] = cvt_pk_bf16(v0[0] * s * __builtin_amdgcn_exp2f(b0[0] * L2E), v0[1] * s * __builtin_amdgcn_exp2f(b0[1] * L2E));
;                             o[1] = cvt_pk_bf16(v0[2] * s * __builtin_amdgcn_exp2f(b0[2] * L2E), v0[3] * s * __builtin_amdgcn_exp2f(b0[3] * L2E));
;                             o[2] = cvt_pk_bf16(v1[0] * s * __builtin_amdgcn_exp2f(b1[0] * L2E), v1[1] * s * __builtin_amdgcn_exp2f(b1[1] * L2E));
;                             o[3] = cvt_pk_bf16(v1[2] * s * __builtin_amdgcn_exp2f(b1[2] * L2E), v1[3] * s * __builtin_amdgcn_exp2f(b1[3] * L2E));
;                             __builtin_nontemporal_store(o, (u32x4*)(d0 + hoff));
;                         } else {
;                             u32x4 o;
;                             o[0] = cvt_pk_bf16(v0[0] * __builtin_amdgcn_exp2f(-b0[0] * L2E), v0[1] * __builtin_amdgcn_exp2f(-b0[1] * L2E));
;                             o[1] = cvt_pk_bf16(v0[2] * __builtin_amdgcn_exp2f(-b0[2] * L2E), v0[3] * __builtin_amdgcn_exp2f(-b0[3] * L2E));
;                             o[2] = cvt_pk_bf16(v1[0] * __builtin_amdgcn_exp2f(-b1[0] * L2E), v1[1] * __builtin_amdgcn_exp2f(-b1[1] * L2E));
;                             o[3] = cvt_pk_bf16(v1[2] * __builtin_amdgcn_exp2f(-b1[2] * L2E), v1[3] * __builtin_amdgcn_exp2f(-b1[3] * L2E));
;                             __builtin_nontemporal_store(o, (u32x4*)(d0 + hoff));
.LBB0_1466:
	s_waitcnt vmcnt(3)
	v_mul_f32_e32 v132, s2, v135
	v_exp_f32_e32 v132, v132
	v_or_b32_e32 v133, 0x1000, v193
	v_mov_b32_e32 v157, v169
	v_lshlrev_b32_e32 v156, 1, v133
	v_mul_f32_e32 v132, v159, v132
	v_cvt_pk_bf16_f32 v147, v158, v132
	v_lshl_add_u64 v[132:133], v[152:153], 0, v[156:157]
	v_mov_b32_e32 v149, v169
	v_lshl_add_u64 v[132:133], v[132:133], 0, v[148:149]
	global_store_dwordx4 v[132:133], v[144:147], off nt
	v_or_b32_e32 v132, 48, v150
	v_ashrrev_i32_e32 v133, 31, v132
	v_lshlrev_b64 v[132:133], 11, v[132:133]
	v_lshl_add_u64 v[132:133], s[22:23], 0, v[132:133]
	v_lshl_add_u64 v[150:151], v[168:169], 2, v[132:133]
	global_load_dwordx4 v[132:135], v[150:151], off offset:16
	global_load_dwordx4 v[140:143], v[150:151], off
	s_waitcnt vmcnt(3)
	s_and_b64 vcc, exec, s[8:9]
	s_mov_b64 s[2:3], -1
	s_cbranch_vccnz .LBB0_1468
	v_mul_f32_e32 v144, 0xbfb8aa3b, v136
	v_mul_f32_e32 v145, 0xbfb8aa3b, v137
	v_exp_f32_e32 v144, v144
	v_exp_f32_e32 v145, v145
	v_mul_f32_e32 v146, 0xbfb8aa3b, v138
	v_mul_f32_e32 v147, 0xbfb8aa3b, v139
	v_exp_f32_e32 v146, v146
	v_pk_mul_f32 v[144:145], v[20:21], v[144:145]
	v_exp_f32_e32 v147, v147
	v_cvt_pk_bf16_f32 v144, v144, v145
	v_mul_f32_e32 v145, 0xbfb8aa3b, v128
	v_exp_f32_e32 v158, v145
	v_mul_f32_e32 v145, 0xbfb8aa3b, v129
	v_exp_f32_e32 v159, v145
	v_mul_f32_e32 v145, 0xbfb8aa3b, v130
	v_exp_f32_e32 v149, v145
	v_pk_mul_f32 v[146:147], v[22:23], v[146:147]
	s_mov_b64 s[2:3], 0
	v_cvt_pk_bf16_f32 v145, v146, v147
	v_pk_mul_f32 v[146:147], v[16:17], v[158:159]
	v_mul_f32_e32 v158, v18, v149
	v_cvt_pk_bf16_f32 v146, v146, v147
	v_mov_b32_e32 v159, v19

;     __device__ __forceinline__ void operator()(const f32x4 (&acc)[2][2][4][2], const Unit& u, int wr, int wc, int fr, int fq) const {
;     ...
;             BC_LOAD(0, 0);
; #pragma unroll
;             for (int g = 0; g < 16; ++g) {
;                 const int ai = g >> 3, m = (g >> 1) & 3, bj = g & 1;
;                 const int r = row0 + ai * HALF + m * 16;
;                 if (g + 1 < 16) BC_LOAD((g + 1) & 1, g + 1);
;                 {
;                     {
;                         const int col = cb + bj * HALF + lc;
;                         const size_t hoff = ((size_t)((r >> 11) * 4 + (col >> 7)) * SEQ + (r & (SEQ - 1))) * 128 + (col & 127);
;                         const f32x4 b0 = bc[g & 1][0], b1 = bc[g & 1][1];
;                         const f32x4 v0 = acc[ai][bj][m][0], v1 = acc[ai][bj][m][1];
;                         const float L2E = 1.4426950408889634f;
;                         if (isq) {
;                             const float s = 0.08838834764831845f;
;                             u32x4 o; o[0] = cvt_pk_bf16(v0[0] * s * __builtin_amdgcn_exp2f(b0[0] * L2E), v0[1] * s * __builtin_amdgcn_exp2f(b0[1] * L2E));
;                             o[1] = cvt_pk_bf16(v0[2] * s * __builtin_amdgcn_exp2f(b0[2] * L2E), v0[3] * s * __builtin_amdgcn_exp2f(b0[3] * L2E));
;                             o[2] = cvt_pk_bf16(v1[0] * s * __builtin_amdgcn_exp2f(b1[0] * L2E), v1[1] * s * __builtin_amdgcn_exp2f(b1[1] * L2E));
;                             o[3] = cvt_pk_bf16(v1[2] * s * __builtin_amdgcn_exp2f(b1[2] * L2E), v1[3] * s * __builtin_amdgcn_exp2f(b1[3] * L2E));
;                             __builtin_nontemporal_store(o, (u32x4*)(d0 + hoff));
;                         } else {
;                             u32x4 o;
;                             o[0] = cvt_pk_bf16(v0[0] * __builtin_amdgcn_exp2f(-b0[0] * L2E), v0[1] * __builtin_amdgcn_exp2f(-b0[1] * L2E));
;                             o[1] = cvt_pk_bf16(v0[2] * __builtin_amdgcn_exp2f(-b0[2] * L2E), v0[3] * __builtin_amdgcn_exp2f(-b0[3] * L2E));
;                             o[2] = cvt_pk_bf16(v1[0] * __builtin_amdgcn_exp2f(-b1[0] * L2E), v1[1] * __builtin_amdgcn_exp2f(-b1[1] * L2E));
;                             o[3] = cvt_pk_bf16(v1[2] * __builtin_amdgcn_exp2f(-b1[2] * L2E), v1[3] * __builtin_amdgcn_exp2f(-b1[3] * L2E));
;                             __builtin_nontemporal_store(o, (u32x4*)(d0 + hoff));
.LBB0_1470:
	v_mul_f32_e32 v128, s2, v131
	v_exp_f32_e32 v130, v128
	v_mov_b32_e32 v157, v169
	v_mov_b32_e32 v149, v169
	v_lshl_add_u64 v[128:129], v[154:155], 0, v[156:157]
	v_mul_f32_e32 v130, v159, v130
	v_cvt_pk_bf16_f32 v147, v158, v130
	v_lshl_add_u64 v[128:129], v[128:129], 0, v[148:149]
	global_store_dwordx4 v[128:129], v[144:147], off nt
	global_load_dwordx4 v[128:131], v[150:151], off offset:528
	s_nop 0
	global_load_dwordx4 v[136:139], v[150:151], off offset:512
	s_and_b64 vcc, exec, s[8:9]
	s_mov_b64 s[2:3], -1
	s_cbranch_vccnz .LBB0_1472
	s_waitcnt vmcnt(3)
	v_mul_f32_e32 v144, 0xbfb8aa3b, v140
	v_mul_f32_e32 v145, 0xbfb8aa3b, v141
	v_exp_f32_e32 v144, v144
	v_exp_f32_e32 v145, v145
	v_mul_f32_e32 v146, 0xbfb8aa3b, v142
	v_mul_f32_e32 v147, 0xbfb8aa3b, v143
	v_exp_f32_e32 v146, v146
	v_pk_mul_f32 v[144:145], v[12:13], v[144:145]
	v_exp_f32_e32 v147, v147
	v_cvt_pk_bf16_f32 v144, v144, v145
	v_mul_f32_e32 v145, 0xbfb8aa3b, v132
	v_exp_f32_e32 v150, v145
	v_mul_f32_e32 v145, 0xbfb8aa3b, v133
	v_exp_f32_e32 v151, v145
	v_mul_f32_e32 v145, 0xbfb8aa3b, v134
	v_exp_f32_e32 v149, v145
	v_pk_mul_f32 v[146:147], v[14:15], v[146:147]
	s_mov_b64 s[2:3], 0
	v_cvt_pk_bf16_f32 v145, v146, v147
	v_pk_mul_f32 v[146:147], v[8:9], v[150:151]
	v_mul_f32_e32 v150, v10, v149
	v_cvt_pk_bf16_f32 v146, v146, v147
	v_mov_b32_e32 v151, v11

; #define ROPE_LOAD(buf, g) do { const int _pos = (row0 + ((g) >> 2) * HALF + ((g) & 3) * 16) & (SEQ - 1); const float* _rp = rope + _pos * 32 + 8 * (fq & 1); \
;                 rc[buf][0] = *(const f32x4*)_rp; rc[buf][1] = *(const f32x4*)(_rp + 4); rc[buf][2] = *(const f32x4*)(_rp + 16); rc[buf][3] = *(const f32x4*)(_rp + 20); } while (0)
;     __device__ __forceinline__ void operator()(const f32x4 (&acc)[2][2][4][2], const Unit& u, int wr, int wc, int fr, int fq) const {
;     ...
;                 if (wc == 0 && g + 1 < 8) ROPE_LOAD((g + 1) & 1, g + 1);
; #pragma unroll
;                 for (int bj = 0; bj < 2; ++bj) {
;                     float v[8] = {acc[ai][bj][m][0][0], acc[ai][bj][m][0][1], acc[ai][bj][m][0][2], acc[ai][bj][m][0][3],
;                                   acc[ai][bj][m][1][0], acc[ai][bj][m][1][1], acc[ai][bj][m][1][2], acc[ai][bj][m][1][3]};
;                     if (wc == 0) {
;                         const f32x4 c0 = rc[g & 1][0], c1 = rc[g & 1][1], s0 = rc[g & 1][2], s1 = rc[g & 1][3];
;                         const float cs[8] = {c0[0], c0[1], c0[2], c0[3], c1[0], c1[1], c1[2], c1[3]}, sn[8] = {s0[0], s0[1], s0[2], s0[3], s1[0], s1[1], s1[2], s1[3]};
; #pragma unroll
;                         for (int i = 0; i < 8; ++i) {
;                             const float pv = __shfl_xor(v[i], 32);
;                             v[i] = (fq < 2) ? (v[i] * cs[i] - pv * sn[i]) : (v[i] * cs[i] + pv * sn[i]);
;                         }
;                     }
.LBB0_1496:
	v_and_b32_e32 v121, 64, v211
	v_xor_b32_e32 v120, 32, v211
	v_add_u32_e32 v121, 64, v121
	v_cmp_lt_i32_e32 vcc, v120, v121
	s_nop 1
	v_cndmask_b32_e32 v120, v211, v120, vcc
	v_lshlrev_b32_e32 v127, 2, v120
	ds_bpermute_b32 v120, v127, v116
	ds_bpermute_b32 v121, v127, v117
	ds_bpermute_b32 v122, v127, v118
	ds_bpermute_b32 v123, v127, v119
	ds_bpermute_b32 v124, v127, v112
	ds_bpermute_b32 v125, v127, v113
	ds_bpermute_b32 v126, v127, v114
	ds_bpermute_b32 v127, v127, v115
	s_waitcnt lgkmcnt(0)
	v_pk_mul_f32 v[120:121], v[156:157], v[120:121]
	v_pk_mul_f32 v[122:123], v[158:159], v[122:123]
	v_pk_mul_f32 v[124:125], v[152:153], v[124:125]
	v_cndmask_b32_e64 v121, v121, -v121, s[0:1]
	v_pk_mul_f32 v[126:127], v[154:155], v[126:127]
	v_cndmask_b32_e64 v120, v120, -v120, s[0:1]
	v_cndmask_b32_e64 v123, v123, -v123, s[0:1]
	v_cndmask_b32_e64 v122, v122, -v122, s[0:1]
	v_cndmask_b32_e64 v125, v125, -v125, s[0:1]
	v_cndmask_b32_e64 v124, v124, -v124, s[0:1]
	v_cndmask_b32_e64 v127, v127, -v127, s[0:1]
	v_cndmask_b32_e64 v126, v126, -v126, s[0:1]
	v_pk_fma_f32 v[114:115], v[114:115], v[150:151], v[126:127]
	v_pk_fma_f32 v[112:113], v[112:113], v[148:149], v[124:125]
	v_pk_fma_f32 v[118:119], v[118:119], v[146:147], v[122:123]
	v_pk_fma_f32 v[116:117], v[116:117], v[144:145], v[120:121]
	s_and_b64 vcc, exec, s[48:49]
	s_cbranch_vccnz .LBB0_1492

; #define ROPE_LOAD(buf, g) do { const int _pos = (row0 + ((g) >> 2) * HALF + ((g) & 3) * 16) & (SEQ - 1); const float* _rp = rope + _pos * 32 + 8 * (fq & 1); \
;                 rc[buf][0] = *(const f32x4*)_rp; rc[buf][1] = *(const f32x4*)(_rp + 4); rc[buf][2] = *(const f32x4*)(_rp + 16); rc[buf][3] = *(const f32x4*)(_rp + 20); } while (0)
;     __device__ __forceinline__ void operator()(const f32x4 (&acc)[2][2][4][2], const Unit& u, int wr, int wc, int fr, int fq) const {
;     ...
;                 if (wc == 0 && g + 1 < 8) ROPE_LOAD((g + 1) & 1, g + 1);
; #pragma unroll
;                 for (int bj = 0; bj < 2; ++bj) {
;                     float v[8] = {acc[ai][bj][m][0][0], acc[ai][bj][m][0][1], acc[ai][bj][m][0][2], acc[ai][bj][m][0][3],
;                                   acc[ai][bj][m][1][0], acc[ai][bj][m][1][1], acc[ai][bj][m][1][2], acc[ai][bj][m][1][3]};
;                     if (wc == 0) {
;                         const f32x4 c0 = rc[g & 1][0], c1 = rc[g & 1][1], s0 = rc[g & 1][2], s1 = rc[g & 1][3];
;                         const float cs[8] = {c0[0], c0[1], c0[2], c0[3], c1[0], c1[1], c1[2], c1[3]}, sn[8] = {s0[0], s0[1], s0[2], s0[3], s1[0], s1[1], s1[2], s1[3]};
; #pragma unroll
;                         for (int i = 0; i < 8; ++i) {
;                             const float pv = __shfl_xor(v[i], 32);
;                             v[i] = (fq < 2) ? (v[i] * cs[i] - pv * sn[i]) : (v[i] * cs[i] + pv * sn[i]);
;                         }
;                     }
.LBB0_1504:
	v_and_b32_e32 v113, 64, v211
	v_xor_b32_e32 v112, 32, v211
	v_add_u32_e32 v113, 64, v113
	v_cmp_lt_i32_e32 vcc, v112, v113
	s_nop 1
	v_cndmask_b32_e32 v112, v211, v112, vcc
	v_lshlrev_b32_e32 v119, 2, v112
	ds_bpermute_b32 v112, v119, v108
	ds_bpermute_b32 v113, v119, v109
	ds_bpermute_b32 v114, v119, v110
	ds_bpermute_b32 v115, v119, v111
	ds_bpermute_b32 v116, v119, v104
	ds_bpermute_b32 v117, v119, v105
	ds_bpermute_b32 v118, v119, v106
	ds_bpermute_b32 v119, v119, v107
	s_waitcnt vmcnt(6) lgkmcnt(0)
	v_pk_mul_f32 v[112:113], v[140:141], v[112:113]
	v_pk_mul_f32 v[114:115], v[142:143], v[114:115]
	v_pk_mul_f32 v[116:117], v[136:137], v[116:117]
	v_cndmask_b32_e64 v113, v113, -v113, s[0:1]
	v_pk_mul_f32 v[118:119], v[138:139], v[118:119]
	v_cndmask_b32_e64 v112, v112, -v112, s[0:1]
	v_cndmask_b32_e64 v115, v115, -v115, s[0:1]
	v_cndmask_b32_e64 v114, v114, -v114, s[0:1]
	v_cndmask_b32_e64 v117, v117, -v117, s[0:1]
	v_cndmask_b32_e64 v116, v116, -v116, s[0:1]
	v_cndmask_b32_e64 v119, v119, -v119, s[0:1]
	v_cndmask_b32_e64 v118, v118, -v118, s[0:1]
	v_pk_fma_f32 v[106:107], v[106:107], v[134:135], v[118:119]
	v_pk_fma_f32 v[104:105], v[104:105], v[132:133], v[116:117]
	v_pk_fma_f32 v[110:111], v[110:111], v[130:131], v[114:115]
	v_pk_fma_f32 v[108:109], v[108:109], v[128:129], v[112:113]
	s_and_b64 vcc, exec, s[48:49]
	s_cbranch_vccnz .LBB0_1502

; #define ROPE_LOAD(buf, g) do { const int _pos = (row0 + ((g) >> 2) * HALF + ((g) & 3) * 16) & (SEQ - 1); const float* _rp = rope + _pos * 32 + 8 * (fq & 1); \
;                 rc[buf][0] = *(const f32x4*)_rp; rc[buf][1] = *(const f32x4*)(_rp + 4); rc[buf][2] = *(const f32x4*)(_rp + 16); rc[buf][3] = *(const f32x4*)(_rp + 20); } while (0)
;     __device__ __forceinline__ void operator()(const f32x4 (&acc)[2][2][4][2], const Unit& u, int wr, int wc, int fr, int fq) const {
;     ...
;                 if (wc == 0 && g + 1 < 8) ROPE_LOAD((g + 1) & 1, g + 1);
; #pragma unroll
;                 for (int bj = 0; bj < 2; ++bj) {
;                     float v[8] = {acc[ai][bj][m][0][0], acc[ai][bj][m][0][1], acc[ai][bj][m][0][2], acc[ai][bj][m][0][3],
;                                   acc[ai][bj][m][1][0], acc[ai][bj][m][1][1], acc[ai][bj][m][1][2], acc[ai][bj][m][1][3]};
;                     if (wc == 0) {
;                         const f32x4 c0 = rc[g & 1][0], c1 = rc[g & 1][1], s0 = rc[g & 1][2], s1 = rc[g & 1][3];
;                         const float cs[8] = {c0[0], c0[1], c0[2], c0[3], c1[0], c1[1], c1[2], c1[3]}, sn[8] = {s0[0], s0[1], s0[2], s0[3], s1[0], s1[1], s1[2], s1[3]};
; #pragma unroll
;                         for (int i = 0; i < 8; ++i) {
;                             const float pv = __shfl_xor(v[i], 32);
;                             v[i] = (fq < 2) ? (v[i] * cs[i] - pv * sn[i]) : (v[i] * cs[i] + pv * sn[i]);
;                         }
;                     }
.LBB0_1510:
	v_and_b32_e32 v105, 64, v211
	v_xor_b32_e32 v104, 32, v211
	v_add_u32_e32 v105, 64, v105
	v_cmp_lt_i32_e32 vcc, v104, v105
	s_nop 1
	v_cndmask_b32_e32 v104, v211, v104, vcc
	v_lshlrev_b32_e32 v111, 2, v104
	ds_bpermute_b32 v104, v111, v100
	ds_bpermute_b32 v105, v111, v101
	ds_bpermute_b32 v106, v111, v102
	ds_bpermute_b32 v107, v111, v103
	ds_bpermute_b32 v108, v111, v96
	ds_bpermute_b32 v109, v111, v97
	ds_bpermute_b32 v110, v111, v98
	ds_bpermute_b32 v111, v111, v99
	s_waitcnt lgkmcnt(0)
	v_pk_mul_f32 v[104:105], v[140:141], v[104:105]
	v_pk_mul_f32 v[106:107], v[142:143], v[106:107]
	v_pk_mul_f32 v[108:109], v[136:137], v[108:109]
	v_cndmask_b32_e64 v105, v105, -v105, s[0:1]
	v_pk_mul_f32 v[110:111], v[138:139], v[110:111]
	v_cndmask_b32_e64 v104, v104, -v104, s[0:1]
	v_cndmask_b32_e64 v107, v107, -v107, s[0:1]
	v_cndmask_b32_e64 v106, v106, -v106, s[0:1]
	v_cndmask_b32_e64 v109, v109, -v109, s[0:1]
	v_cndmask_b32_e64 v108, v108, -v108, s[0:1]
	v_cndmask_b32_e64 v111, v111, -v111, s[0:1]
	v_cndmask_b32_e64 v110, v110, -v110, s[0:1]
	v_pk_fma_f32 v[98:99], v[98:99], v[134:135], v[110:111]
	v_pk_fma_f32 v[96:97], v[96:97], v[132:133], v[108:109]
	v_pk_fma_f32 v[102:103], v[102:103], v[130:131], v[106:107]
	v_pk_fma_f32 v[100:101], v[100:101], v[128:129], v[104:105]
	s_and_b64 vcc, exec, s[48:49]
	s_cbranch_vccnz .LBB0_1509

; #define ROPE_LOAD(buf, g) do { const int _pos = (row0 + ((g) >> 2) * HALF + ((g) & 3) * 16) & (SEQ - 1); const float* _rp = rope + _pos * 32 + 8 * (fq & 1); \
;                 rc[buf][0] = *(const f32x4*)_rp; rc[buf][1] = *(const f32x4*)(_rp + 4); rc[buf][2] = *(const f32x4*)(_rp + 16); rc[buf][3] = *(const f32x4*)(_rp + 20); } while (0)
;     __device__ __forceinline__ void operator()(const f32x4 (&acc)[2][2][4][2], const Unit& u, int wr, int wc, int fr, int fq) const {
;     ...
;                 if (wc == 0 && g + 1 < 8) ROPE_LOAD((g + 1) & 1, g + 1);
; #pragma unroll
;                 for (int bj = 0; bj < 2; ++bj) {
;                     float v[8] = {acc[ai][bj][m][0][0], acc[ai][bj][m][0][1], acc[ai][bj][m][0][2], acc[ai][bj][m][0][3],
;                                   acc[ai][bj][m][1][0], acc[ai][bj][m][1][1], acc[ai][bj][m][1][2], acc[ai][bj][m][1][3]};
;                     if (wc == 0) {
;                         const f32x4 c0 = rc[g & 1][0], c1 = rc[g & 1][1], s0 = rc[g & 1][2], s1 = rc[g & 1][3];
;                         const float cs[8] = {c0[0], c0[1], c0[2], c0[3], c1[0], c1[1], c1[2], c1[3]}, sn[8] = {s0[0], s0[1], s0[2], s0[3], s1[0], s1[1], s1[2], s1[3]};
; #pragma unroll
;                         for (int i = 0; i < 8; ++i) {
;                             const float pv = __shfl_xor(v[i], 32);
;                             v[i] = (fq < 2) ? (v[i] * cs[i] - pv * sn[i]) : (v[i] * cs[i] + pv * sn[i]);
;                         }
;                     }
.LBB0_1518:
	v_and_b32_e32 v97, 64, v211
	v_xor_b32_e32 v96, 32, v211
	v_add_u32_e32 v97, 64, v97
	v_cmp_lt_i32_e32 vcc, v96, v97
	s_nop 1
	v_cndmask_b32_e32 v96, v211, v96, vcc
	v_lshlrev_b32_e32 v103, 2, v96
	ds_bpermute_b32 v96, v103, v92
	ds_bpermute_b32 v97, v103, v93
	ds_bpermute_b32 v98, v103, v94
	ds_bpermute_b32 v99, v103, v95
	ds_bpermute_b32 v100, v103, v88
	ds_bpermute_b32 v101, v103, v89
	ds_bpermute_b32 v102, v103, v90
	ds_bpermute_b32 v103, v103, v91
	s_waitcnt vmcnt(6) lgkmcnt(0)
	v_pk_mul_f32 v[96:97], v[156:157], v[96:97]
	v_pk_mul_f32 v[98:99], v[158:159], v[98:99]
	v_pk_mul_f32 v[100:101], v[152:153], v[100:101]
	v_cndmask_b32_e64 v97, v97, -v97, s[0:1]
	v_pk_mul_f32 v[102:103], v[154:155], v[102:103]
	v_cndmask_b32_e64 v96, v96, -v96, s[0:1]
	v_cndmask_b32_e64 v99, v99, -v99, s[0:1]
	v_cndmask_b32_e64 v98, v98, -v98, s[0:1]
	v_cndmask_b32_e64 v101, v101, -v101, s[0:1]
	v_cndmask_b32_e64 v100, v100, -v100, s[0:1]
	v_cndmask_b32_e64 v103, v103, -v103, s[0:1]
	v_cndmask_b32_e64 v102, v102, -v102, s[0:1]
	v_pk_fma_f32 v[90:91], v[90:91], v[150:151], v[102:103]
	v_pk_fma_f32 v[88:89], v[88:89], v[148:149], v[100:101]
	v_pk_fma_f32 v[94:95], v[94:95], v[146:147], v[98:99]
	v_pk_fma_f32 v[92:93], v[92:93], v[144:145], v[96:97]
	s_and_b64 vcc, exec, s[48:49]
	s_cbranch_vccnz .LBB0_1516

; #define ROPE_LOAD(buf, g) do { const int _pos = (row0 + ((g) >> 2) * HALF + ((g) & 3) * 16) & (SEQ - 1); const float* _rp = rope + _pos * 32 + 8 * (fq & 1); \
;                 rc[buf][0] = *(const f32x4*)_rp; rc[buf][1] = *(const f32x4*)(_rp + 4); rc[buf][2] = *(const f32x4*)(_rp + 16); rc[buf][3] = *(const f32x4*)(_rp + 20); } while (0)
;     __device__ __forceinline__ void operator()(const f32x4 (&acc)[2][2][4][2], const Unit& u, int wr, int wc, int fr, int fq) const {
;     ...
;                 if (wc == 0 && g + 1 < 8) ROPE_LOAD((g + 1) & 1, g + 1);
; #pragma unroll
;                 for (int bj = 0; bj < 2; ++bj) {
;                     float v[8] = {acc[ai][bj][m][0][0], acc[ai][bj][m][0][1], acc[ai][bj][m][0][2], acc[ai][bj][m][0][3],
;                                   acc[ai][bj][m][1][0], acc[ai][bj][m][1][1], acc[ai][bj][m][1][2], acc[ai][bj][m][1][3]};
;                     if (wc == 0) {
;                         const f32x4 c0 = rc[g & 1][0], c1 = rc[g & 1][1], s0 = rc[g & 1][2], s1 = rc[g & 1][3];
;                         const float cs[8] = {c0[0], c0[1], c0[2], c0[3], c1[0], c1[1], c1[2], c1[3]}, sn[8] = {s0[0], s0[1], s0[2], s0[3], s1[0], s1[1], s1[2], s1[3]};
; #pragma unroll
;                         for (int i = 0; i < 8; ++i) {
;                             const float pv = __shfl_xor(v[i], 32);
;                             v[i] = (fq < 2) ? (v[i] * cs[i] - pv * sn[i]) : (v[i] * cs[i] + pv * sn[i]);
;                         }
;                     }
.LBB0_1524:
	v_and_b32_e32 v89, 64, v211
	v_xor_b32_e32 v88, 32, v211
	v_add_u32_e32 v89, 64, v89
	v_cmp_lt_i32_e32 vcc, v88, v89
	s_nop 1
	v_cndmask_b32_e32 v88, v211, v88, vcc
	v_lshlrev_b32_e32 v95, 2, v88
	ds_bpermute_b32 v88, v95, v84
	ds_bpermute_b32 v89, v95, v85
	ds_bpermute_b32 v90, v95, v86
	ds_bpermute_b32 v91, v95, v87
	ds_bpermute_b32 v92, v95, v80
	ds_bpermute_b32 v93, v95, v81
	ds_bpermute_b32 v94, v95, v82
	ds_bpermute_b32 v95, v95, v83
	s_waitcnt lgkmcnt(0)
	v_pk_mul_f32 v[88:89], v[156:157], v[88:89]
	v_pk_mul_f32 v[90:91], v[158:159], v[90:91]
	v_pk_mul_f32 v[92:93], v[152:153], v[92:93]
	v_cndmask_b32_e64 v89, v89, -v89, s[0:1]
	v_pk_mul_f32 v[94:95], v[154:155], v[94:95]
	v_cndmask_b32_e64 v88, v88, -v88, s[0:1]
	v_cndmask_b32_e64 v91, v91, -v91, s[0:1]
	v_cndmask_b32_e64 v90, v90, -v90, s[0:1]
	v_cndmask_b32_e64 v93, v93, -v93, s[0:1]
	v_cndmask_b32_e64 v92, v92, -v92, s[0:1]
	v_cndmask_b32_e64 v95, v95, -v95, s[0:1]
	v_cndmask_b32_e64 v94, v94, -v94, s[0:1]
	v_pk_fma_f32 v[82:83], v[82:83], v[150:151], v[94:95]
	v_pk_fma_f32 v[80:81], v[80:81], v[148:149], v[92:93]
	v_pk_fma_f32 v[86:87], v[86:87], v[146:147], v[90:91]
	v_pk_fma_f32 v[84:85], v[84:85], v[144:145], v[88:89]
	s_and_b64 vcc, exec, s[48:49]
	s_cbranch_vccnz .LBB0_1523

; #define ROPE_LOAD(buf, g) do { const int _pos = (row0 + ((g) >> 2) * HALF + ((g) & 3) * 16) & (SEQ - 1); const float* _rp = rope + _pos * 32 + 8 * (fq & 1); \
;                 rc[buf][0] = *(const f32x4*)_rp; rc[buf][1] = *(const f32x4*)(_rp + 4); rc[buf][2] = *(const f32x4*)(_rp + 16); rc[buf][3] = *(const f32x4*)(_rp + 20); } while (0)
;     __device__ __forceinline__ void operator()(const f32x4 (&acc)[2][2][4][2], const Unit& u, int wr, int wc, int fr, int fq) const {
;     ...
;                 if (wc == 0 && g + 1 < 8) ROPE_LOAD((g + 1) & 1, g + 1);
; #pragma unroll
;                 for (int bj = 0; bj < 2; ++bj) {
;                     float v[8] = {acc[ai][bj][m][0][0], acc[ai][bj][m][0][1], acc[ai][bj][m][0][2], acc[ai][bj][m][0][3],
;                                   acc[ai][bj][m][1][0], acc[ai][bj][m][1][1], acc[ai][bj][m][1][2], acc[ai][bj][m][1][3]};
;                     if (wc == 0) {
;                         const f32x4 c0 = rc[g & 1][0], c1 = rc[g & 1][1], s0 = rc[g & 1][2], s1 = rc[g & 1][3];
;                         const float cs[8] = {c0[0], c0[1], c0[2], c0[3], c1[0], c1[1], c1[2], c1[3]}, sn[8] = {s0[0], s0[1], s0[2], s0[3], s1[0], s1[1], s1[2], s1[3]};
; #pragma unroll
;                         for (int i = 0; i < 8; ++i) {
;                             const float pv = __shfl_xor(v[i], 32);
;                             v[i] = (fq < 2) ? (v[i] * cs[i] - pv * sn[i]) : (v[i] * cs[i] + pv * sn[i]);
;                         }
;                     }
.LBB0_1532:
	v_and_b32_e32 v81, 64, v211
	v_xor_b32_e32 v80, 32, v211
	v_add_u32_e32 v81, 64, v81
	v_cmp_lt_i32_e32 vcc, v80, v81
	s_nop 1
	v_cndmask_b32_e32 v80, v211, v80, vcc
	v_lshlrev_b32_e32 v87, 2, v80
	ds_bpermute_b32 v80, v87, v76
	ds_bpermute_b32 v81, v87, v77
	ds_bpermute_b32 v82, v87, v78
	ds_bpermute_b32 v83, v87, v79
	ds_bpermute_b32 v84, v87, v72
	ds_bpermute_b32 v85, v87, v73
	ds_bpermute_b32 v86, v87, v74
	ds_bpermute_b32 v87, v87, v75
	s_waitcnt vmcnt(6) lgkmcnt(0)
	v_pk_mul_f32 v[80:81], v[140:141], v[80:81]
	v_pk_mul_f32 v[82:83], v[142:143], v[82:83]
	v_pk_mul_f32 v[84:85], v[136:137], v[84:85]
	v_cndmask_b32_e64 v81, v81, -v81, s[0:1]
	v_pk_mul_f32 v[86:87], v[138:139], v[86:87]
	v_cndmask_b32_e64 v80, v80, -v80, s[0:1]
	v_cndmask_b32_e64 v83, v83, -v83, s[0:1]
	v_cndmask_b32_e64 v82, v82, -v82, s[0:1]
	v_cndmask_b32_e64 v85, v85, -v85, s[0:1]
	v_cndmask_b32_e64 v84, v84, -v84, s[0:1]
	v_cndmask_b32_e64 v87, v87, -v87, s[0:1]
	v_cndmask_b32_e64 v86, v86, -v86, s[0:1]
	v_pk_fma_f32 v[74:75], v[74:75], v[134:135], v[86:87]
	v_pk_fma_f32 v[72:73], v[72:73], v[132:133], v[84:85]
	v_pk_fma_f32 v[78:79], v[78:79], v[130:131], v[82:83]
	v_pk_fma_f32 v[76:77], v[76:77], v[128:129], v[80:81]
	s_and_b64 vcc, exec, s[48:49]
	s_cbranch_vccnz .LBB0_1530

; #define ROPE_LOAD(buf, g) do { const int _pos = (row0 + ((g) >> 2) * HALF + ((g) & 3) * 16) & (SEQ - 1); const float* _rp = rope + _pos * 32 + 8 * (fq & 1); \
;                 rc[buf][0] = *(const f32x4*)_rp; rc[buf][1] = *(const f32x4*)(_rp + 4); rc[buf][2] = *(const f32x4*)(_rp + 16); rc[buf][3] = *(const f32x4*)(_rp + 20); } while (0)
;     __device__ __forceinline__ void operator()(const f32x4 (&acc)[2][2][4][2], const Unit& u, int wr, int wc, int fr, int fq) const {
;     ...
;                 if (wc == 0 && g + 1 < 8) ROPE_LOAD((g + 1) & 1, g + 1);
; #pragma unroll
;                 for (int bj = 0; bj < 2; ++bj) {
;                     float v[8] = {acc[ai][bj][m][0][0], acc[ai][bj][m][0][1], acc[ai][bj][m][0][2], acc[ai][bj][m][0][3],
;                                   acc[ai][bj][m][1][0], acc[ai][bj][m][1][1], acc[ai][bj][m][1][2], acc[ai][bj][m][1][3]};
;                     if (wc == 0) {
;                         const f32x4 c0 = rc[g & 1][0], c1 = rc[g & 1][1], s0 = rc[g & 1][2], s1 = rc[g & 1][3];
;                         const float cs[8] = {c0[0], c0[1], c0[2], c0[3], c1[0], c1[1], c1[2], c1[3]}, sn[8] = {s0[0], s0[1], s0[2], s0[3], s1[0], s1[1], s1[2], s1[3]};
; #pragma unroll
;                         for (int i = 0; i < 8; ++i) {
;                             const float pv = __shfl_xor(v[i], 32);
;                             v[i] = (fq < 2) ? (v[i] * cs[i] - pv * sn[i]) : (v[i] * cs[i] + pv * sn[i]);
;                         }
;                     }
.LBB0_1538:
	v_and_b32_e32 v73, 64, v211
	v_xor_b32_e32 v72, 32, v211
	v_add_u32_e32 v73, 64, v73
	v_cmp_lt_i32_e32 vcc, v72, v73
	s_nop 1
	v_cndmask_b32_e32 v72, v211, v72, vcc
	v_lshlrev_b32_e32 v79, 2, v72
	ds_bpermute_b32 v72, v79, v68
	ds_bpermute_b32 v73, v79, v69
	ds_bpermute_b32 v74, v79, v70
	ds_bpermute_b32 v75, v79, v71
	ds_bpermute_b32 v76, v79, v64
	ds_bpermute_b32 v77, v79, v65
	ds_bpermute_b32 v78, v79, v66
	ds_bpermute_b32 v79, v79, v67
	s_waitcnt lgkmcnt(0)
	v_pk_mul_f32 v[72:73], v[140:141], v[72:73]
	v_pk_mul_f32 v[74:75], v[142:143], v[74:75]
	v_pk_mul_f32 v[76:77], v[136:137], v[76:77]
	v_cndmask_b32_e64 v73, v73, -v73, s[0:1]
	v_pk_mul_f32 v[78:79], v[138:139], v[78:79]
	v_cndmask_b32_e64 v72, v72, -v72, s[0:1]
	v_cndmask_b32_e64 v75, v75, -v75, s[0:1]
	v_cndmask_b32_e64 v74, v74, -v74, s[0:1]
	v_cndmask_b32_e64 v77, v77, -v77, s[0:1]
	v_cndmask_b32_e64 v76, v76, -v76, s[0:1]
	v_cndmask_b32_e64 v79, v79, -v79, s[0:1]
	v_cndmask_b32_e64 v78, v78, -v78, s[0:1]
	v_pk_fma_f32 v[66:67], v[66:67], v[134:135], v[78:79]
	v_pk_fma_f32 v[64:65], v[64:65], v[132:133], v[76:77]
	v_pk_fma_f32 v[70:71], v[70:71], v[130:131], v[74:75]
	v_pk_fma_f32 v[68:69], v[68:69], v[128:129], v[72:73]
	s_and_b64 vcc, exec, s[48:49]
	s_cbranch_vccnz .LBB0_1537

; #define ROPE_LOAD(buf, g) do { const int _pos = (row0 + ((g) >> 2) * HALF + ((g) & 3) * 16) & (SEQ - 1); const float* _rp = rope + _pos * 32 + 8 * (fq & 1); \
;                 rc[buf][0] = *(const f32x4*)_rp; rc[buf][1] = *(const f32x4*)(_rp + 4); rc[buf][2] = *(const f32x4*)(_rp + 16); rc[buf][3] = *(const f32x4*)(_rp + 20); } while (0)
;     __device__ __forceinline__ void operator()(const f32x4 (&acc)[2][2][4][2], const Unit& u, int wr, int wc, int fr, int fq) const {
;     ...
;                 if (wc == 0 && g + 1 < 8) ROPE_LOAD((g + 1) & 1, g + 1);
; #pragma unroll
;                 for (int bj = 0; bj < 2; ++bj) {
;                     float v[8] = {acc[ai][bj][m][0][0], acc[ai][bj][m][0][1], acc[ai][bj][m][0][2], acc[ai][bj][m][0][3],
;                                   acc[ai][bj][m][1][0], acc[ai][bj][m][1][1], acc[ai][bj][m][1][2], acc[ai][bj][m][1][3]};
;                     if (wc == 0) {
;                         const f32x4 c0 = rc[g & 1][0], c1 = rc[g & 1][1], s0 = rc[g & 1][2], s1 = rc[g & 1][3];
;                         const float cs[8] = {c0[0], c0[1], c0[2], c0[3], c1[0], c1[1], c1[2], c1[3]}, sn[8] = {s0[0], s0[1], s0[2], s0[3], s1[0], s1[1], s1[2], s1[3]};
; #pragma unroll
;                         for (int i = 0; i < 8; ++i) {
;                             const float pv = __shfl_xor(v[i], 32);
;                             v[i] = (fq < 2) ? (v[i] * cs[i] - pv * sn[i]) : (v[i] * cs[i] + pv * sn[i]);
;                         }
;                     }
.LBB0_1546:
	v_and_b32_e32 v65, 64, v211
	v_xor_b32_e32 v64, 32, v211
	v_add_u32_e32 v65, 64, v65
	v_cmp_lt_i32_e32 vcc, v64, v65
	s_nop 1
	v_cndmask_b32_e32 v64, v211, v64, vcc
	v_lshlrev_b32_e32 v71, 2, v64
	ds_bpermute_b32 v64, v71, v60
	ds_bpermute_b32 v65, v71, v61
	ds_bpermute_b32 v66, v71, v62
	ds_bpermute_b32 v67, v71, v63
	ds_bpermute_b32 v68, v71, v56
	ds_bpermute_b32 v69, v71, v57
	ds_bpermute_b32 v70, v71, v58
	ds_bpermute_b32 v71, v71, v59
	s_waitcnt vmcnt(6) lgkmcnt(0)
	v_pk_mul_f32 v[64:65], v[156:157], v[64:65]
	v_pk_mul_f32 v[66:67], v[158:159], v[66:67]
	v_pk_mul_f32 v[68:69], v[152:153], v[68:69]
	v_cndmask_b32_e64 v65, v65, -v65, s[0:1]
	v_pk_mul_f32 v[70:71], v[154:155], v[70:71]
	v_cndmask_b32_e64 v64, v64, -v64, s[0:1]
	v_cndmask_b32_e64 v67, v67, -v67, s[0:1]
	v_cndmask_b32_e64 v66, v66, -v66, s[0:1]
	v_cndmask_b32_e64 v69, v69, -v69, s[0:1]
	v_cndmask_b32_e64 v68, v68, -v68, s[0:1]
	v_cndmask_b32_e64 v71, v71, -v71, s[0:1]
	v_cndmask_b32_e64 v70, v70, -v70, s[0:1]
	v_pk_fma_f32 v[58:59], v[58:59], v[150:151], v[70:71]
	v_pk_fma_f32 v[56:57], v[56:57], v[148:149], v[68:69]
	v_pk_fma_f32 v[62:63], v[62:63], v[146:147], v[66:67]
	v_pk_fma_f32 v[60:61], v[60:61], v[144:145], v[64:65]
	s_and_b64 vcc, exec, s[48:49]
	s_cbranch_vccnz .LBB0_1544

; #define ROPE_LOAD(buf, g) do { const int _pos = (row0 + ((g) >> 2) * HALF + ((g) & 3) * 16) & (SEQ - 1); const float* _rp = rope + _pos * 32 + 8 * (fq & 1); \
;                 rc[buf][0] = *(const f32x4*)_rp; rc[buf][1] = *(const f32x4*)(_rp + 4); rc[buf][2] = *(const f32x4*)(_rp + 16); rc[buf][3] = *(const f32x4*)(_rp + 20); } while (0)
;     __device__ __forceinline__ void operator()(const f32x4 (&acc)[2][2][4][2], const Unit& u, int wr, int wc, int fr, int fq) const {
;     ...
;                 if (wc == 0 && g + 1 < 8) ROPE_LOAD((g + 1) & 1, g + 1);
; #pragma unroll
;                 for (int bj = 0; bj < 2; ++bj) {
;                     float v[8] = {acc[ai][bj][m][0][0], acc[ai][bj][m][0][1], acc[ai][bj][m][0][2], acc[ai][bj][m][0][3],
;                                   acc[ai][bj][m][1][0], acc[ai][bj][m][1][1], acc[ai][bj][m][1][2], acc[ai][bj][m][1][3]};
;                     if (wc == 0) {
;                         const f32x4 c0 = rc[g & 1][0], c1 = rc[g & 1][1], s0 = rc[g & 1][2], s1 = rc[g & 1][3];
;                         const float cs[8] = {c0[0], c0[1], c0[2], c0[3], c1[0], c1[1], c1[2], c1[3]}, sn[8] = {s0[0], s0[1], s0[2], s0[3], s1[0], s1[1], s1[2], s1[3]};
; #pragma unroll
;                         for (int i = 0; i < 8; ++i) {
;                             const float pv = __shfl_xor(v[i], 32);
;                             v[i] = (fq < 2) ? (v[i] * cs[i] - pv * sn[i]) : (v[i] * cs[i] + pv * sn[i]);
;                         }
;                     }
.LBB0_1552:
	v_and_b32_e32 v59, 64, v211
	v_xor_b32_e32 v58, 32, v211
	v_add_u32_e32 v59, 64, v59
	v_cmp_lt_i32_e32 vcc, v58, v59
	s_nop 1
	v_cndmask_b32_e32 v58, v211, v58, vcc
	v_lshlrev_b32_e32 v79, 2, v58
	ds_bpermute_b32 v58, v79, v52
	ds_bpermute_b32 v59, v79, v53
	ds_bpermute_b32 v60, v79, v54
	ds_bpermute_b32 v61, v79, v55
	ds_bpermute_b32 v62, v79, v48
	ds_bpermute_b32 v63, v79, v49
	ds_bpermute_b32 v78, v79, v50
	ds_bpermute_b32 v79, v79, v51
	s_waitcnt lgkmcnt(0)
	v_pk_mul_f32 v[58:59], v[156:157], v[58:59]
	v_pk_mul_f32 v[60:61], v[158:159], v[60:61]
	v_pk_mul_f32 v[62:63], v[152:153], v[62:63]
	v_cndmask_b32_e64 v59, v59, -v59, s[0:1]
	v_pk_mul_f32 v[78:79], v[154:155], v[78:79]
	v_cndmask_b32_e64 v58, v58, -v58, s[0:1]
	v_cndmask_b32_e64 v61, v61, -v61, s[0:1]
	v_cndmask_b32_e64 v60, v60, -v60, s[0:1]
	v_cndmask_b32_e64 v63, v63, -v63, s[0:1]
	v_cndmask_b32_e64 v62, v62, -v62, s[0:1]
	v_cndmask_b32_e64 v79, v79, -v79, s[0:1]
	v_cndmask_b32_e64 v78, v78, -v78, s[0:1]
	v_pk_fma_f32 v[50:51], v[50:51], v[150:151], v[78:79]
	v_pk_fma_f32 v[48:49], v[48:49], v[148:149], v[62:63]
	v_pk_fma_f32 v[54:55], v[54:55], v[146:147], v[60:61]
	v_pk_fma_f32 v[52:53], v[52:53], v[144:145], v[58:59]
	s_and_b64 vcc, exec, s[48:49]
	s_cbranch_vccnz .LBB0_1551

; #define ROPE_LOAD(buf, g) do { const int _pos = (row0 + ((g) >> 2) * HALF + ((g) & 3) * 16) & (SEQ - 1); const float* _rp = rope + _pos * 32 + 8 * (fq & 1); \
;                 rc[buf][0] = *(const f32x4*)_rp; rc[buf][1] = *(const f32x4*)(_rp + 4); rc[buf][2] = *(const f32x4*)(_rp + 16); rc[buf][3] = *(const f32x4*)(_rp + 20); } while (0)
;     __device__ __forceinline__ void operator()(const f32x4 (&acc)[2][2][4][2], const Unit& u, int wr, int wc, int fr, int fq) const {
;     ...
;                 if (wc == 0 && g + 1 < 8) ROPE_LOAD((g + 1) & 1, g + 1);
; #pragma unroll
;                 for (int bj = 0; bj < 2; ++bj) {
;                     float v[8] = {acc[ai][bj][m][0][0], acc[ai][bj][m][0][1], acc[ai][bj][m][0][2], acc[ai][bj][m][0][3],
;                                   acc[ai][bj][m][1][0], acc[ai][bj][m][1][1], acc[ai][bj][m][1][2], acc[ai][bj][m][1][3]};
;                     if (wc == 0) {
;                         const f32x4 c0 = rc[g & 1][0], c1 = rc[g & 1][1], s0 = rc[g & 1][2], s1 = rc[g & 1][3];
;                         const float cs[8] = {c0[0], c0[1], c0[2], c0[3], c1[0], c1[1], c1[2], c1[3]}, sn[8] = {s0[0], s0[1], s0[2], s0[3], s1[0], s1[1], s1[2], s1[3]};
; #pragma unroll
;                         for (int i = 0; i < 8; ++i) {
;                             const float pv = __shfl_xor(v[i], 32);
;                             v[i] = (fq < 2) ? (v[i] * cs[i] - pv * sn[i]) : (v[i] * cs[i] + pv * sn[i]);
;                         }
;                     }
.LBB0_1560:
	v_and_b32_e32 v51, 64, v211
	v_xor_b32_e32 v50, 32, v211
	v_add_u32_e32 v51, 64, v51
	v_cmp_lt_i32_e32 vcc, v50, v51
	s_nop 1
	v_cndmask_b32_e32 v50, v211, v50, vcc
	v_lshlrev_b32_e32 v75, 2, v50
	ds_bpermute_b32 v50, v75, v44
	ds_bpermute_b32 v51, v75, v45
	ds_bpermute_b32 v52, v75, v46
	ds_bpermute_b32 v53, v75, v47
	ds_bpermute_b32 v54, v75, v40
	ds_bpermute_b32 v55, v75, v41
	ds_bpermute_b32 v74, v75, v42
	ds_bpermute_b32 v75, v75, v43
	s_waitcnt vmcnt(6) lgkmcnt(0)
	v_pk_mul_f32 v[50:51], v[140:141], v[50:51]
	v_pk_mul_f32 v[52:53], v[142:143], v[52:53]
	v_pk_mul_f32 v[54:55], v[136:137], v[54:55]
	v_cndmask_b32_e64 v51, v51, -v51, s[0:1]
	v_pk_mul_f32 v[74:75], v[138:139], v[74:75]
	v_cndmask_b32_e64 v50, v50, -v50, s[0:1]
	v_cndmask_b32_e64 v53, v53, -v53, s[0:1]
	v_cndmask_b32_e64 v52, v52, -v52, s[0:1]
	v_cndmask_b32_e64 v55, v55, -v55, s[0:1]
	v_cndmask_b32_e64 v54, v54, -v54, s[0:1]
	v_cndmask_b32_e64 v75, v75, -v75, s[0:1]
	v_cndmask_b32_e64 v74, v74, -v74, s[0:1]
	v_pk_fma_f32 v[42:43], v[42:43], v[134:135], v[74:75]
	v_pk_fma_f32 v[40:41], v[40:41], v[132:133], v[54:55]
	v_pk_fma_f32 v[46:47], v[46:47], v[130:131], v[52:53]
	v_pk_fma_f32 v[44:45], v[44:45], v[128:129], v[50:51]
	s_and_b64 vcc, exec, s[48:49]
	s_cbranch_vccnz .LBB0_1558

; #define ROPE_LOAD(buf, g) do { const int _pos = (row0 + ((g) >> 2) * HALF + ((g) & 3) * 16) & (SEQ - 1); const float* _rp = rope + _pos * 32 + 8 * (fq & 1); \
;                 rc[buf][0] = *(const f32x4*)_rp; rc[buf][1] = *(const f32x4*)(_rp + 4); rc[buf][2] = *(const f32x4*)(_rp + 16); rc[buf][3] = *(const f32x4*)(_rp + 20); } while (0)
;     __device__ __forceinline__ void operator()(const f32x4 (&acc)[2][2][4][2], const Unit& u, int wr, int wc, int fr, int fq) const {
;     ...
;                 if (wc == 0 && g + 1 < 8) ROPE_LOAD((g + 1) & 1, g + 1);
; #pragma unroll
;                 for (int bj = 0; bj < 2; ++bj) {
;                     float v[8] = {acc[ai][bj][m][0][0], acc[ai][bj][m][0][1], acc[ai][bj][m][0][2], acc[ai][bj][m][0][3],
;                                   acc[ai][bj][m][1][0], acc[ai][bj][m][1][1], acc[ai][bj][m][1][2], acc[ai][bj][m][1][3]};
;                     if (wc == 0) {
;                         const f32x4 c0 = rc[g & 1][0], c1 = rc[g & 1][1], s0 = rc[g & 1][2], s1 = rc[g & 1][3];
;                         const float cs[8] = {c0[0], c0[1], c0[2], c0[3], c1[0], c1[1], c1[2], c1[3]}, sn[8] = {s0[0], s0[1], s0[2], s0[3], s1[0], s1[1], s1[2], s1[3]};
; #pragma unroll
;                         for (int i = 0; i < 8; ++i) {
;                             const float pv = __shfl_xor(v[i], 32);
;                             v[i] = (fq < 2) ? (v[i] * cs[i] - pv * sn[i]) : (v[i] * cs[i] + pv * sn[i]);
;                         }
;                     }
.LBB0_1566:
	v_and_b32_e32 v41, 64, v211
	v_xor_b32_e32 v40, 32, v211
	v_add_u32_e32 v41, 64, v41
	v_cmp_lt_i32_e32 vcc, v40, v41
	s_nop 1
	v_cndmask_b32_e32 v40, v211, v40, vcc
	v_lshlrev_b32_e32 v47, 2, v40
	ds_bpermute_b32 v40, v47, v36
	ds_bpermute_b32 v41, v47, v37
	ds_bpermute_b32 v42, v47, v38
	ds_bpermute_b32 v43, v47, v39
	ds_bpermute_b32 v44, v47, v32
	ds_bpermute_b32 v45, v47, v33
	ds_bpermute_b32 v46, v47, v34
	ds_bpermute_b32 v47, v47, v35
	s_waitcnt lgkmcnt(0)
	v_pk_mul_f32 v[40:41], v[140:141], v[40:41]
	v_pk_mul_f32 v[42:43], v[142:143], v[42:43]
	v_pk_mul_f32 v[44:45], v[136:137], v[44:45]
	v_cndmask_b32_e64 v41, v41, -v41, s[0:1]
	v_pk_mul_f32 v[46:47], v[138:139], v[46:47]
	v_cndmask_b32_e64 v40, v40, -v40, s[0:1]
	v_cndmask_b32_e64 v43, v43, -v43, s[0:1]
	v_cndmask_b32_e64 v42, v42, -v42, s[0:1]
	v_cndmask_b32_e64 v45, v45, -v45, s[0:1]
	v_cndmask_b32_e64 v44, v44, -v44, s[0:1]
	v_cndmask_b32_e64 v47, v47, -v47, s[0:1]
	v_cndmask_b32_e64 v46, v46, -v46, s[0:1]
	v_pk_fma_f32 v[34:35], v[34:35], v[134:135], v[46:47]
	v_pk_fma_f32 v[32:33], v[32:33], v[132:133], v[44:45]
	v_pk_fma_f32 v[38:39], v[38:39], v[130:131], v[42:43]
	v_pk_fma_f32 v[36:37], v[36:37], v[128:129], v[40:41]
	s_and_b64 vcc, exec, s[48:49]
	s_cbranch_vccnz .LBB0_1565

; #define ROPE_LOAD(buf, g) do { const int _pos = (row0 + ((g) >> 2) * HALF + ((g) & 3) * 16) & (SEQ - 1); const float* _rp = rope + _pos * 32 + 8 * (fq & 1); \
;                 rc[buf][0] = *(const f32x4*)_rp; rc[buf][1] = *(const f32x4*)(_rp + 4); rc[buf][2] = *(const f32x4*)(_rp + 16); rc[buf][3] = *(const f32x4*)(_rp + 20); } while (0)
;     __device__ __forceinline__ void operator()(const f32x4 (&acc)[2][2][4][2], const Unit& u, int wr, int wc, int fr, int fq) const {
;     ...
;                 if (wc == 0 && g + 1 < 8) ROPE_LOAD((g + 1) & 1, g + 1);
; #pragma unroll
;                 for (int bj = 0; bj < 2; ++bj) {
;                     float v[8] = {acc[ai][bj][m][0][0], acc[ai][bj][m][0][1], acc[ai][bj][m][0][2], acc[ai][bj][m][0][3],
;                                   acc[ai][bj][m][1][0], acc[ai][bj][m][1][1], acc[ai][bj][m][1][2], acc[ai][bj][m][1][3]};
;                     if (wc == 0) {
;                         const f32x4 c0 = rc[g & 1][0], c1 = rc[g & 1][1], s0 = rc[g & 1][2], s1 = rc[g & 1][3];
;                         const float cs[8] = {c0[0], c0[1], c0[2], c0[3], c1[0], c1[1], c1[2], c1[3]}, sn[8] = {s0[0], s0[1], s0[2], s0[3], s1[0], s1[1], s1[2], s1[3]};
; #pragma unroll
;                         for (int i = 0; i < 8; ++i) {
;                             const float pv = __shfl_xor(v[i], 32);
;                             v[i] = (fq < 2) ? (v[i] * cs[i] - pv * sn[i]) : (v[i] * cs[i] + pv * sn[i]);
;                         }
;                     }
.LBB0_1574:
	v_and_b32_e32 v33, 64, v211
	v_xor_b32_e32 v32, 32, v211
	v_add_u32_e32 v33, 64, v33
	v_cmp_lt_i32_e32 vcc, v32, v33
	s_nop 1
	v_cndmask_b32_e32 v32, v211, v32, vcc
	v_lshlrev_b32_e32 v39, 2, v32
	ds_bpermute_b32 v32, v39, v28
	ds_bpermute_b32 v33, v39, v29
	ds_bpermute_b32 v34, v39, v30
	ds_bpermute_b32 v35, v39, v31
	ds_bpermute_b32 v36, v39, v24
	ds_bpermute_b32 v37, v39, v25
	ds_bpermute_b32 v38, v39, v26
	ds_bpermute_b32 v39, v39, v27
	s_waitcnt vmcnt(6) lgkmcnt(0)
	v_pk_mul_f32 v[32:33], v[156:157], v[32:33]
	v_pk_mul_f32 v[34:35], v[158:159], v[34:35]
	v_pk_mul_f32 v[36:37], v[152:153], v[36:37]
	v_cndmask_b32_e64 v33, v33, -v33, s[0:1]
	v_pk_mul_f32 v[38:39], v[154:155], v[38:39]
	v_cndmask_b32_e64 v32, v32, -v32, s[0:1]
	v_cndmask_b32_e64 v35, v35, -v35, s[0:1]
	v_cndmask_b32_e64 v34, v34, -v34, s[0:1]
	v_cndmask_b32_e64 v37, v37, -v37, s[0:1]
	v_cndmask_b32_e64 v36, v36, -v36, s[0:1]
	v_cndmask_b32_e64 v39, v39, -v39, s[0:1]
	v_cndmask_b32_e64 v38, v38, -v38, s[0:1]
	v_pk_fma_f32 v[26:27], v[26:27], v[150:151], v[38:39]
	v_pk_fma_f32 v[24:25], v[24:25], v[148:149], v[36:37]
	v_pk_fma_f32 v[30:31], v[30:31], v[146:147], v[34:35]
	v_pk_fma_f32 v[28:29], v[28:29], v[144:145], v[32:33]
	s_and_b64 vcc, exec, s[48:49]
	s_cbranch_vccnz .LBB0_1572

; #define ROPE_LOAD(buf, g) do { const int _pos = (row0 + ((g) >> 2) * HALF + ((g) & 3) * 16) & (SEQ - 1); const float* _rp = rope + _pos * 32 + 8 * (fq & 1); \
;                 rc[buf][0] = *(const f32x4*)_rp; rc[buf][1] = *(const f32x4*)(_rp + 4); rc[buf][2] = *(const f32x4*)(_rp + 16); rc[buf][3] = *(const f32x4*)(_rp + 20); } while (0)
;     __device__ __forceinline__ void operator()(const f32x4 (&acc)[2][2][4][2], const Unit& u, int wr, int wc, int fr, int fq) const {
;     ...
;                 if (wc == 0 && g + 1 < 8) ROPE_LOAD((g + 1) & 1, g + 1);
; #pragma unroll
;                 for (int bj = 0; bj < 2; ++bj) {
;                     float v[8] = {acc[ai][bj][m][0][0], acc[ai][bj][m][0][1], acc[ai][bj][m][0][2], acc[ai][bj][m][0][3],
;                                   acc[ai][bj][m][1][0], acc[ai][bj][m][1][1], acc[ai][bj][m][1][2], acc[ai][bj][m][1][3]};
;                     if (wc == 0) {
;                         const f32x4 c0 = rc[g & 1][0], c1 = rc[g & 1][1], s0 = rc[g & 1][2], s1 = rc[g & 1][3];
;                         const float cs[8] = {c0[0], c0[1], c0[2], c0[3], c1[0], c1[1], c1[2], c1[3]}, sn[8] = {s0[0], s0[1], s0[2], s0[3], s1[0], s1[1], s1[2], s1[3]};
; #pragma unroll
;                         for (int i = 0; i < 8; ++i) {
;                             const float pv = __shfl_xor(v[i], 32);
;                             v[i] = (fq < 2) ? (v[i] * cs[i] - pv * sn[i]) : (v[i] * cs[i] + pv * sn[i]);
;                         }
;                     }
.LBB0_1580:
	v_and_b32_e32 v25, 64, v211
	v_xor_b32_e32 v24, 32, v211
	v_add_u32_e32 v25, 64, v25
	v_cmp_lt_i32_e32 vcc, v24, v25
	s_nop 1
	v_cndmask_b32_e32 v24, v211, v24, vcc
	v_lshlrev_b32_e32 v31, 2, v24
	ds_bpermute_b32 v24, v31, v20
	ds_bpermute_b32 v25, v31, v21
	ds_bpermute_b32 v26, v31, v22
	ds_bpermute_b32 v27, v31, v23
	ds_bpermute_b32 v28, v31, v16
	ds_bpermute_b32 v29, v31, v17
	ds_bpermute_b32 v30, v31, v18
	ds_bpermute_b32 v31, v31, v19
	s_waitcnt lgkmcnt(0)
	v_pk_mul_f32 v[24:25], v[156:157], v[24:25]
	v_pk_mul_f32 v[26:27], v[158:159], v[26:27]
	v_pk_mul_f32 v[28:29], v[152:153], v[28:29]
	v_cndmask_b32_e64 v25, v25, -v25, s[0:1]
	v_pk_mul_f32 v[30:31], v[154:155], v[30:31]
	v_cndmask_b32_e64 v24, v24, -v24, s[0:1]
	v_cndmask_b32_e64 v27, v27, -v27, s[0:1]
	v_cndmask_b32_e64 v26, v26, -v26, s[0:1]
	v_cndmask_b32_e64 v29, v29, -v29, s[0:1]
	v_cndmask_b32_e64 v28, v28, -v28, s[0:1]
	v_cndmask_b32_e64 v31, v31, -v31, s[0:1]
	v_cndmask_b32_e64 v30, v30, -v30, s[0:1]
	v_pk_fma_f32 v[18:19], v[18:19], v[150:151], v[30:31]
	v_pk_fma_f32 v[16:17], v[16:17], v[148:149], v[28:29]
	v_pk_fma_f32 v[22:23], v[22:23], v[146:147], v[26:27]
	v_pk_fma_f32 v[20:21], v[20:21], v[144:145], v[24:25]
	s_and_b64 vcc, exec, s[48:49]
	s_cbranch_vccnz .LBB0_1579

; #define ROPE_LOAD(buf, g) do { const int _pos = (row0 + ((g) >> 2) * HALF + ((g) & 3) * 16) & (SEQ - 1); const float* _rp = rope + _pos * 32 + 8 * (fq & 1); \
;                 rc[buf][0] = *(const f32x4*)_rp; rc[buf][1] = *(const f32x4*)(_rp + 4); rc[buf][2] = *(const f32x4*)(_rp + 16); rc[buf][3] = *(const f32x4*)(_rp + 20); } while (0)
;     __device__ __forceinline__ void operator()(const f32x4 (&acc)[2][2][4][2], const Unit& u, int wr, int wc, int fr, int fq) const {
;     ...
;                 if (wc == 0 && g + 1 < 8) ROPE_LOAD((g + 1) & 1, g + 1);
; #pragma unroll
;                 for (int bj = 0; bj < 2; ++bj) {
;                     float v[8] = {acc[ai][bj][m][0][0], acc[ai][bj][m][0][1], acc[ai][bj][m][0][2], acc[ai][bj][m][0][3],
;                                   acc[ai][bj][m][1][0], acc[ai][bj][m][1][1], acc[ai][bj][m][1][2], acc[ai][bj][m][1][3]};
;                     if (wc == 0) {
;                         const f32x4 c0 = rc[g & 1][0], c1 = rc[g & 1][1], s0 = rc[g & 1][2], s1 = rc[g & 1][3];
;                         const float cs[8] = {c0[0], c0[1], c0[2], c0[3], c1[0], c1[1], c1[2], c1[3]}, sn[8] = {s0[0], s0[1], s0[2], s0[3], s1[0], s1[1], s1[2], s1[3]};
; #pragma unroll
;                         for (int i = 0; i < 8; ++i) {
;                             const float pv = __shfl_xor(v[i], 32);
;                             v[i] = (fq < 2) ? (v[i] * cs[i] - pv * sn[i]) : (v[i] * cs[i] + pv * sn[i]);
;                         }
;                     }
.LBB0_1586:
	v_and_b32_e32 v17, 64, v211
	v_xor_b32_e32 v16, 32, v211
	v_add_u32_e32 v17, 64, v17
	v_cmp_lt_i32_e32 vcc, v16, v17
	s_nop 1
	v_cndmask_b32_e32 v16, v211, v16, vcc
	v_lshlrev_b32_e32 v23, 2, v16
	ds_bpermute_b32 v16, v23, v12
	ds_bpermute_b32 v17, v23, v13
	ds_bpermute_b32 v18, v23, v14
	ds_bpermute_b32 v19, v23, v15
	ds_bpermute_b32 v20, v23, v8
	ds_bpermute_b32 v21, v23, v9
	ds_bpermute_b32 v22, v23, v10
	ds_bpermute_b32 v23, v23, v11
	s_waitcnt vmcnt(2) lgkmcnt(0)
	v_pk_mul_f32 v[16:17], v[140:141], v[16:17]
	v_pk_mul_f32 v[18:19], v[142:143], v[18:19]
	v_pk_mul_f32 v[20:21], v[136:137], v[20:21]
	v_cndmask_b32_e64 v17, v17, -v17, s[0:1]
	v_pk_mul_f32 v[22:23], v[138:139], v[22:23]
	v_cndmask_b32_e64 v16, v16, -v16, s[0:1]
	v_cndmask_b32_e64 v19, v19, -v19, s[0:1]
	v_cndmask_b32_e64 v18, v18, -v18, s[0:1]
	v_cndmask_b32_e64 v21, v21, -v21, s[0:1]
	v_cndmask_b32_e64 v20, v20, -v20, s[0:1]
	v_cndmask_b32_e64 v23, v23, -v23, s[0:1]
	v_cndmask_b32_e64 v22, v22, -v22, s[0:1]
	v_pk_fma_f32 v[10:11], v[10:11], v[134:135], v[22:23]
	v_pk_fma_f32 v[8:9], v[8:9], v[132:133], v[20:21]
	v_pk_fma_f32 v[14:15], v[14:15], v[130:131], v[18:19]
	v_pk_fma_f32 v[12:13], v[12:13], v[128:129], v[16:17]
	s_and_b64 vcc, exec, s[48:49]
	s_cbranch_vccnz .LBB0_1585

; #define ROPE_LOAD(buf, g) do { const int _pos = (row0 + ((g) >> 2) * HALF + ((g) & 3) * 16) & (SEQ - 1); const float* _rp = rope + _pos * 32 + 8 * (fq & 1); \
;                 rc[buf][0] = *(const f32x4*)_rp; rc[buf][1] = *(const f32x4*)(_rp + 4); rc[buf][2] = *(const f32x4*)(_rp + 16); rc[buf][3] = *(const f32x4*)(_rp + 20); } while (0)
;     __device__ __forceinline__ void operator()(const f32x4 (&acc)[2][2][4][2], const Unit& u, int wr, int wc, int fr, int fq) const {
;     ...
;                 if (wc == 0 && g + 1 < 8) ROPE_LOAD((g + 1) & 1, g + 1);
; #pragma unroll
;                 for (int bj = 0; bj < 2; ++bj) {
;                     float v[8] = {acc[ai][bj][m][0][0], acc[ai][bj][m][0][1], acc[ai][bj][m][0][2], acc[ai][bj][m][0][3],
;                                   acc[ai][bj][m][1][0], acc[ai][bj][m][1][1], acc[ai][bj][m][1][2], acc[ai][bj][m][1][3]};
;                     if (wc == 0) {
;                         const f32x4 c0 = rc[g & 1][0], c1 = rc[g & 1][1], s0 = rc[g & 1][2], s1 = rc[g & 1][3];
;                         const float cs[8] = {c0[0], c0[1], c0[2], c0[3], c1[0], c1[1], c1[2], c1[3]}, sn[8] = {s0[0], s0[1], s0[2], s0[3], s1[0], s1[1], s1[2], s1[3]};
; #pragma unroll
;                         for (int i = 0; i < 8; ++i) {
;                             const float pv = __shfl_xor(v[i], 32);
;                             v[i] = (fq < 2) ? (v[i] * cs[i] - pv * sn[i]) : (v[i] * cs[i] + pv * sn[i]);
;                         }
;                     }
.LBB0_1592:
	v_and_b32_e32 v9, 64, v211
	v_xor_b32_e32 v8, 32, v211
	v_add_u32_e32 v9, 64, v9
	v_cmp_lt_i32_e32 vcc, v8, v9
	s_nop 1
	v_cndmask_b32_e32 v8, v211, v8, vcc
	v_lshlrev_b32_e32 v15, 2, v8
	ds_bpermute_b32 v8, v15, v4
	ds_bpermute_b32 v9, v15, v5
	ds_bpermute_b32 v10, v15, v6
	ds_bpermute_b32 v11, v15, v7
	ds_bpermute_b32 v12, v15, v0
	ds_bpermute_b32 v13, v15, v1
	ds_bpermute_b32 v14, v15, v2
	ds_bpermute_b32 v15, v15, v3
	s_waitcnt lgkmcnt(0)
	v_pk_mul_f32 v[8:9], v[140:141], v[8:9]
	v_pk_mul_f32 v[10:11], v[142:143], v[10:11]
	v_pk_mul_f32 v[12:13], v[136:137], v[12:13]
	v_cndmask_b32_e64 v9, v9, -v9, s[0:1]
	v_pk_mul_f32 v[14:15], v[138:139], v[14:15]
	v_cndmask_b32_e64 v8, v8, -v8, s[0:1]
	v_cndmask_b32_e64 v11, v11, -v11, s[0:1]
	v_cndmask_b32_e64 v10, v10, -v10, s[0:1]
	v_cndmask_b32_e64 v13, v13, -v13, s[0:1]
	v_cndmask_b32_e64 v12, v12, -v12, s[0:1]
	v_cndmask_b32_e64 v15, v15, -v15, s[0:1]
	v_cndmask_b32_e64 v14, v14, -v14, s[0:1]
	v_pk_fma_f32 v[2:3], v[2:3], v[134:135], v[14:15]
	v_pk_fma_f32 v[0:1], v[0:1], v[132:133], v[12:13]
	v_pk_fma_f32 v[6:7], v[6:7], v[130:131], v[10:11]
	v_pk_fma_f32 v[4:5], v[4:5], v[128:129], v[8:9]
	s_and_b64 vcc, exec, s[48:49]
	s_cbranch_vccnz .LBB0_1591
